# GEMM epilogues: per-row scale loads of a unit issued together up front (inproj, moe1, moe2) and inproj q/k rope tables read from an LDS copy instead of dependent global loads
# speedup vs baseline: 1.0224x; 1.0224x over previous
;     __device__ __forceinline__ void operator()(const pg8::i32x4 (&acc)[2][2][4][2], const Unit& u, int wr, int wc, int fr, int fq) const {
;     ...
;                         if (lat) { const int pos = bj ? (tok & 63) : (tok >> 6); const f32x4 c = *(const f32x4*)(ropec + pos * 16 + 4 * fq), s = *(const f32x4*)(ropes + pos * 16 + 4 * fq);
.LBB0_275:
	s_add_u32 s18, s18, 0x2f134800
	s_addc_u32 s19, s19, 0
	s_lshl_b32 s30, s68, 7
	s_lshl_b64 s[44:45], s[30:31], 2
	s_add_u32 s16, s16, s44
	s_addc_u32 s17, s17, s45
	s_add_u32 s14, s14, 0x398000
	s_addc_u32 s15, s15, 0
	s_add_u32 s12, s12, 0x3d8000
	s_addc_u32 s13, s13, 0
	s_add_u32 s44, s10, 0x2f104800
	s_addc_u32 s45, s11, 0
	s_mul_i32 s11, s68, 0x3000
	s_mul_hi_u32 s10, s68, 0x3000
	s_add_u32 s30, s6, s11
	s_addc_u32 s41, s7, s10
	s_and_b32 s10, s39, 3
	s_add_i32 m0, s37, 0x18000
	v_lshl_add_u64 v[6:7], v[6:7], 0, s[8:9]
	s_lshl_b32 s11, s46, 6
	s_lshl_b32 s39, s46, 13
	s_lshl_b32 s48, s10, 5
	s_lshl_b32 s46, s10, 12
	s_waitcnt vmcnt(2)
	s_barrier
	global_load_lds_dwordx4 v[6:7], off
	v_lshl_add_u64 v[4:5], v[4:5], 0, s[8:9]
	s_add_i32 m0, s37, 0x1a000
	s_add_i32 s60, s37, 0x8000
	s_add_i32 s61, s37, 0xa000
	global_load_lds_dwordx4 v[4:5], off
	v_lshl_add_u64 v[0:1], v[0:1], 0, s[8:9]
	s_mov_b32 m0, s60
	s_add_u32 s6, s2, 0x20080
	global_load_lds_dwordx4 v[0:1], off
	v_lshl_add_u64 v[0:1], v[2:3], 0, s[8:9]
	s_mov_b32 m0, s61
	s_addc_u32 s7, s3, 0
	global_load_lds_dwordx4 v[0:1], off
	s_add_i32 m0, s37, 0x1c000
	v_lshl_add_u64 v[0:1], s[6:7], 0, v[146:147]
	global_load_lds_dwordx4 v[0:1], off
	v_lshl_add_u64 v[0:1], s[6:7], 0, v[148:149]
	s_add_i32 m0, s37, 0x1e000
	v_and_b32_e32 v198, 15, v8
	global_load_lds_dwordx4 v[0:1], off
	v_bfe_u32 v1, v8, 4, 2
	v_lshlrev_b32_e32 v144, 4, v1
	v_lshlrev_b32_e32 v2, 6, v198
	v_lshlrev_b32_e32 v5, 2, v198
	v_or_b32_e32 v3, v2, v144
	v_and_b32_e32 v4, 32, v5
	v_lshlrev_b32_e32 v0, 3, v1
	v_bitop3_b32 v8, v3, s39, v4 bitop3:0xde
	v_bitop3_b32 v200, v3, s46, v4 bitop3:0xde
	s_cmpk_lt_u32 s38, 0x100
	v_lshlrev_b32_e32 v4, 2, v1
	v_lshlrev_b32_e32 v1, 6, v1
	s_movk_i32 s6, 0x80
	s_cselect_b64 s[46:47], -1, 0
	v_bitop3_b32 v205, v1, s6, v5 bitop3:0x36
	s_ashr_i32 s62, s29, 31
	s_ashr_i32 s63, s28, 31
	s_lshl_b32 s6, s10, 7
	s_add_u32 s6, s30, s6
	s_addc_u32 s7, s41, 0
	v_lshl_add_u64 v[6:7], s[6:7], 0, v[144:145]
	s_mov_b64 s[6:7], 0x2f128800
	v_bitop3_b32 v204, v1, 64, v5 bitop3:0x36
	v_lshl_add_u64 v[150:151], v[6:7], 0, s[6:7]
	v_lshl_add_u64 v[6:7], s[16:17], 0, v[144:145]
	s_mov_b64 s[6:7], 0x418000
	v_mov_b32_e32 v3, v145
	v_lshlrev_b32_e32 v1, 13, v12
	v_lshl_add_u64 v[152:153], v[6:7], 0, s[6:7]
	v_lshl_add_u64 v[6:7], s[14:15], 0, v[2:3]
	v_lshl_add_u64 v[2:3], s[12:13], 0, v[2:3]
	v_and_b32_e32 v1, 0xffffc000, v1
	v_lshl_add_u64 v[160:161], v[2:3], 0, v[144:145]
	v_lshl_add_u32 v1, v13, 10, v1
	v_and_b32_e32 v2, 1, v12
	v_lshl_or_b32 v1, v2, 6, v1
	v_lshl_add_u32 v162, v14, 1, v1
	v_lshlrev_b32_e32 v1, 13, v9
	v_and_b32_e32 v1, 0xffffc000, v1
	s_waitcnt vmcnt(6)
	v_lshl_add_u32 v1, v10, 10, v1
	v_and_b32_e32 v2, 1, v9
	v_or_b32_e32 v199, s11, v198
	v_lshl_or_b32 v1, v2, 6, v1
	v_or_b32_e32 v201, 16, v199
	v_or_b32_e32 v202, 32, v199
	v_or_b32_e32 v203, 48, v199
	v_lshl_add_u64 v[154:155], s[14:15], 0, v[144:145]
	v_lshl_add_u64 v[156:157], s[12:13], 0, v[144:145]
	v_lshl_add_u64 v[158:159], v[6:7], 0, v[144:145]
	v_mbcnt_lo_u32_b32 v20, -1, 0
	v_mbcnt_hi_u32_b32 v20, -1, v20
	v_readlane_b32 s6, v254, 6
	s_nop 3
	v_lshl_add_u32 v20, s6, 6, v20
	v_lshlrev_b32_e32 v21, 3, v20
	global_load_dwordx2 v[22:23], v21, s[12:13]
	global_load_dwordx2 v[24:25], v21, s[14:15]
	v_add_u32_e32 v21, 0x20000, v21
	s_waitcnt vmcnt(0)
	ds_write_b64 v21, v[22:23]
	ds_write_b64 v21, v[24:25] offset:4096
	s_waitcnt lgkmcnt(0)
	v_mov_b32_e32 v163, v145
	v_lshl_add_u32 v164, v11, 1, v1
	v_mov_b32_e32 v165, v145
	s_mov_b32 s12, 0
	v_add_u32_e32 v206, 0, v8
	s_lshl_b32 s13, s48, 1
	v_lshlrev_b32_e32 v166, 1, v0
	v_lshlrev_b32_e32 v144, 1, v4
	s_barrier
	s_branch .LBB0_278

; __device__ __forceinline__ u32x4 pack8(f32x4 a, f32x4 b) { u32x4 w; w.x = pk2(a[0], a[1]); w.y = pk2(a[2], a[3]); w.z = pk2(b[0], b[1]); w.w = pk2(b[2], b[3]); return w; }
;     __device__ __forceinline__ void operator()(const pg8::i32x4 (&acc)[2][2][4][2], const Unit& u, int wr, int wc, int fr, int fq) const {
;     ...
;         f32x4 swv[2][2];
; #pragma unroll
;         for (int bj = 0; bj < 2; ++bj)
; #pragma unroll
;             for (int n = 0; n < 2; ++n) swv[bj][n] = *(const f32x4*)(swin + pn * 256 + 128 * bj + 32 * wc + 16 * n + 4 * fq);
;     ...
;             size_t boff; int cb, ldc;
;             if (pn < 6) { boff = U_V; cb = 256 * (pn - 4); ldc = 512; } else if (pn < 8) { boff = U_Z; cb = 256 * (pn - 6); ldc = 512; } else { boff = U_XBC; cb = 256 * (pn - 8); ldc = 1024; }
;             bf16_t* base = (bf16_t*)(U + boff);
; #pragma unroll
;             for (int ai = 0; ai < 2; ++ai)
; #pragma unroll
;                 for (int m = 0; m < 4; ++m) {
;                     const int row = u.pm * 256 + ai * 128 + wr * 64 + m * 16 + fr; const float sa = sah[row];
; #pragma unroll
;                     for (int bj = 0; bj < 2; ++bj) { f32x4 x0, x1;
; #pragma unroll
;                         for (int i = 0; i < 4; ++i) { x0[i] = (float)acc[ai][bj][m][0][i] * (sa * swv[bj][0][i]); x1[i] = (float)acc[ai][bj][m][1][i] * (sa * swv[bj][1][i]); }
;                         *(u32x4*)(base + (size_t)row * ldc + cb + 128 * bj + 32 * wc + 8 * fq) = pack8(x0, x1); }
;                 }
.LBB0_284:
	s_lshl_b32 s2, s56, 8
	s_ashr_i32 s3, s2, 31
	v_lshl_add_u64 v[4:5], s[2:3], 2, v[150:151]
	global_load_dwordx4 v[16:19], v[4:5], off
	global_load_dwordx4 v[12:15], v[4:5], off offset:64
	global_load_dwordx4 v[8:11], v[4:5], off offset:512
	s_nop 0
	global_load_dwordx4 v[4:7], v[4:5], off offset:576
	v_cvt_f32_i32_e32 v195, v141
	v_cvt_f32_i32_e32 v194, v140
	v_cvt_f32_i32_e32 v191, v137
	v_cvt_f32_i32_e32 v190, v136
	v_cvt_f32_i32_e32 v193, v143
	v_cvt_f32_i32_e32 v192, v142
	v_cvt_f32_i32_e32 v189, v139
	v_cvt_f32_i32_e32 v188, v138
	v_cvt_f32_i32_e32 v187, v125
	v_cvt_f32_i32_e32 v186, v124
	v_cvt_f32_i32_e32 v183, v121
	v_cvt_f32_i32_e32 v182, v120
	v_cvt_f32_i32_e32 v185, v127
	v_cvt_f32_i32_e32 v184, v126
	v_cvt_f32_i32_e32 v181, v123
	v_cvt_f32_i32_e32 v180, v122
	v_cvt_f32_i32_e32 v177, v133
	v_cvt_f32_i32_e32 v176, v132
	v_cvt_f32_i32_e32 v173, v129
	v_cvt_f32_i32_e32 v172, v128
	v_cvt_f32_i32_e32 v175, v135
	v_cvt_f32_i32_e32 v174, v134
	v_cvt_f32_i32_e32 v171, v131
	v_cvt_f32_i32_e32 v170, v130
	v_cvt_f32_i32_e32 v169, v109
	v_cvt_f32_i32_e32 v168, v108
	v_cvt_f32_i32_e32 v141, v105
	v_cvt_f32_i32_e32 v140, v104
	v_cvt_f32_i32_e32 v143, v111
	v_cvt_f32_i32_e32 v142, v110
	v_cvt_f32_i32_e32 v139, v107
	v_cvt_f32_i32_e32 v138, v106
	v_cvt_f32_i32_e32 v137, v117
	v_cvt_f32_i32_e32 v136, v116
	v_cvt_f32_i32_e32 v133, v113
	v_cvt_f32_i32_e32 v132, v112
	v_cvt_f32_i32_e32 v135, v119
	v_cvt_f32_i32_e32 v134, v118
	v_cvt_f32_i32_e32 v131, v115
	v_cvt_f32_i32_e32 v130, v114
	v_cvt_f32_i32_e32 v127, v93
	v_cvt_f32_i32_e32 v126, v92
	v_cvt_f32_i32_e32 v123, v89
	v_cvt_f32_i32_e32 v122, v88
	v_cvt_f32_i32_e32 v125, v95
	v_cvt_f32_i32_e32 v124, v94
	v_cvt_f32_i32_e32 v121, v91
	v_cvt_f32_i32_e32 v120, v90
	v_cvt_f32_i32_e32 v117, v101
	v_cvt_f32_i32_e32 v116, v100
	v_cvt_f32_i32_e32 v113, v97
	v_cvt_f32_i32_e32 v112, v96
	v_cvt_f32_i32_e32 v115, v103
	v_cvt_f32_i32_e32 v114, v102
	v_cvt_f32_i32_e32 v111, v99
	v_cvt_f32_i32_e32 v110, v98
	v_cvt_f32_i32_e32 v109, v85
	v_cvt_f32_i32_e32 v108, v84
	v_cvt_f32_i32_e32 v105, v81
	v_cvt_f32_i32_e32 v104, v80
	v_cvt_f32_i32_e32 v107, v87
	v_cvt_f32_i32_e32 v106, v86
	v_cvt_f32_i32_e32 v103, v83
	v_cvt_f32_i32_e32 v102, v82
	v_cvt_f32_i32_e32 v101, v77
	v_cvt_f32_i32_e32 v100, v76
	v_cvt_f32_i32_e32 v97, v73
	v_cvt_f32_i32_e32 v96, v72
	v_cvt_f32_i32_e32 v99, v79
	v_cvt_f32_i32_e32 v98, v78
	v_cvt_f32_i32_e32 v95, v75
	v_cvt_f32_i32_e32 v94, v74
	v_cvt_f32_i32_e32 v93, v61
	v_cvt_f32_i32_e32 v92, v60
	v_cvt_f32_i32_e32 v89, v57
	v_cvt_f32_i32_e32 v88, v56
	v_cvt_f32_i32_e32 v91, v63
	v_cvt_f32_i32_e32 v90, v62
	v_cvt_f32_i32_e32 v87, v59
	v_cvt_f32_i32_e32 v86, v58
	v_cvt_f32_i32_e32 v85, v69
	v_cvt_f32_i32_e32 v84, v68
	v_cvt_f32_i32_e32 v81, v65
	v_cvt_f32_i32_e32 v80, v64
	v_cvt_f32_i32_e32 v83, v71
	v_cvt_f32_i32_e32 v82, v70
	v_cvt_f32_i32_e32 v79, v67
	v_cvt_f32_i32_e32 v78, v66
	v_cvt_f32_i32_e32 v77, v45
	v_cvt_f32_i32_e32 v76, v44
	v_cvt_f32_i32_e32 v73, v41
	v_cvt_f32_i32_e32 v72, v40
	v_cvt_f32_i32_e32 v75, v47
	v_cvt_f32_i32_e32 v74, v46
	v_cvt_f32_i32_e32 v71, v43
	v_cvt_f32_i32_e32 v70, v42
	v_cvt_f32_i32_e32 v69, v53
	v_cvt_f32_i32_e32 v68, v52
	v_cvt_f32_i32_e32 v65, v49
	v_cvt_f32_i32_e32 v64, v48
	v_cvt_f32_i32_e32 v67, v55
	v_cvt_f32_i32_e32 v66, v54
	v_cvt_f32_i32_e32 v63, v51
	v_cvt_f32_i32_e32 v62, v50
	v_cvt_f32_i32_e32 v61, v29
	v_cvt_f32_i32_e32 v60, v28
	v_cvt_f32_i32_e32 v57, v25
	v_cvt_f32_i32_e32 v56, v24
	v_cvt_f32_i32_e32 v59, v31
	v_cvt_f32_i32_e32 v58, v30
	v_cvt_f32_i32_e32 v55, v27
	v_cvt_f32_i32_e32 v54, v26
	v_cvt_f32_i32_e32 v51, v37
	v_cvt_f32_i32_e32 v50, v36
	v_cvt_f32_i32_e32 v47, v33
	v_cvt_f32_i32_e32 v46, v32
	v_cvt_f32_i32_e32 v53, v39
	v_cvt_f32_i32_e32 v52, v38
	v_cvt_f32_i32_e32 v49, v35
	v_cvt_f32_i32_e32 v48, v34
	v_cvt_f32_i32_e32 v43, v21
	v_cvt_f32_i32_e32 v42, v20
	v_cvt_f32_i32_e32 v41, v1
	v_cvt_f32_i32_e32 v40, v0
	v_cvt_f32_i32_e32 v45, v23
	v_cvt_f32_i32_e32 v44, v22
	v_cvt_f32_i32_e32 v1, v3
	s_cmp_gt_i32 s56, 3
	s_mov_b64 s[4:5], -1
	s_cbranch_scc0 .LBB0_287
	s_cmp_lt_u32 s56, 6
	s_cselect_b64 s[4:5], -1, 0
	s_cmp_lt_u32 s56, 8
	s_cselect_b64 s[6:7], -1, 0
	s_and_b64 s[14:15], s[6:7], exec
	s_movk_i32 s3, 0xfa00
	s_mov_b32 s14, 0x6c00000
	s_cselect_b32 s3, s3, 0xfffff800
	s_cselect_b32 s14, s14, 0x9000000
	s_and_b64 s[4:5], s[4:5], exec
	s_cselect_b32 s3, 0xfffffc00, s3
	s_cselect_b32 s4, 0x4800000, s14
	s_add_i32 s30, s3, s2
	s_add_u32 s4, s18, s4
	s_addc_u32 s5, s19, 0
	s_lshl_b64 s[2:3], s[30:31], 1
	s_add_u32 s2, s4, s2
	s_addc_u32 s3, s5, s3
	s_add_u32 s2, s2, s13
	s_addc_u32 s3, s3, 0
	v_mov_b32_e32 v167, v145
	v_lshl_add_u64 v[20:21], s[2:3], 0, v[166:167]
	s_lshl_b32 s3, s40, 8
	v_add_u32_e32 v22, s3, v199
	v_lshlrev_b32_e32 v129, 2, v22
	global_load_dword v34, v129, s[44:45]
	global_load_dword v35, v129, s[44:45] offset:64
	global_load_dword v36, v129, s[44:45] offset:128
	global_load_dword v37, v129, s[44:45] offset:192
	global_load_dword v38, v129, s[44:45] offset:512
	global_load_dword v39, v129, s[44:45] offset:576
	global_load_dword v118, v129, s[44:45] offset:640
	global_load_dword v128, v129, s[44:45] offset:704
	v_ashrrev_i32_e32 v23, 31, v22
	v_lshl_add_u64 v[24:25], v[22:23], 2, s[44:45]
	s_and_b64 s[4:5], s[6:7], exec
	s_cselect_b32 s2, 9, 10
	v_lshlrev_b64 v[24:25], s2, v[22:23]
	v_lshl_add_u64 v[28:29], v[24:25], 1, v[20:21]
	s_waitcnt vmcnt(0)
; __device__ __forceinline__ u32x4 pack8(f32x4 a, f32x4 b) { u32x4 w; w.x = pk2(a[0], a[1]); w.y = pk2(a[2], a[3]); w.z = pk2(b[0], b[1]); w.w = pk2(b[2], b[3]); return w; }
;     __device__ __forceinline__ void operator()(const pg8::i32x4 (&acc)[2][2][4][2], const Unit& u, int wr, int wc, int fr, int fq) const {
;     ...
; #pragma unroll
;             for (int ai = 0; ai < 2; ++ai)
; #pragma unroll
;                 for (int m = 0; m < 4; ++m) {
;                     const int row = u.pm * 256 + ai * 128 + wr * 64 + m * 16 + fr; const float sa = sah[row];
; #pragma unroll
;                     for (int bj = 0; bj < 2; ++bj) { f32x4 x0, x1;
; #pragma unroll
;                         for (int i = 0; i < 4; ++i) { x0[i] = (float)acc[ai][bj][m][0][i] * (sa * swv[bj][0][i]); x1[i] = (float)acc[ai][bj][m][1][i] * (sa * swv[bj][1][i]); }
;                         *(u32x4*)(base + (size_t)row * ldc + cb + 128 * bj + 32 * wc + 8 * fq) = pack8(x0, x1); }
;                 }
	v_mov_b32_e32 v0, v34
	v_pk_mul_f32 v[24:25], v[16:17], v[0:1] op_sel_hi:[1,0]
	v_pk_mul_f32 v[26:27], v[12:13], v[0:1] op_sel_hi:[1,0]
	v_pk_mul_f32 v[30:31], v[18:19], v[0:1] op_sel_hi:[1,0]
	v_pk_mul_f32 v[32:33], v[14:15], v[0:1] op_sel_hi:[1,0]
	v_pk_mul_f32 v[24:25], v[24:25], v[194:195]
	v_pk_mul_f32 v[26:27], v[26:27], v[190:191]
	v_pk_mul_f32 v[30:31], v[30:31], v[192:193]
	v_pk_mul_f32 v[32:33], v[32:33], v[188:189]
	v_cvt_pk_bf16_f32 v24, v24, v25
	v_cvt_pk_bf16_f32 v25, v30, v31
	v_cvt_pk_bf16_f32 v26, v26, v27
	v_cvt_pk_bf16_f32 v27, v32, v33
	global_store_dwordx4 v[28:29], v[24:27], off
	v_pk_mul_f32 v[30:31], v[10:11], v[0:1] op_sel_hi:[1,0]
	v_pk_mul_f32 v[32:33], v[6:7], v[0:1] op_sel_hi:[1,0]
	v_pk_mul_f32 v[24:25], v[8:9], v[0:1] op_sel_hi:[1,0]
	v_pk_mul_f32 v[26:27], v[4:5], v[0:1] op_sel_hi:[1,0]
	v_pk_mul_f32 v[24:25], v[24:25], v[186:187]
	v_pk_mul_f32 v[26:27], v[26:27], v[182:183]
	v_pk_mul_f32 v[30:31], v[30:31], v[184:185]
	v_pk_mul_f32 v[32:33], v[32:33], v[180:181]
	v_cvt_pk_bf16_f32 v24, v24, v25
	v_cvt_pk_bf16_f32 v25, v30, v31
	v_cvt_pk_bf16_f32 v26, v26, v27
	v_cvt_pk_bf16_f32 v27, v32, v33
	global_store_dwordx4 v[28:29], v[24:27], off offset:256
	s_nop 1
	v_add_u32_e32 v24, s3, v201
	v_ashrrev_i32_e32 v25, 31, v24
	v_lshl_add_u64 v[26:27], v[24:25], 2, s[44:45]
	v_mov_b32_e32 v0, v35
	v_lshlrev_b64 v[24:25], s2, v[24:25]
	v_lshl_add_u64 v[28:29], v[24:25], 1, v[20:21]
	v_pk_mul_f32 v[24:25], v[16:17], v[0:1] op_sel_hi:[1,0]
	v_pk_mul_f32 v[26:27], v[12:13], v[0:1] op_sel_hi:[1,0]
	v_pk_mul_f32 v[30:31], v[18:19], v[0:1] op_sel_hi:[1,0]
	v_pk_mul_f32 v[32:33], v[14:15], v[0:1] op_sel_hi:[1,0]
	v_pk_mul_f32 v[24:25], v[24:25], v[176:177]
	v_pk_mul_f32 v[26:27], v[26:27], v[172:173]
	v_pk_mul_f32 v[30:31], v[30:31], v[174:175]
	v_pk_mul_f32 v[32:33], v[32:33], v[170:171]
	v_cvt_pk_bf16_f32 v24, v24, v25
	v_cvt_pk_bf16_f32 v25, v30, v31
	v_cvt_pk_bf16_f32 v26, v26, v27
	v_cvt_pk_bf16_f32 v27, v32, v33
	global_store_dwordx4 v[28:29], v[24:27], off
	v_pk_mul_f32 v[30:31], v[10:11], v[0:1] op_sel_hi:[1,0]
	v_pk_mul_f32 v[32:33], v[6:7], v[0:1] op_sel_hi:[1,0]
	v_pk_mul_f32 v[24:25], v[8:9], v[0:1] op_sel_hi:[1,0]
	v_pk_mul_f32 v[26:27], v[4:5], v[0:1] op_sel_hi:[1,0]
	v_pk_mul_f32 v[24:25], v[24:25], v[168:169]
	v_pk_mul_f32 v[26:27], v[26:27], v[140:141]
	v_pk_mul_f32 v[30:31], v[30:31], v[142:143]
	v_pk_mul_f32 v[32:33], v[32:33], v[138:139]
	v_cvt_pk_bf16_f32 v24, v24, v25
	v_cvt_pk_bf16_f32 v25, v30, v31
	v_cvt_pk_bf16_f32 v26, v26, v27
	v_cvt_pk_bf16_f32 v27, v32, v33
	global_store_dwordx4 v[28:29], v[24:27], off offset:256
	s_nop 1
	v_add_u32_e32 v24, s3, v202
	v_ashrrev_i32_e32 v25, 31, v24
	v_lshl_add_u64 v[26:27], v[24:25], 2, s[44:45]
	v_mov_b32_e32 v0, v36
	v_lshlrev_b64 v[24:25], s2, v[24:25]
	v_lshl_add_u64 v[28:29], v[24:25], 1, v[20:21]
	v_pk_mul_f32 v[24:25], v[16:17], v[0:1] op_sel_hi:[1,0]
	v_pk_mul_f32 v[26:27], v[12:13], v[0:1] op_sel_hi:[1,0]
	v_pk_mul_f32 v[30:31], v[18:19], v[0:1] op_sel_hi:[1,0]
	v_pk_mul_f32 v[32:33], v[14:15], v[0:1] op_sel_hi:[1,0]
	v_pk_mul_f32 v[24:25], v[24:25], v[136:137]
	v_pk_mul_f32 v[26:27], v[26:27], v[132:133]
	v_pk_mul_f32 v[30:31], v[30:31], v[134:135]
	v_pk_mul_f32 v[32:33], v[32:33], v[130:131]
	v_cvt_pk_bf16_f32 v24, v24, v25
	v_cvt_pk_bf16_f32 v25, v30, v31
	v_cvt_pk_bf16_f32 v26, v26, v27
	v_cvt_pk_bf16_f32 v27, v32, v33
	global_store_dwordx4 v[28:29], v[24:27], off
	v_pk_mul_f32 v[30:31], v[10:11], v[0:1] op_sel_hi:[1,0]
	v_pk_mul_f32 v[32:33], v[6:7], v[0:1] op_sel_hi:[1,0]
	v_pk_mul_f32 v[24:25], v[8:9], v[0:1] op_sel_hi:[1,0]
	v_pk_mul_f32 v[26:27], v[4:5], v[0:1] op_sel_hi:[1,0]
	v_pk_mul_f32 v[24:25], v[24:25], v[126:127]
	v_pk_mul_f32 v[26:27], v[26:27], v[122:123]
	v_pk_mul_f32 v[30:31], v[30:31], v[124:125]
	v_pk_mul_f32 v[32:33], v[32:33], v[120:121]
	v_cvt_pk_bf16_f32 v24, v24, v25
	v_cvt_pk_bf16_f32 v25, v30, v31
	v_cvt_pk_bf16_f32 v26, v26, v27
	v_cvt_pk_bf16_f32 v27, v32, v33
	global_store_dwordx4 v[28:29], v[24:27], off offset:256
	s_nop 1
	v_add_u32_e32 v24, s3, v203
	v_ashrrev_i32_e32 v25, 31, v24
	v_lshl_add_u64 v[26:27], v[24:25], 2, s[44:45]
	v_mov_b32_e32 v0, v37
	v_lshlrev_b64 v[24:25], s2, v[24:25]
	v_lshl_add_u64 v[28:29], v[24:25], 1, v[20:21]
	v_pk_mul_f32 v[24:25], v[16:17], v[0:1] op_sel_hi:[1,0]
	v_pk_mul_f32 v[26:27], v[12:13], v[0:1] op_sel_hi:[1,0]
	v_pk_mul_f32 v[30:31], v[18:19], v[0:1] op_sel_hi:[1,0]
	v_pk_mul_f32 v[32:33], v[14:15], v[0:1] op_sel_hi:[1,0]
	v_pk_mul_f32 v[24:25], v[24:25], v[116:117]
	v_pk_mul_f32 v[26:27], v[26:27], v[112:113]
	v_pk_mul_f32 v[30:31], v[30:31], v[114:115]
	v_pk_mul_f32 v[32:33], v[32:33], v[110:111]
	v_cvt_pk_bf16_f32 v24, v24, v25
	v_cvt_pk_bf16_f32 v25, v30, v31
	v_cvt_pk_bf16_f32 v26, v26, v27
	v_cvt_pk_bf16_f32 v27, v32, v33
	global_store_dwordx4 v[28:29], v[24:27], off
	v_pk_mul_f32 v[30:31], v[10:11], v[0:1] op_sel_hi:[1,0]
	v_pk_mul_f32 v[32:33], v[6:7], v[0:1] op_sel_hi:[1,0]
	v_pk_mul_f32 v[24:25], v[8:9], v[0:1] op_sel_hi:[1,0]
	v_pk_mul_f32 v[26:27], v[4:5], v[0:1] op_sel_hi:[1,0]
	v_pk_mul_f32 v[24:25], v[24:25], v[108:109]
	v_pk_mul_f32 v[26:27], v[26:27], v[104:105]
	v_pk_mul_f32 v[30:31], v[30:31], v[106:107]
	v_pk_mul_f32 v[32:33], v[32:33], v[102:103]
	v_cvt_pk_bf16_f32 v24, v24, v25
	v_cvt_pk_bf16_f32 v25, v30, v31
	v_cvt_pk_bf16_f32 v26, v26, v27
	v_cvt_pk_bf16_f32 v27, v32, v33
	global_store_dwordx4 v[28:29], v[24:27], off offset:256
	s_nop 1
	v_add_u32_e32 v24, 0x80, v22
	v_ashrrev_i32_e32 v25, 31, v24
	v_lshl_add_u64 v[26:27], v[24:25], 2, s[44:45]
; __device__ __forceinline__ u32x4 pack8(f32x4 a, f32x4 b) { u32x4 w; w.x = pk2(a[0], a[1]); w.y = pk2(a[2], a[3]); w.z = pk2(b[0], b[1]); w.w = pk2(b[2], b[3]); return w; }
;     __device__ __forceinline__ void operator()(const pg8::i32x4 (&acc)[2][2][4][2], const Unit& u, int wr, int wc, int fr, int fq) const {
;     ...
; #pragma unroll
;             for (int ai = 0; ai < 2; ++ai)
; #pragma unroll
;                 for (int m = 0; m < 4; ++m) {
;                     const int row = u.pm * 256 + ai * 128 + wr * 64 + m * 16 + fr; const float sa = sah[row];
; #pragma unroll
;                     for (int bj = 0; bj < 2; ++bj) { f32x4 x0, x1;
; #pragma unroll
;                         for (int i = 0; i < 4; ++i) { x0[i] = (float)acc[ai][bj][m][0][i] * (sa * swv[bj][0][i]); x1[i] = (float)acc[ai][bj][m][1][i] * (sa * swv[bj][1][i]); }
;                         *(u32x4*)(base + (size_t)row * ldc + cb + 128 * bj + 32 * wc + 8 * fq) = pack8(x0, x1); }
;                 }
	v_mov_b32_e32 v0, v38
	v_lshlrev_b64 v[24:25], s2, v[24:25]
	v_lshl_add_u64 v[28:29], v[24:25], 1, v[20:21]
	v_pk_mul_f32 v[24:25], v[16:17], v[0:1] op_sel_hi:[1,0]
	v_pk_mul_f32 v[26:27], v[12:13], v[0:1] op_sel_hi:[1,0]
	v_pk_mul_f32 v[30:31], v[18:19], v[0:1] op_sel_hi:[1,0]
	v_pk_mul_f32 v[32:33], v[14:15], v[0:1] op_sel_hi:[1,0]
	v_pk_mul_f32 v[24:25], v[24:25], v[100:101]
	v_pk_mul_f32 v[26:27], v[26:27], v[96:97]
	v_pk_mul_f32 v[30:31], v[30:31], v[98:99]
	v_pk_mul_f32 v[32:33], v[32:33], v[94:95]
	v_cvt_pk_bf16_f32 v24, v24, v25
	v_cvt_pk_bf16_f32 v25, v30, v31
	v_cvt_pk_bf16_f32 v26, v26, v27
	v_cvt_pk_bf16_f32 v27, v32, v33
	global_store_dwordx4 v[28:29], v[24:27], off
	v_pk_mul_f32 v[30:31], v[10:11], v[0:1] op_sel_hi:[1,0]
	v_pk_mul_f32 v[32:33], v[6:7], v[0:1] op_sel_hi:[1,0]
	v_pk_mul_f32 v[24:25], v[8:9], v[0:1] op_sel_hi:[1,0]
	v_pk_mul_f32 v[26:27], v[4:5], v[0:1] op_sel_hi:[1,0]
	v_pk_mul_f32 v[24:25], v[24:25], v[92:93]
	v_pk_mul_f32 v[26:27], v[26:27], v[88:89]
	v_pk_mul_f32 v[30:31], v[30:31], v[90:91]
	v_pk_mul_f32 v[32:33], v[32:33], v[86:87]
	v_cvt_pk_bf16_f32 v24, v24, v25
	v_cvt_pk_bf16_f32 v25, v30, v31
	v_cvt_pk_bf16_f32 v26, v26, v27
	v_cvt_pk_bf16_f32 v27, v32, v33
	global_store_dwordx4 v[28:29], v[24:27], off offset:256
	s_nop 1
	v_add_u32_e32 v24, 0x90, v22
	v_ashrrev_i32_e32 v25, 31, v24
	v_lshl_add_u64 v[26:27], v[24:25], 2, s[44:45]
	v_mov_b32_e32 v0, v39
	v_lshlrev_b64 v[24:25], s2, v[24:25]
	v_lshl_add_u64 v[28:29], v[24:25], 1, v[20:21]
	v_pk_mul_f32 v[24:25], v[16:17], v[0:1] op_sel_hi:[1,0]
	v_pk_mul_f32 v[26:27], v[12:13], v[0:1] op_sel_hi:[1,0]
	v_pk_mul_f32 v[30:31], v[18:19], v[0:1] op_sel_hi:[1,0]
	v_pk_mul_f32 v[32:33], v[14:15], v[0:1] op_sel_hi:[1,0]
	v_pk_mul_f32 v[24:25], v[24:25], v[84:85]
	v_pk_mul_f32 v[26:27], v[26:27], v[80:81]
	v_pk_mul_f32 v[30:31], v[30:31], v[82:83]
	v_pk_mul_f32 v[32:33], v[32:33], v[78:79]
	v_cvt_pk_bf16_f32 v24, v24, v25
	v_cvt_pk_bf16_f32 v25, v30, v31
	v_cvt_pk_bf16_f32 v26, v26, v27
	v_cvt_pk_bf16_f32 v27, v32, v33
	global_store_dwordx4 v[28:29], v[24:27], off
	v_pk_mul_f32 v[30:31], v[10:11], v[0:1] op_sel_hi:[1,0]
	v_pk_mul_f32 v[32:33], v[6:7], v[0:1] op_sel_hi:[1,0]
	v_pk_mul_f32 v[24:25], v[8:9], v[0:1] op_sel_hi:[1,0]
	v_pk_mul_f32 v[26:27], v[4:5], v[0:1] op_sel_hi:[1,0]
	v_pk_mul_f32 v[24:25], v[24:25], v[76:77]
	v_pk_mul_f32 v[26:27], v[26:27], v[72:73]
	v_pk_mul_f32 v[30:31], v[30:31], v[74:75]
	v_pk_mul_f32 v[32:33], v[32:33], v[70:71]
	v_cvt_pk_bf16_f32 v24, v24, v25
	v_cvt_pk_bf16_f32 v25, v30, v31
	v_cvt_pk_bf16_f32 v26, v26, v27
	v_cvt_pk_bf16_f32 v27, v32, v33
	global_store_dwordx4 v[28:29], v[24:27], off offset:256
	s_nop 1
	v_add_u32_e32 v24, 0xa0, v22
	v_ashrrev_i32_e32 v25, 31, v24
	v_lshl_add_u64 v[26:27], v[24:25], 2, s[44:45]
	v_mov_b32_e32 v0, v118
	v_lshlrev_b64 v[24:25], s2, v[24:25]
	v_lshl_add_u64 v[28:29], v[24:25], 1, v[20:21]
	v_add_u32_e32 v22, 0xb0, v22
	v_ashrrev_i32_e32 v23, 31, v22
	v_pk_mul_f32 v[24:25], v[16:17], v[0:1] op_sel_hi:[1,0]
	v_pk_mul_f32 v[26:27], v[12:13], v[0:1] op_sel_hi:[1,0]
	v_pk_mul_f32 v[30:31], v[18:19], v[0:1] op_sel_hi:[1,0]
	v_pk_mul_f32 v[32:33], v[14:15], v[0:1] op_sel_hi:[1,0]
	v_pk_mul_f32 v[24:25], v[24:25], v[68:69]
	v_pk_mul_f32 v[26:27], v[26:27], v[64:65]
	v_pk_mul_f32 v[30:31], v[30:31], v[66:67]
	v_pk_mul_f32 v[32:33], v[32:33], v[62:63]
	v_cvt_pk_bf16_f32 v24, v24, v25
	v_cvt_pk_bf16_f32 v25, v30, v31
	v_cvt_pk_bf16_f32 v26, v26, v27
	v_cvt_pk_bf16_f32 v27, v32, v33
	global_store_dwordx4 v[28:29], v[24:27], off
	v_pk_mul_f32 v[30:31], v[10:11], v[0:1] op_sel_hi:[1,0]
	v_pk_mul_f32 v[32:33], v[6:7], v[0:1] op_sel_hi:[1,0]
	v_pk_mul_f32 v[24:25], v[8:9], v[0:1] op_sel_hi:[1,0]
	v_pk_mul_f32 v[26:27], v[4:5], v[0:1] op_sel_hi:[1,0]
	v_pk_mul_f32 v[24:25], v[24:25], v[60:61]
	v_pk_mul_f32 v[26:27], v[26:27], v[56:57]
	v_pk_mul_f32 v[30:31], v[30:31], v[58:59]
	v_pk_mul_f32 v[32:33], v[32:33], v[54:55]
	v_cvt_pk_bf16_f32 v24, v24, v25
	v_cvt_pk_bf16_f32 v25, v30, v31
	v_cvt_pk_bf16_f32 v26, v26, v27
	v_cvt_pk_bf16_f32 v27, v32, v33
	global_store_dwordx4 v[28:29], v[24:27], off offset:256
	v_cvt_f32_i32_e32 v0, v2
	s_nop 0
	v_lshl_add_u64 v[24:25], v[22:23], 2, s[44:45]
	v_mov_b32_e32 v24, v128
	v_lshlrev_b64 v[22:23], s2, v[22:23]
	v_lshl_add_u64 v[26:27], v[22:23], 1, v[20:21]
	v_pk_mul_f32 v[20:21], v[16:17], v[24:25] op_sel_hi:[1,0]
	v_pk_mul_f32 v[22:23], v[12:13], v[24:25] op_sel_hi:[1,0]
	v_pk_mul_f32 v[28:29], v[18:19], v[24:25] op_sel_hi:[1,0]
	v_pk_mul_f32 v[30:31], v[14:15], v[24:25] op_sel_hi:[1,0]
	v_pk_mul_f32 v[20:21], v[20:21], v[50:51]
	v_pk_mul_f32 v[22:23], v[22:23], v[46:47]
	v_pk_mul_f32 v[28:29], v[28:29], v[52:53]
	v_pk_mul_f32 v[30:31], v[30:31], v[48:49]
	v_cvt_pk_bf16_f32 v20, v20, v21
	v_cvt_pk_bf16_f32 v21, v28, v29
	v_cvt_pk_bf16_f32 v22, v22, v23
	v_cvt_pk_bf16_f32 v23, v30, v31
	global_store_dwordx4 v[26:27], v[20:23], off
	v_pk_mul_f32 v[28:29], v[10:11], v[24:25] op_sel_hi:[1,0]
	s_nop 0
	v_pk_mul_f32 v[20:21], v[8:9], v[24:25] op_sel_hi:[1,0]
	v_pk_mul_f32 v[22:23], v[4:5], v[24:25] op_sel_hi:[1,0]
	v_pk_mul_f32 v[24:25], v[6:7], v[24:25] op_sel_hi:[1,0]
	v_pk_mul_f32 v[20:21], v[20:21], v[42:43]
	v_pk_mul_f32 v[22:23], v[22:23], v[40:41]
	v_pk_mul_f32 v[28:29], v[28:29], v[44:45]
	v_pk_mul_f32 v[24:25], v[24:25], v[0:1]
	v_cvt_pk_bf16_f32 v20, v20, v21
	v_cvt_pk_bf16_f32 v21, v28, v29
	v_cvt_pk_bf16_f32 v22, v22, v23
	v_cvt_pk_bf16_f32 v23, v24, v25
	global_store_dwordx4 v[26:27], v[20:23], off offset:256
	s_cbranch_execz .LBB0_288

;     __device__ __forceinline__ void operator()(const pg8::i32x4 (&acc)[2][2][4][2], const Unit& u, int wr, int wc, int fr, int fq) const {
;     ...
;         if (pn < 4) {
;             const bool isq = pn < 2; bf16_t* base = (bf16_t*)(U + (isq ? U_Q : U_K)); const float* nw = qkw + (isq ? 0 : 64); const float osc = isq ? 0.125f * LOG2E : 1.f;
;             const int hg = 4 * (pn & 1) + wc;
;             f32x4 w[2][2];
; #pragma unroll
;             for (int bj = 0; bj < 2; ++bj)
; #pragma unroll
;                 for (int n = 0; n < 2; ++n) w[bj][n] = *(const f32x4*)(nw + 32 * bj + 16 * n + 4 * fq);
; #pragma unroll
;             for (int ai = 0; ai < 2; ++ai)
; #pragma unroll
;                 for (int m = 0; m < 4; ++m) {
;                     const int row = u.pm * 256 + ai * 128 + wr * 64 + m * 16 + fr;
;                     float ss = 0.f; const float sa = sah[row]; f32x4 xf[2][2];
; #pragma unroll
;                     for (int bj = 0; bj < 2; ++bj)
; #pragma unroll
;                         for (int n = 0; n < 2; ++n) { f32x4 x;
; #pragma unroll
;                             for (int i = 0; i < 4; ++i) x[i] = (float)acc[ai][bj][m][n][i] * (sa * swv[bj][n][i]);
;                             xf[bj][n] = x; ss += x[0] * x[0] + x[1] * x[1] + x[2] * x[2] + x[3] * x[3]; }
;                     { const int ln = fq * 16 + fr; ss += shx(ss, 16, ln); ss += shx(ss, 32, ln); }
;                     const float rstd = rsqrtf(ss * (1.f / 64.f) + EPS);
;                     const bool lat = row < NL; const int tok = row & 2047;
; #pragma unroll
;                     for (int bj = 0; bj < 2; ++bj) {
;                         f32x4 x1 = xf[bj][0] * rstd * w[bj][0], x2 = xf[bj][1] * rstd * w[bj][1];
;                         if (lat) { const int pos = bj ? (tok & 63) : (tok >> 6); const f32x4 c = *(const f32x4*)(ropec + pos * 16 + 4 * fq), s = *(const f32x4*)(ropes + pos * 16 + 4 * fq);
;                             const f32x4 o1 = x1 * c - x2 * s, o2 = x1 * s + x2 * c; x1 = o1; x2 = o2; }
;                         x1 = x1 * osc; x2 = x2 * osc;
;                         bf16_t* p = base + (size_t)row * 512 + 64 * hg + 32 * bj + 4 * fq;
;                         *(u32x2*)p = (u32x2){pk2(x1[0], x1[1]), pk2(x1[2], x1[3])};
;                         *(u32x2*)(p + 16) = (u32x2){pk2(x2[0], x2[1]), pk2(x2[2], x2[3])};
;                     }
.LBB0_288:
	s_cmp_lt_i32 s56, 2
	s_cselect_b64 vcc, -1, 0
	s_and_b64 s[2:3], vcc, exec
	s_cselect_b32 s30, 0, 0x100
	s_lshl_b32 s4, s40, 8
	s_add_i32 s4, s4, s11
	v_or_b32_e32 v196, s4, v198
	v_lshlrev_b32_e32 v224, 2, v196
	global_load_dword v216, v224, s[44:45]
	global_load_dword v217, v224, s[44:45] offset:64
	global_load_dword v218, v224, s[44:45] offset:128
	global_load_dword v219, v224, s[44:45] offset:192
	global_load_dword v220, v224, s[44:45] offset:512
	global_load_dword v221, v224, s[44:45] offset:576
	global_load_dword v222, v224, s[44:45] offset:640
	global_load_dword v223, v224, s[44:45] offset:704
	v_mbcnt_lo_u32_b32 v225, -1, 0
	v_mbcnt_hi_u32_b32 v225, -1, v225
	v_and_b32_e32 v225, 48, v225
	v_add_u32_e32 v225, 0x20000, v225
	v_lshl_add_u32 v226, v198, 6, v225
	v_ashrrev_i32_e32 v197, 31, v196
	v_lshl_add_u64 v[20:21], v[152:153], 0, s[30:31]
	v_lshl_add_u64 v[36:37], v[196:197], 2, s[44:45]
	global_load_dwordx4 v[32:35], v[20:21], off
	global_load_dwordx4 v[28:31], v[20:21], off offset:64
	global_load_dwordx4 v[24:27], v[20:21], off offset:128
	s_nop 0
	global_load_dwordx4 v[20:23], v[20:21], off offset:192
	s_mov_b32 s2, 0x8000
	s_waitcnt vmcnt(0)
	v_mov_b32_e32 v0, v216
	v_pk_mul_f32 v[36:37], v[16:17], v[0:1] op_sel_hi:[1,0]
	v_pk_mul_f32 v[118:119], v[12:13], v[0:1] op_sel_hi:[1,0]
	v_pk_mul_f32 v[36:37], v[36:37], v[194:195]
	v_pk_mul_f32 v[118:119], v[118:119], v[190:191]
	v_pk_mul_f32 v[128:129], v[14:15], v[0:1] op_sel_hi:[1,0]
	v_pk_mul_f32 v[38:39], v[18:19], v[0:1] op_sel_hi:[1,0]
	v_pk_mul_f32 v[128:129], v[128:129], v[188:189]
	v_mov_b32_e32 v188, v37
	v_mov_b32_e32 v189, v119
	v_pk_mul_f32 v[38:39], v[38:39], v[192:193]
	v_mov_b32_e32 v178, v36
	v_mov_b32_e32 v179, v118
	v_pk_mul_f32 v[188:189], v[188:189], v[188:189]
	s_nop 0
	v_pk_fma_f32 v[178:179], v[178:179], v[178:179], v[188:189]
	v_mov_b32_e32 v188, v38
	v_mov_b32_e32 v189, v128
	v_pk_fma_f32 v[178:179], v[188:189], v[188:189], v[178:179]
	v_mov_b32_e32 v188, v39
	v_mov_b32_e32 v189, v129
	v_pk_fma_f32 v[178:179], v[188:189], v[188:189], v[178:179]
	v_pk_mul_f32 v[188:189], v[8:9], v[0:1] op_sel_hi:[1,0]
	s_nop 0
	v_pk_mul_f32 v[186:187], v[188:189], v[186:187]
	v_pk_mul_f32 v[188:189], v[10:11], v[0:1] op_sel_hi:[1,0]
	v_mov_b32_e32 v191, v187
	v_pk_mul_f32 v[184:185], v[188:189], v[184:185]
	v_pk_mul_f32 v[188:189], v[4:5], v[0:1] op_sel_hi:[1,0]
	s_nop 0
	v_pk_mul_f32 v[182:183], v[188:189], v[182:183]
	v_pk_mul_f32 v[188:189], v[6:7], v[0:1] op_sel_hi:[1,0]
	v_mov_b32_e32 v190, v183
	v_pk_mul_f32 v[180:181], v[188:189], v[180:181]
	v_mov_b32_e32 v188, v182
	v_mov_b32_e32 v189, v186
	v_pk_mul_f32 v[190:191], v[190:191], v[190:191]
	v_add_f32_e32 v0, v178, v179
	v_pk_fma_f32 v[188:189], v[188:189], v[188:189], v[190:191]
	v_mov_b32_e32 v190, v180
	v_mov_b32_e32 v191, v184
	v_pk_fma_f32 v[188:189], v[190:191], v[190:191], v[188:189]
	v_mov_b32_e32 v190, v181
	v_mov_b32_e32 v191, v185
	v_pk_fma_f32 v[188:189], v[190:191], v[190:191], v[188:189]
	s_nop 0
	v_add_f32_e32 v0, v189, v0
	v_add_f32_e32 v0, v188, v0
	ds_bpermute_b32 v3, v204, v0
	s_waitcnt lgkmcnt(0)
	v_add_f32_e32 v0, v0, v3
	ds_bpermute_b32 v3, v205, v0
	s_waitcnt lgkmcnt(0)
	v_add_f32_e32 v0, v0, v3
	v_fmamk_f32 v0, v0, 0x3c800000, v246
	v_cmp_gt_f32_e64 s[40:41], s22, v0
	v_mul_f32_e32 v3, 0x4b800000, v0
	s_nop 0
	v_cndmask_b32_e64 v0, v0, v3, s[40:41]
	v_rsq_f32_e32 v0, v0
	s_nop 0
	v_mul_f32_e32 v3, 0x45800000, v0
	v_cndmask_b32_e64 v188, v0, v3, s[40:41]
	v_pk_mul_f32 v[36:37], v[36:37], v[188:189] op_sel_hi:[1,0]
	v_pk_mul_f32 v[38:39], v[38:39], v[188:189] op_sel_hi:[1,0]
	v_pk_mul_f32 v[118:119], v[118:119], v[188:189] op_sel_hi:[1,0]
	v_pk_mul_f32 v[128:129], v[128:129], v[188:189] op_sel_hi:[1,0]
	v_cmp_gt_i32_e64 s[40:41], s2, v196
	v_pk_mul_f32 v[38:39], v[34:35], v[38:39]
	v_pk_mul_f32 v[36:37], v[32:33], v[36:37]
	v_pk_mul_f32 v[192:193], v[30:31], v[128:129]
	v_pk_mul_f32 v[194:195], v[28:29], v[118:119]
	s_and_saveexec_b64 s[2:3], s[40:41]
	s_cbranch_execz .LBB0_290
	s_and_b32 s30, s4, 0x7c0
	v_add_u32_e32 v118, s30, v225
	ds_read_b128 v[208:211], v118
	v_add_u32_e32 v118, s30, v225
	ds_read_b128 v[212:215], v118 offset:4096
	s_waitcnt lgkmcnt(1)
	v_pk_mul_f32 v[118:119], v[192:193], v[210:211]
	v_pk_mul_f32 v[128:129], v[194:195], v[208:209]
	v_pk_mul_f32 v[178:179], v[38:39], v[210:211]
	v_pk_mul_f32 v[190:191], v[36:37], v[208:209]
	s_waitcnt lgkmcnt(0)
	v_pk_fma_f32 v[38:39], v[38:39], v[214:215], v[118:119] neg_lo:[0,0,1] neg_hi:[0,0,1]
	v_pk_fma_f32 v[36:37], v[36:37], v[212:213], v[128:129] neg_lo:[0,0,1] neg_hi:[0,0,1]
	v_pk_fma_f32 v[192:193], v[192:193], v[214:215], v[178:179]
	v_pk_fma_f32 v[194:195], v[194:195], v[212:213], v[190:191]
; __device__ __forceinline__ unsigned pk2(float lo, float hi) { f32x2_t v = {lo, hi}; bf16x2_t b = __builtin_convertvector(v, bf16x2_t); return __builtin_bit_cast(unsigned, b); }
; __device__ __forceinline__ float shx(float v, int m, int lane) { return __int_as_float(__builtin_amdgcn_ds_bpermute((lane ^ m) << 2, __float_as_int(v))); }
;     __device__ __forceinline__ void operator()(const pg8::i32x4 (&acc)[2][2][4][2], const Unit& u, int wr, int wc, int fr, int fq) const {
;     ...
;             for (int ai = 0; ai < 2; ++ai)
; #pragma unroll
;                 for (int m = 0; m < 4; ++m) {
;                     const int row = u.pm * 256 + ai * 128 + wr * 64 + m * 16 + fr;
;                     float ss = 0.f; const float sa = sah[row]; f32x4 xf[2][2];
; #pragma unroll
;                     for (int bj = 0; bj < 2; ++bj)
; #pragma unroll
;                         for (int n = 0; n < 2; ++n) { f32x4 x;
; #pragma unroll
;                             for (int i = 0; i < 4; ++i) x[i] = (float)acc[ai][bj][m][n][i] * (sa * swv[bj][n][i]);
;                             xf[bj][n] = x; ss += x[0] * x[0] + x[1] * x[1] + x[2] * x[2] + x[3] * x[3]; }
;                     { const int ln = fq * 16 + fr; ss += shx(ss, 16, ln); ss += shx(ss, 32, ln); }
;                     const float rstd = rsqrtf(ss * (1.f / 64.f) + EPS);
;                     const bool lat = row < NL; const int tok = row & 2047;
; #pragma unroll
;                     for (int bj = 0; bj < 2; ++bj) {
;                         f32x4 x1 = xf[bj][0] * rstd * w[bj][0], x2 = xf[bj][1] * rstd * w[bj][1];
;                         if (lat) { const int pos = bj ? (tok & 63) : (tok >> 6); const f32x4 c = *(const f32x4*)(ropec + pos * 16 + 4 * fq), s = *(const f32x4*)(ropes + pos * 16 + 4 * fq);
;                             const f32x4 o1 = x1 * c - x2 * s, o2 = x1 * s + x2 * c; x1 = o1; x2 = o2; }
;                         x1 = x1 * osc; x2 = x2 * osc;
;                         bf16_t* p = base + (size_t)row * 512 + 64 * hg + 32 * bj + 4 * fq;
;                         *(u32x2*)p = (u32x2){pk2(x1[0], x1[1]), pk2(x1[2], x1[3])};
;                         *(u32x2*)(p + 16) = (u32x2){pk2(x2[0], x2[1]), pk2(x2[2], x2[3])};
;                     }
.LBB0_290:
	s_or_b64 exec, exec, s[2:3]
	s_and_b64 s[2:3], vcc, exec
	s_cselect_b32 s2, 0, 0x2400000
	s_lshl_b32 s3, s56, 2
	s_and_b32 s3, s3, 4
	s_add_u32 s2, s18, s2
	s_addc_u32 s5, s19, 0
	s_or_b32 s3, s3, s10
	s_lshl_b32 s3, s3, 7
	v_mov_b32_e32 v0, 0x3e38aa3b
	s_add_u32 s2, s2, s3
	v_cndmask_b32_e32 v118, 1.0, v0, vcc
	s_addc_u32 s3, s5, 0
	v_lshl_add_u64 v[128:129], s[2:3], 0, v[144:145]
	v_lshlrev_b64 v[178:179], 10, v[196:197]
	v_pk_mul_f32 v[38:39], v[118:119], v[38:39] op_sel_hi:[0,1]
	v_pk_mul_f32 v[36:37], v[118:119], v[36:37] op_sel_hi:[0,1]
	v_lshl_add_u64 v[190:191], v[128:129], 0, v[178:179]
	v_pk_mul_f32 v[178:179], v[118:119], v[192:193] op_sel_hi:[0,1]
	v_pk_mul_f32 v[192:193], v[118:119], v[194:195] op_sel_hi:[0,1]
	v_cvt_pk_bf16_f32 v36, v36, v37
	v_cvt_pk_bf16_f32 v37, v38, v39
	v_mov_b32_e32 v189, v188
	global_store_dwordx2 v[190:191], v[36:37], off
	v_cvt_pk_bf16_f32 v36, v192, v193
	v_cvt_pk_bf16_f32 v37, v178, v179
	v_mov_b32_e32 v178, v188
	v_mov_b32_e32 v179, v188
	global_store_dwordx2 v[190:191], v[36:37], off offset:32
	v_pk_mul_f32 v[36:37], v[186:187], v[188:189]
	v_pk_mul_f32 v[38:39], v[184:185], v[178:179]
	v_pk_mul_f32 v[182:183], v[182:183], v[188:189]
	v_pk_mul_f32 v[178:179], v[180:181], v[178:179]
	v_pk_mul_f32 v[38:39], v[26:27], v[38:39]
	v_pk_mul_f32 v[36:37], v[24:25], v[36:37]
	v_pk_mul_f32 v[180:181], v[22:23], v[178:179]
	v_pk_mul_f32 v[184:185], v[20:21], v[182:183]
	s_and_saveexec_b64 s[2:3], s[40:41]
	s_cbranch_execz .LBB0_292
	ds_read_b128 v[186:189], v226
	ds_read_b128 v[192:195], v226 offset:4096
	s_waitcnt lgkmcnt(1)
	v_pk_mul_f32 v[178:179], v[180:181], v[188:189]
	v_pk_mul_f32 v[182:183], v[184:185], v[186:187]
	v_pk_mul_f32 v[188:189], v[38:39], v[188:189]
	v_pk_mul_f32 v[186:187], v[36:37], v[186:187]
	s_waitcnt lgkmcnt(0)
	v_pk_fma_f32 v[38:39], v[38:39], v[194:195], v[178:179] neg_lo:[0,0,1] neg_hi:[0,0,1]
	v_pk_fma_f32 v[36:37], v[36:37], v[192:193], v[182:183] neg_lo:[0,0,1] neg_hi:[0,0,1]
	v_pk_fma_f32 v[180:181], v[180:181], v[194:195], v[188:189]
	v_pk_fma_f32 v[184:185], v[184:185], v[192:193], v[186:187]
.LBB0_292:
	s_or_b64 exec, exec, s[2:3]
	v_mov_b32_e32 v119, v118
	v_mov_b32_e32 v182, v118
	v_mov_b32_e32 v183, v118
	v_pk_mul_f32 v[38:39], v[182:183], v[38:39]
	v_pk_mul_f32 v[36:37], v[118:119], v[36:37]
	v_pk_mul_f32 v[178:179], v[182:183], v[180:181]
	v_pk_mul_f32 v[180:181], v[118:119], v[184:185]
	v_cvt_pk_bf16_f32 v36, v36, v37
	v_cvt_pk_bf16_f32 v37, v38, v39
	global_store_dwordx2 v[190:191], v[36:37], off offset:64
	v_cvt_pk_bf16_f32 v36, v180, v181
	v_or_b32_e32 v180, 16, v196
	v_cvt_pk_bf16_f32 v37, v178, v179
	v_ashrrev_i32_e32 v181, 31, v180
	global_store_dwordx2 v[190:191], v[36:37], off offset:96
	v_lshl_add_u64 v[36:37], v[180:181], 2, s[44:45]
	v_mov_b32_e32 v0, v217
	s_mov_b32 s2, 0x8000
	v_pk_mul_f32 v[38:39], v[18:19], v[0:1] op_sel_hi:[1,0]
	v_pk_mul_f32 v[36:37], v[16:17], v[0:1] op_sel_hi:[1,0]
	v_pk_mul_f32 v[38:39], v[38:39], v[174:175]
	v_pk_mul_f32 v[174:175], v[12:13], v[0:1] op_sel_hi:[1,0]
	v_pk_mul_f32 v[36:37], v[36:37], v[176:177]
	v_pk_mul_f32 v[172:173], v[174:175], v[172:173]
	v_pk_mul_f32 v[174:175], v[14:15], v[0:1] op_sel_hi:[1,0]
	v_mov_b32_e32 v176, v37
	v_mov_b32_e32 v177, v173
	v_pk_mul_f32 v[170:171], v[174:175], v[170:171]
	v_mov_b32_e32 v174, v36
	v_mov_b32_e32 v175, v172
	v_pk_mul_f32 v[176:177], v[176:177], v[176:177]
	s_nop 0
	v_pk_fma_f32 v[174:175], v[174:175], v[174:175], v[176:177]
	v_mov_b32_e32 v176, v38
	v_mov_b32_e32 v177, v170
	v_pk_fma_f32 v[174:175], v[176:177], v[176:177], v[174:175]
	v_mov_b32_e32 v176, v39
	v_mov_b32_e32 v177, v171
	v_pk_fma_f32 v[174:175], v[176:177], v[176:177], v[174:175]
	v_pk_mul_f32 v[176:177], v[8:9], v[0:1] op_sel_hi:[1,0]
	s_nop 0
	v_pk_mul_f32 v[168:169], v[176:177], v[168:169]
	v_pk_mul_f32 v[176:177], v[10:11], v[0:1] op_sel_hi:[1,0]
	v_mov_b32_e32 v179, v169
	v_pk_mul_f32 v[142:143], v[176:177], v[142:143]
	v_pk_mul_f32 v[176:177], v[4:5], v[0:1] op_sel_hi:[1,0]
	s_nop 0
	v_pk_mul_f32 v[140:141], v[176:177], v[140:141]
	v_pk_mul_f32 v[176:177], v[6:7], v[0:1] op_sel_hi:[1,0]
	v_mov_b32_e32 v178, v141
	v_pk_mul_f32 v[138:139], v[176:177], v[138:139]
	v_mov_b32_e32 v176, v140
	v_mov_b32_e32 v177, v168
	v_pk_mul_f32 v[178:179], v[178:179], v[178:179]
	v_add_f32_e32 v0, v174, v175
	v_pk_fma_f32 v[176:177], v[176:177], v[176:177], v[178:179]
	v_mov_b32_e32 v178, v138
	v_mov_b32_e32 v179, v142
	v_pk_fma_f32 v[176:177], v[178:179], v[178:179], v[176:177]
	v_mov_b32_e32 v178, v139
	v_mov_b32_e32 v179, v143
	v_pk_fma_f32 v[176:177], v[178:179], v[178:179], v[176:177]
	s_nop 0
	v_add_f32_e32 v0, v177, v0
	v_add_f32_e32 v0, v176, v0
	ds_bpermute_b32 v3, v204, v0
	s_waitcnt lgkmcnt(0)
	v_add_f32_e32 v0, v0, v3
	ds_bpermute_b32 v3, v205, v0
	s_waitcnt lgkmcnt(0)
	v_add_f32_e32 v0, v0, v3
	v_fmamk_f32 v0, v0, 0x3c800000, v246
	v_cmp_gt_f32_e32 vcc, s22, v0
	v_mul_f32_e32 v3, 0x4b800000, v0
	s_nop 0
	v_cndmask_b32_e32 v0, v0, v3, vcc
	v_rsq_f32_e32 v0, v0
	s_nop 0
	v_mul_f32_e32 v3, 0x45800000, v0
	v_cndmask_b32_e32 v174, v0, v3, vcc
	v_pk_mul_f32 v[36:37], v[36:37], v[174:175] op_sel_hi:[1,0]
	v_pk_mul_f32 v[38:39], v[38:39], v[174:175] op_sel_hi:[1,0]
	v_pk_mul_f32 v[176:177], v[172:173], v[174:175] op_sel_hi:[1,0]
	v_pk_mul_f32 v[170:171], v[170:171], v[174:175] op_sel_hi:[1,0]
	v_cmp_gt_i32_e32 vcc, s2, v180
	v_pk_mul_f32 v[38:39], v[34:35], v[38:39]
	v_pk_mul_f32 v[36:37], v[32:33], v[36:37]
	v_pk_mul_f32 v[172:173], v[30:31], v[170:171]
	v_pk_mul_f32 v[176:177], v[28:29], v[176:177]
	s_and_saveexec_b64 s[2:3], vcc
	s_cbranch_execz .LBB0_294
	s_and_b32 s30, s4, 0x7c0
	v_add_u32_e32 v170, s30, v225
	ds_read_b128 v[184:187], v170
	v_add_u32_e32 v170, s30, v225
	ds_read_b128 v[188:191], v170 offset:4096
	s_waitcnt lgkmcnt(1)
	v_pk_mul_f32 v[170:171], v[172:173], v[186:187]
	v_pk_mul_f32 v[178:179], v[176:177], v[184:185]
	v_pk_mul_f32 v[186:187], v[38:39], v[186:187]
	v_pk_mul_f32 v[184:185], v[36:37], v[184:185]
	s_waitcnt lgkmcnt(0)
	v_pk_fma_f32 v[38:39], v[38:39], v[190:191], v[170:171] neg_lo:[0,0,1] neg_hi:[0,0,1]
	v_pk_fma_f32 v[36:37], v[36:37], v[188:189], v[178:179] neg_lo:[0,0,1] neg_hi:[0,0,1]
	v_pk_fma_f32 v[172:173], v[172:173], v[190:191], v[186:187]
	v_pk_fma_f32 v[176:177], v[176:177], v[188:189], v[184:185]
; __device__ __forceinline__ unsigned pk2(float lo, float hi) { f32x2_t v = {lo, hi}; bf16x2_t b = __builtin_convertvector(v, bf16x2_t); return __builtin_bit_cast(unsigned, b); }
; __device__ __forceinline__ float shx(float v, int m, int lane) { return __int_as_float(__builtin_amdgcn_ds_bpermute((lane ^ m) << 2, __float_as_int(v))); }
;     __device__ __forceinline__ void operator()(const pg8::i32x4 (&acc)[2][2][4][2], const Unit& u, int wr, int wc, int fr, int fq) const {
;     ...
;             for (int ai = 0; ai < 2; ++ai)
; #pragma unroll
;                 for (int m = 0; m < 4; ++m) {
;                     const int row = u.pm * 256 + ai * 128 + wr * 64 + m * 16 + fr;
;                     float ss = 0.f; const float sa = sah[row]; f32x4 xf[2][2];
; #pragma unroll
;                     for (int bj = 0; bj < 2; ++bj)
; #pragma unroll
;                         for (int n = 0; n < 2; ++n) { f32x4 x;
; #pragma unroll
;                             for (int i = 0; i < 4; ++i) x[i] = (float)acc[ai][bj][m][n][i] * (sa * swv[bj][n][i]);
;                             xf[bj][n] = x; ss += x[0] * x[0] + x[1] * x[1] + x[2] * x[2] + x[3] * x[3]; }
;                     { const int ln = fq * 16 + fr; ss += shx(ss, 16, ln); ss += shx(ss, 32, ln); }
;                     const float rstd = rsqrtf(ss * (1.f / 64.f) + EPS);
;                     const bool lat = row < NL; const int tok = row & 2047;
; #pragma unroll
;                     for (int bj = 0; bj < 2; ++bj) {
;                         f32x4 x1 = xf[bj][0] * rstd * w[bj][0], x2 = xf[bj][1] * rstd * w[bj][1];
;                         if (lat) { const int pos = bj ? (tok & 63) : (tok >> 6); const f32x4 c = *(const f32x4*)(ropec + pos * 16 + 4 * fq), s = *(const f32x4*)(ropes + pos * 16 + 4 * fq);
;                             const f32x4 o1 = x1 * c - x2 * s, o2 = x1 * s + x2 * c; x1 = o1; x2 = o2; }
;                         x1 = x1 * osc; x2 = x2 * osc;
;                         bf16_t* p = base + (size_t)row * 512 + 64 * hg + 32 * bj + 4 * fq;
;                         *(u32x2*)p = (u32x2){pk2(x1[0], x1[1]), pk2(x1[2], x1[3])};
;                         *(u32x2*)(p + 16) = (u32x2){pk2(x2[0], x2[1]), pk2(x2[2], x2[3])};
;                     }
.LBB0_294:
	s_or_b64 exec, exec, s[2:3]
	v_lshlrev_b64 v[170:171], 10, v[180:181]
	v_pk_mul_f32 v[38:39], v[182:183], v[38:39]
	v_pk_mul_f32 v[36:37], v[118:119], v[36:37]
	v_lshl_add_u64 v[170:171], v[128:129], 0, v[170:171]
	v_pk_mul_f32 v[172:173], v[182:183], v[172:173]
	v_pk_mul_f32 v[176:177], v[118:119], v[176:177]
	v_cvt_pk_bf16_f32 v36, v36, v37
	v_cvt_pk_bf16_f32 v37, v38, v39
	v_mov_b32_e32 v175, v174
	global_store_dwordx2 v[170:171], v[36:37], off
	v_cvt_pk_bf16_f32 v36, v176, v177
	v_cvt_pk_bf16_f32 v37, v172, v173
	global_store_dwordx2 v[170:171], v[36:37], off offset:32
	v_pk_mul_f32 v[36:37], v[168:169], v[174:175]
	v_mov_b32_e32 v168, v174
	v_mov_b32_e32 v169, v174
	v_pk_mul_f32 v[38:39], v[142:143], v[168:169]
	v_pk_mul_f32 v[140:141], v[140:141], v[174:175]
	v_pk_mul_f32 v[138:139], v[138:139], v[168:169]
	v_pk_mul_f32 v[38:39], v[26:27], v[38:39]
	v_pk_mul_f32 v[36:37], v[24:25], v[36:37]
	v_pk_mul_f32 v[138:139], v[22:23], v[138:139]
	v_pk_mul_f32 v[142:143], v[20:21], v[140:141]
	s_and_saveexec_b64 s[2:3], vcc
	s_cbranch_execz .LBB0_296
	v_lshlrev_b32_e32 v0, 6, v180
	v_and_b32_e32 v140, 0x7c0, v0
	v_mov_b32_e32 v141, v145
	v_add_u32_e32 v168, v140, v225
	ds_read_b128 v[172:175], v168
	v_add_u32_e32 v140, v140, v225
	ds_read_b128 v[180:183], v140 offset:4096
	s_waitcnt lgkmcnt(1)
	v_pk_mul_f32 v[140:141], v[138:139], v[174:175]
	v_pk_mul_f32 v[168:169], v[142:143], v[172:173]
	v_pk_mul_f32 v[174:175], v[38:39], v[174:175]
	v_pk_mul_f32 v[172:173], v[36:37], v[172:173]
	s_waitcnt lgkmcnt(0)
	v_pk_fma_f32 v[38:39], v[38:39], v[182:183], v[140:141] neg_lo:[0,0,1] neg_hi:[0,0,1]
	v_pk_fma_f32 v[36:37], v[36:37], v[180:181], v[168:169] neg_lo:[0,0,1] neg_hi:[0,0,1]
	v_pk_fma_f32 v[138:139], v[138:139], v[182:183], v[174:175]
	v_pk_fma_f32 v[142:143], v[142:143], v[180:181], v[172:173]
.LBB0_296:
	s_or_b64 exec, exec, s[2:3]
	v_mov_b32_e32 v140, v118
	v_mov_b32_e32 v141, v118
	v_pk_mul_f32 v[38:39], v[140:141], v[38:39]
	v_pk_mul_f32 v[36:37], v[118:119], v[36:37]
	v_pk_mul_f32 v[138:139], v[140:141], v[138:139]
	v_cvt_pk_bf16_f32 v36, v36, v37
	v_cvt_pk_bf16_f32 v37, v38, v39
	v_pk_mul_f32 v[142:143], v[118:119], v[142:143]
	global_store_dwordx2 v[170:171], v[36:37], off offset:64
	v_cvt_pk_bf16_f32 v37, v138, v139
	v_or_b32_e32 v138, 32, v196
	v_cvt_pk_bf16_f32 v36, v142, v143
	v_ashrrev_i32_e32 v139, 31, v138
	global_store_dwordx2 v[170:171], v[36:37], off offset:96
	v_lshl_add_u64 v[36:37], v[138:139], 2, s[44:45]
	v_mov_b32_e32 v0, v218
	s_mov_b32 s2, 0x8000
	v_pk_mul_f32 v[38:39], v[18:19], v[0:1] op_sel_hi:[1,0]
	v_pk_mul_f32 v[36:37], v[16:17], v[0:1] op_sel_hi:[1,0]
	v_pk_mul_f32 v[38:39], v[38:39], v[134:135]
	v_pk_mul_f32 v[134:135], v[12:13], v[0:1] op_sel_hi:[1,0]
	v_pk_mul_f32 v[36:37], v[36:37], v[136:137]
	v_pk_mul_f32 v[132:133], v[134:135], v[132:133]
	v_pk_mul_f32 v[134:135], v[14:15], v[0:1] op_sel_hi:[1,0]
	v_mov_b32_e32 v136, v37
	v_mov_b32_e32 v137, v133
	v_pk_mul_f32 v[130:131], v[134:135], v[130:131]
	v_mov_b32_e32 v134, v36
	v_mov_b32_e32 v135, v132
	v_pk_mul_f32 v[136:137], v[136:137], v[136:137]
	s_nop 0
	v_pk_fma_f32 v[134:135], v[134:135], v[134:135], v[136:137]
	v_mov_b32_e32 v136, v38
	v_mov_b32_e32 v137, v130
	v_pk_fma_f32 v[134:135], v[136:137], v[136:137], v[134:135]
	v_mov_b32_e32 v136, v39
	v_mov_b32_e32 v137, v131
	v_pk_fma_f32 v[134:135], v[136:137], v[136:137], v[134:135]
	v_pk_mul_f32 v[136:137], v[8:9], v[0:1] op_sel_hi:[1,0]
	s_nop 0
	v_pk_mul_f32 v[126:127], v[136:137], v[126:127]
	v_pk_mul_f32 v[136:137], v[10:11], v[0:1] op_sel_hi:[1,0]
	v_mov_b32_e32 v143, v127
	v_pk_mul_f32 v[124:125], v[136:137], v[124:125]
	v_pk_mul_f32 v[136:137], v[4:5], v[0:1] op_sel_hi:[1,0]
	s_nop 0
	v_pk_mul_f32 v[122:123], v[136:137], v[122:123]
	v_pk_mul_f32 v[136:137], v[6:7], v[0:1] op_sel_hi:[1,0]
	v_mov_b32_e32 v142, v123
	v_pk_mul_f32 v[120:121], v[136:137], v[120:121]
	v_mov_b32_e32 v136, v122
	v_mov_b32_e32 v137, v126
	v_pk_mul_f32 v[142:143], v[142:143], v[142:143]
	v_add_f32_e32 v0, v134, v135
	v_pk_fma_f32 v[136:137], v[136:137], v[136:137], v[142:143]
	v_mov_b32_e32 v142, v120
	v_mov_b32_e32 v143, v124
	v_pk_fma_f32 v[136:137], v[142:143], v[142:143], v[136:137]
	v_mov_b32_e32 v142, v121
	v_mov_b32_e32 v143, v125
	v_pk_fma_f32 v[136:137], v[142:143], v[142:143], v[136:137]
	s_nop 0
	v_add_f32_e32 v0, v137, v0
	v_add_f32_e32 v0, v136, v0
	ds_bpermute_b32 v3, v204, v0
	s_waitcnt lgkmcnt(0)
	v_add_f32_e32 v0, v0, v3
	ds_bpermute_b32 v3, v205, v0
	s_waitcnt lgkmcnt(0)
	v_add_f32_e32 v0, v0, v3
	v_fmamk_f32 v0, v0, 0x3c800000, v246
	v_cmp_gt_f32_e32 vcc, s22, v0
	v_mul_f32_e32 v3, 0x4b800000, v0
	s_nop 0
	v_cndmask_b32_e32 v0, v0, v3, vcc
	v_rsq_f32_e32 v0, v0
	s_nop 0
	v_mul_f32_e32 v3, 0x45800000, v0
	v_cndmask_b32_e32 v134, v0, v3, vcc
	v_pk_mul_f32 v[36:37], v[36:37], v[134:135] op_sel_hi:[1,0]
	v_pk_mul_f32 v[38:39], v[38:39], v[134:135] op_sel_hi:[1,0]
	v_pk_mul_f32 v[136:137], v[132:133], v[134:135] op_sel_hi:[1,0]
	v_pk_mul_f32 v[130:131], v[130:131], v[134:135] op_sel_hi:[1,0]
	v_cmp_gt_i32_e32 vcc, s2, v138
	v_pk_mul_f32 v[38:39], v[34:35], v[38:39]
	v_pk_mul_f32 v[36:37], v[32:33], v[36:37]
	v_pk_mul_f32 v[132:133], v[30:31], v[130:131]
	v_pk_mul_f32 v[136:137], v[28:29], v[136:137]
	s_and_saveexec_b64 s[2:3], vcc
	s_cbranch_execz .LBB0_298
	s_and_b32 s30, s4, 0x7c0
	v_add_u32_e32 v130, s30, v225
	ds_read_b128 v[168:171], v130
	v_add_u32_e32 v130, s30, v225
	ds_read_b128 v[172:175], v130 offset:4096
	s_waitcnt lgkmcnt(1)
	v_pk_mul_f32 v[130:131], v[132:133], v[170:171]
	v_pk_mul_f32 v[142:143], v[136:137], v[168:169]
	v_pk_mul_f32 v[170:171], v[38:39], v[170:171]
	v_pk_mul_f32 v[168:169], v[36:37], v[168:169]
	s_waitcnt lgkmcnt(0)
	v_pk_fma_f32 v[38:39], v[38:39], v[174:175], v[130:131] neg_lo:[0,0,1] neg_hi:[0,0,1]
	v_pk_fma_f32 v[36:37], v[36:37], v[172:173], v[142:143] neg_lo:[0,0,1] neg_hi:[0,0,1]
	v_pk_fma_f32 v[132:133], v[132:133], v[174:175], v[170:171]
	v_pk_fma_f32 v[136:137], v[136:137], v[172:173], v[168:169]
; __device__ __forceinline__ unsigned pk2(float lo, float hi) { f32x2_t v = {lo, hi}; bf16x2_t b = __builtin_convertvector(v, bf16x2_t); return __builtin_bit_cast(unsigned, b); }
; __device__ __forceinline__ float shx(float v, int m, int lane) { return __int_as_float(__builtin_amdgcn_ds_bpermute((lane ^ m) << 2, __float_as_int(v))); }
;     __device__ __forceinline__ void operator()(const pg8::i32x4 (&acc)[2][2][4][2], const Unit& u, int wr, int wc, int fr, int fq) const {
;     ...
;             for (int ai = 0; ai < 2; ++ai)
; #pragma unroll
;                 for (int m = 0; m < 4; ++m) {
;                     const int row = u.pm * 256 + ai * 128 + wr * 64 + m * 16 + fr;
;                     float ss = 0.f; const float sa = sah[row]; f32x4 xf[2][2];
; #pragma unroll
;                     for (int bj = 0; bj < 2; ++bj)
; #pragma unroll
;                         for (int n = 0; n < 2; ++n) { f32x4 x;
; #pragma unroll
;                             for (int i = 0; i < 4; ++i) x[i] = (float)acc[ai][bj][m][n][i] * (sa * swv[bj][n][i]);
;                             xf[bj][n] = x; ss += x[0] * x[0] + x[1] * x[1] + x[2] * x[2] + x[3] * x[3]; }
;                     { const int ln = fq * 16 + fr; ss += shx(ss, 16, ln); ss += shx(ss, 32, ln); }
;                     const float rstd = rsqrtf(ss * (1.f / 64.f) + EPS);
;                     const bool lat = row < NL; const int tok = row & 2047;
; #pragma unroll
;                     for (int bj = 0; bj < 2; ++bj) {
;                         f32x4 x1 = xf[bj][0] * rstd * w[bj][0], x2 = xf[bj][1] * rstd * w[bj][1];
;                         if (lat) { const int pos = bj ? (tok & 63) : (tok >> 6); const f32x4 c = *(const f32x4*)(ropec + pos * 16 + 4 * fq), s = *(const f32x4*)(ropes + pos * 16 + 4 * fq);
;                             const f32x4 o1 = x1 * c - x2 * s, o2 = x1 * s + x2 * c; x1 = o1; x2 = o2; }
;                         x1 = x1 * osc; x2 = x2 * osc;
;                         bf16_t* p = base + (size_t)row * 512 + 64 * hg + 32 * bj + 4 * fq;
;                         *(u32x2*)p = (u32x2){pk2(x1[0], x1[1]), pk2(x1[2], x1[3])};
;                         *(u32x2*)(p + 16) = (u32x2){pk2(x2[0], x2[1]), pk2(x2[2], x2[3])};
;                     }
.LBB0_298:
	s_or_b64 exec, exec, s[2:3]
	v_lshlrev_b64 v[130:131], 10, v[138:139]
	v_pk_mul_f32 v[38:39], v[140:141], v[38:39]
	v_pk_mul_f32 v[36:37], v[118:119], v[36:37]
	v_lshl_add_u64 v[130:131], v[128:129], 0, v[130:131]
	v_pk_mul_f32 v[132:133], v[140:141], v[132:133]
	v_pk_mul_f32 v[136:137], v[118:119], v[136:137]
	v_cvt_pk_bf16_f32 v36, v36, v37
	v_cvt_pk_bf16_f32 v37, v38, v39
	v_mov_b32_e32 v135, v134
	global_store_dwordx2 v[130:131], v[36:37], off
	v_cvt_pk_bf16_f32 v36, v136, v137
	v_cvt_pk_bf16_f32 v37, v132, v133
	global_store_dwordx2 v[130:131], v[36:37], off offset:32
	v_pk_mul_f32 v[36:37], v[126:127], v[134:135]
	v_mov_b32_e32 v126, v134
	v_mov_b32_e32 v127, v134
	v_pk_mul_f32 v[38:39], v[124:125], v[126:127]
	v_pk_mul_f32 v[122:123], v[122:123], v[134:135]
	v_pk_mul_f32 v[120:121], v[120:121], v[126:127]
	v_pk_mul_f32 v[38:39], v[26:27], v[38:39]
	v_pk_mul_f32 v[36:37], v[24:25], v[36:37]
	v_pk_mul_f32 v[120:121], v[22:23], v[120:121]
	v_pk_mul_f32 v[124:125], v[20:21], v[122:123]
	s_and_saveexec_b64 s[2:3], vcc
	s_cbranch_execz .LBB0_300
	v_lshlrev_b32_e32 v0, 6, v138
	v_and_b32_e32 v122, 0xbc0, v0
	v_mov_b32_e32 v123, v145
	v_add_u32_e32 v126, v122, v225
	ds_read_b128 v[132:135], v126
	v_add_u32_e32 v122, v122, v225
	ds_read_b128 v[136:139], v122 offset:4096
	s_waitcnt lgkmcnt(1)
	v_pk_mul_f32 v[122:123], v[120:121], v[134:135]
	v_pk_mul_f32 v[126:127], v[124:125], v[132:133]
	v_pk_mul_f32 v[134:135], v[38:39], v[134:135]
	v_pk_mul_f32 v[132:133], v[36:37], v[132:133]
	s_waitcnt lgkmcnt(0)
	v_pk_fma_f32 v[38:39], v[38:39], v[138:139], v[122:123] neg_lo:[0,0,1] neg_hi:[0,0,1]
	v_pk_fma_f32 v[36:37], v[36:37], v[136:137], v[126:127] neg_lo:[0,0,1] neg_hi:[0,0,1]
	v_pk_fma_f32 v[120:121], v[120:121], v[138:139], v[134:135]
	v_pk_fma_f32 v[124:125], v[124:125], v[136:137], v[132:133]
.LBB0_300:
	s_or_b64 exec, exec, s[2:3]
	v_mov_b32_e32 v122, v118
	v_mov_b32_e32 v123, v118
	v_pk_mul_f32 v[38:39], v[122:123], v[38:39]
	v_pk_mul_f32 v[36:37], v[118:119], v[36:37]
	v_pk_mul_f32 v[120:121], v[122:123], v[120:121]
	v_cvt_pk_bf16_f32 v36, v36, v37
	v_cvt_pk_bf16_f32 v37, v38, v39
	v_pk_mul_f32 v[124:125], v[118:119], v[124:125]
	global_store_dwordx2 v[130:131], v[36:37], off offset:64
	v_cvt_pk_bf16_f32 v37, v120, v121
	v_or_b32_e32 v120, 48, v196
	v_cvt_pk_bf16_f32 v36, v124, v125
	v_ashrrev_i32_e32 v121, 31, v120
	global_store_dwordx2 v[130:131], v[36:37], off offset:96
	v_lshl_add_u64 v[36:37], v[120:121], 2, s[44:45]
	v_mov_b32_e32 v0, v219
	s_mov_b32 s2, 0x8000
	v_pk_mul_f32 v[38:39], v[18:19], v[0:1] op_sel_hi:[1,0]
	v_pk_mul_f32 v[36:37], v[16:17], v[0:1] op_sel_hi:[1,0]
	v_pk_mul_f32 v[38:39], v[38:39], v[114:115]
	v_pk_mul_f32 v[114:115], v[12:13], v[0:1] op_sel_hi:[1,0]
	v_pk_mul_f32 v[36:37], v[36:37], v[116:117]
	v_pk_mul_f32 v[112:113], v[114:115], v[112:113]
	v_pk_mul_f32 v[114:115], v[14:15], v[0:1] op_sel_hi:[1,0]
	v_mov_b32_e32 v116, v37
	v_mov_b32_e32 v117, v113
	v_pk_mul_f32 v[110:111], v[114:115], v[110:111]
	v_mov_b32_e32 v114, v36
	v_mov_b32_e32 v115, v112
	v_pk_mul_f32 v[116:117], v[116:117], v[116:117]
	s_nop 0
	v_pk_fma_f32 v[114:115], v[114:115], v[114:115], v[116:117]
	v_mov_b32_e32 v116, v38
	v_mov_b32_e32 v117, v110
	v_pk_fma_f32 v[114:115], v[116:117], v[116:117], v[114:115]
	v_mov_b32_e32 v116, v39
	v_mov_b32_e32 v117, v111
	v_pk_fma_f32 v[114:115], v[116:117], v[116:117], v[114:115]
	v_pk_mul_f32 v[116:117], v[8:9], v[0:1] op_sel_hi:[1,0]
	s_nop 0
	v_pk_mul_f32 v[108:109], v[116:117], v[108:109]
	v_pk_mul_f32 v[116:117], v[10:11], v[0:1] op_sel_hi:[1,0]
	v_mov_b32_e32 v125, v109
	v_pk_mul_f32 v[106:107], v[116:117], v[106:107]
	v_pk_mul_f32 v[116:117], v[4:5], v[0:1] op_sel_hi:[1,0]
	s_nop 0
	v_pk_mul_f32 v[104:105], v[116:117], v[104:105]
	v_pk_mul_f32 v[116:117], v[6:7], v[0:1] op_sel_hi:[1,0]
	v_mov_b32_e32 v124, v105
	v_pk_mul_f32 v[102:103], v[116:117], v[102:103]
	v_mov_b32_e32 v116, v104
	v_mov_b32_e32 v117, v108
	v_pk_mul_f32 v[124:125], v[124:125], v[124:125]
	v_add_f32_e32 v0, v114, v115
	v_pk_fma_f32 v[116:117], v[116:117], v[116:117], v[124:125]
	v_mov_b32_e32 v124, v102
	v_mov_b32_e32 v125, v106
	v_pk_fma_f32 v[116:117], v[124:125], v[124:125], v[116:117]
	v_mov_b32_e32 v124, v103
	v_mov_b32_e32 v125, v107
	v_pk_fma_f32 v[116:117], v[124:125], v[124:125], v[116:117]
	s_nop 0
	v_add_f32_e32 v0, v117, v0
	v_add_f32_e32 v0, v116, v0
	ds_bpermute_b32 v3, v204, v0
	s_waitcnt lgkmcnt(0)
	v_add_f32_e32 v0, v0, v3
	ds_bpermute_b32 v3, v205, v0
	s_waitcnt lgkmcnt(0)
	v_add_f32_e32 v0, v0, v3
	v_fmamk_f32 v0, v0, 0x3c800000, v246
	v_cmp_gt_f32_e32 vcc, s22, v0
	v_mul_f32_e32 v3, 0x4b800000, v0
	s_nop 0
	v_cndmask_b32_e32 v0, v0, v3, vcc
	v_rsq_f32_e32 v0, v0
	s_nop 0
	v_mul_f32_e32 v3, 0x45800000, v0
	v_cndmask_b32_e32 v114, v0, v3, vcc
	v_pk_mul_f32 v[36:37], v[36:37], v[114:115] op_sel_hi:[1,0]
	v_pk_mul_f32 v[38:39], v[38:39], v[114:115] op_sel_hi:[1,0]
	v_pk_mul_f32 v[116:117], v[112:113], v[114:115] op_sel_hi:[1,0]
	v_pk_mul_f32 v[110:111], v[110:111], v[114:115] op_sel_hi:[1,0]
	v_cmp_gt_i32_e32 vcc, s2, v120
	v_pk_mul_f32 v[38:39], v[34:35], v[38:39]
	v_pk_mul_f32 v[36:37], v[32:33], v[36:37]
	v_pk_mul_f32 v[112:113], v[30:31], v[110:111]
	v_pk_mul_f32 v[116:117], v[28:29], v[116:117]
	s_and_saveexec_b64 s[2:3], vcc
	s_cbranch_execz .LBB0_302
	s_and_b32 s30, s4, 0x7c0
	v_add_u32_e32 v110, s30, v225
	ds_read_b128 v[124:127], v110
	v_add_u32_e32 v110, s30, v225
	ds_read_b128 v[130:133], v110 offset:4096
	s_waitcnt lgkmcnt(1)
	v_pk_mul_f32 v[110:111], v[112:113], v[126:127]
	v_pk_mul_f32 v[134:135], v[116:117], v[124:125]
	v_pk_mul_f32 v[126:127], v[38:39], v[126:127]
	v_pk_mul_f32 v[124:125], v[36:37], v[124:125]
	s_waitcnt lgkmcnt(0)
	v_pk_fma_f32 v[38:39], v[38:39], v[132:133], v[110:111] neg_lo:[0,0,1] neg_hi:[0,0,1]
	v_pk_fma_f32 v[36:37], v[36:37], v[130:131], v[134:135] neg_lo:[0,0,1] neg_hi:[0,0,1]
	v_pk_fma_f32 v[112:113], v[112:113], v[132:133], v[126:127]
	v_pk_fma_f32 v[116:117], v[116:117], v[130:131], v[124:125]
; __device__ __forceinline__ unsigned pk2(float lo, float hi) { f32x2_t v = {lo, hi}; bf16x2_t b = __builtin_convertvector(v, bf16x2_t); return __builtin_bit_cast(unsigned, b); }
; __device__ __forceinline__ float shx(float v, int m, int lane) { return __int_as_float(__builtin_amdgcn_ds_bpermute((lane ^ m) << 2, __float_as_int(v))); }
;     __device__ __forceinline__ void operator()(const pg8::i32x4 (&acc)[2][2][4][2], const Unit& u, int wr, int wc, int fr, int fq) const {
;     ...
; #pragma unroll
;             for (int ai = 0; ai < 2; ++ai)
; #pragma unroll
;                 for (int m = 0; m < 4; ++m) {
;                     const int row = u.pm * 256 + ai * 128 + wr * 64 + m * 16 + fr;
;                     float ss = 0.f; const float sa = sah[row]; f32x4 xf[2][2];
; #pragma unroll
;                     for (int bj = 0; bj < 2; ++bj)
; #pragma unroll
;                         for (int n = 0; n < 2; ++n) { f32x4 x;
; #pragma unroll
;                             for (int i = 0; i < 4; ++i) x[i] = (float)acc[ai][bj][m][n][i] * (sa * swv[bj][n][i]);
;                             xf[bj][n] = x; ss += x[0] * x[0] + x[1] * x[1] + x[2] * x[2] + x[3] * x[3]; }
;                     { const int ln = fq * 16 + fr; ss += shx(ss, 16, ln); ss += shx(ss, 32, ln); }
;                     const float rstd = rsqrtf(ss * (1.f / 64.f) + EPS);
;                     const bool lat = row < NL; const int tok = row & 2047;
; #pragma unroll
;                     for (int bj = 0; bj < 2; ++bj) {
;                         f32x4 x1 = xf[bj][0] * rstd * w[bj][0], x2 = xf[bj][1] * rstd * w[bj][1];
;                         if (lat) { const int pos = bj ? (tok & 63) : (tok >> 6); const f32x4 c = *(const f32x4*)(ropec + pos * 16 + 4 * fq), s = *(const f32x4*)(ropes + pos * 16 + 4 * fq);
;                             const f32x4 o1 = x1 * c - x2 * s, o2 = x1 * s + x2 * c; x1 = o1; x2 = o2; }
;                         x1 = x1 * osc; x2 = x2 * osc;
;                         bf16_t* p = base + (size_t)row * 512 + 64 * hg + 32 * bj + 4 * fq;
;                         *(u32x2*)p = (u32x2){pk2(x1[0], x1[1]), pk2(x1[2], x1[3])};
;                         *(u32x2*)(p + 16) = (u32x2){pk2(x2[0], x2[1]), pk2(x2[2], x2[3])};
;                     }
.LBB0_302:
	s_or_b64 exec, exec, s[2:3]
	v_lshlrev_b64 v[110:111], 10, v[120:121]
	v_pk_mul_f32 v[38:39], v[122:123], v[38:39]
	v_pk_mul_f32 v[36:37], v[118:119], v[36:37]
	v_lshl_add_u64 v[110:111], v[128:129], 0, v[110:111]
	v_pk_mul_f32 v[112:113], v[122:123], v[112:113]
	v_pk_mul_f32 v[116:117], v[118:119], v[116:117]
	v_cvt_pk_bf16_f32 v36, v36, v37
	v_cvt_pk_bf16_f32 v37, v38, v39
	v_mov_b32_e32 v115, v114
	global_store_dwordx2 v[110:111], v[36:37], off
	v_cvt_pk_bf16_f32 v36, v116, v117
	v_cvt_pk_bf16_f32 v37, v112, v113
	global_store_dwordx2 v[110:111], v[36:37], off offset:32
	v_pk_mul_f32 v[36:37], v[108:109], v[114:115]
	v_mov_b32_e32 v108, v114
	v_mov_b32_e32 v109, v114
	v_pk_mul_f32 v[38:39], v[106:107], v[108:109]
	v_pk_mul_f32 v[104:105], v[104:105], v[114:115]
	v_pk_mul_f32 v[102:103], v[102:103], v[108:109]
	v_pk_mul_f32 v[38:39], v[26:27], v[38:39]
	v_pk_mul_f32 v[36:37], v[24:25], v[36:37]
	v_pk_mul_f32 v[102:103], v[22:23], v[102:103]
	v_pk_mul_f32 v[106:107], v[20:21], v[104:105]
	s_and_saveexec_b64 s[2:3], vcc
	s_cbranch_execz .LBB0_304
	v_lshlrev_b32_e32 v0, 6, v120
	v_and_b32_e32 v104, 0xfc0, v0
	v_mov_b32_e32 v105, v145
	v_add_u32_e32 v108, v104, v225
	ds_read_b128 v[112:115], v108
	v_add_u32_e32 v104, v104, v225
	ds_read_b128 v[120:123], v104 offset:4096
	s_waitcnt lgkmcnt(1)
	v_pk_mul_f32 v[104:105], v[102:103], v[114:115]
	v_pk_mul_f32 v[108:109], v[106:107], v[112:113]
	v_pk_mul_f32 v[114:115], v[38:39], v[114:115]
	v_pk_mul_f32 v[112:113], v[36:37], v[112:113]
	s_waitcnt lgkmcnt(0)
	v_pk_fma_f32 v[38:39], v[38:39], v[122:123], v[104:105] neg_lo:[0,0,1] neg_hi:[0,0,1]
	v_pk_fma_f32 v[36:37], v[36:37], v[120:121], v[108:109] neg_lo:[0,0,1] neg_hi:[0,0,1]
	v_pk_fma_f32 v[102:103], v[102:103], v[122:123], v[114:115]
	v_pk_fma_f32 v[106:107], v[106:107], v[120:121], v[112:113]
.LBB0_304:
	s_or_b64 exec, exec, s[2:3]
	v_mov_b32_e32 v104, v118
	v_mov_b32_e32 v105, v118
	v_pk_mul_f32 v[38:39], v[104:105], v[38:39]
	v_pk_mul_f32 v[36:37], v[118:119], v[36:37]
	v_pk_mul_f32 v[102:103], v[104:105], v[102:103]
	v_cvt_pk_bf16_f32 v36, v36, v37
	v_cvt_pk_bf16_f32 v37, v38, v39
	s_addk_i32 s4, 0x80
	v_pk_mul_f32 v[106:107], v[118:119], v[106:107]
	global_store_dwordx2 v[110:111], v[36:37], off offset:64
	v_cvt_pk_bf16_f32 v37, v102, v103
	v_or_b32_e32 v102, s4, v198
	v_cvt_pk_bf16_f32 v36, v106, v107
	v_ashrrev_i32_e32 v103, 31, v102
	global_store_dwordx2 v[110:111], v[36:37], off offset:96
	v_lshl_add_u64 v[36:37], v[102:103], 2, s[44:45]
	v_mov_b32_e32 v0, v220
	s_mov_b32 s2, 0x8000
	v_pk_mul_f32 v[38:39], v[18:19], v[0:1] op_sel_hi:[1,0]
	v_pk_mul_f32 v[36:37], v[16:17], v[0:1] op_sel_hi:[1,0]
	v_pk_mul_f32 v[38:39], v[38:39], v[98:99]
	v_pk_mul_f32 v[98:99], v[12:13], v[0:1] op_sel_hi:[1,0]
	v_pk_mul_f32 v[36:37], v[36:37], v[100:101]
	v_pk_mul_f32 v[96:97], v[98:99], v[96:97]
	v_pk_mul_f32 v[98:99], v[14:15], v[0:1] op_sel_hi:[1,0]
	v_mov_b32_e32 v100, v37
	v_mov_b32_e32 v101, v97
	v_pk_mul_f32 v[94:95], v[98:99], v[94:95]
	v_mov_b32_e32 v98, v36
	v_mov_b32_e32 v99, v96
	v_pk_mul_f32 v[100:101], v[100:101], v[100:101]
	s_nop 0
	v_pk_fma_f32 v[98:99], v[98:99], v[98:99], v[100:101]
	v_mov_b32_e32 v100, v38
	v_mov_b32_e32 v101, v94
	v_pk_fma_f32 v[98:99], v[100:101], v[100:101], v[98:99]
	v_mov_b32_e32 v100, v39
	v_mov_b32_e32 v101, v95
	v_pk_fma_f32 v[98:99], v[100:101], v[100:101], v[98:99]
	v_pk_mul_f32 v[100:101], v[8:9], v[0:1] op_sel_hi:[1,0]
	s_nop 0
	v_pk_mul_f32 v[92:93], v[100:101], v[92:93]
	v_pk_mul_f32 v[100:101], v[10:11], v[0:1] op_sel_hi:[1,0]
	v_mov_b32_e32 v107, v93
	v_pk_mul_f32 v[90:91], v[100:101], v[90:91]
	v_pk_mul_f32 v[100:101], v[4:5], v[0:1] op_sel_hi:[1,0]
	s_nop 0
	v_pk_mul_f32 v[88:89], v[100:101], v[88:89]
	v_pk_mul_f32 v[100:101], v[6:7], v[0:1] op_sel_hi:[1,0]
	v_mov_b32_e32 v106, v89
	v_pk_mul_f32 v[86:87], v[100:101], v[86:87]
	v_mov_b32_e32 v100, v88
	v_mov_b32_e32 v101, v92
	v_pk_mul_f32 v[106:107], v[106:107], v[106:107]
	v_add_f32_e32 v0, v98, v99
	v_pk_fma_f32 v[100:101], v[100:101], v[100:101], v[106:107]
	v_mov_b32_e32 v106, v86
	v_mov_b32_e32 v107, v90
	v_pk_fma_f32 v[100:101], v[106:107], v[106:107], v[100:101]
	v_mov_b32_e32 v106, v87
	v_mov_b32_e32 v107, v91
	v_pk_fma_f32 v[100:101], v[106:107], v[106:107], v[100:101]
	s_nop 0
	v_add_f32_e32 v0, v101, v0
	v_add_f32_e32 v0, v100, v0
	ds_bpermute_b32 v3, v204, v0
	s_waitcnt lgkmcnt(0)
	v_add_f32_e32 v0, v0, v3
	ds_bpermute_b32 v3, v205, v0
	s_waitcnt lgkmcnt(0)
	v_add_f32_e32 v0, v0, v3
	v_fmamk_f32 v0, v0, 0x3c800000, v246
	v_cmp_gt_f32_e32 vcc, s22, v0
	v_mul_f32_e32 v3, 0x4b800000, v0
	s_nop 0
	v_cndmask_b32_e32 v0, v0, v3, vcc
	v_rsq_f32_e32 v0, v0
	s_nop 0
	v_mul_f32_e32 v3, 0x45800000, v0
	v_cndmask_b32_e32 v98, v0, v3, vcc
	v_pk_mul_f32 v[36:37], v[36:37], v[98:99] op_sel_hi:[1,0]
	v_pk_mul_f32 v[38:39], v[38:39], v[98:99] op_sel_hi:[1,0]
	v_pk_mul_f32 v[100:101], v[96:97], v[98:99] op_sel_hi:[1,0]
	v_pk_mul_f32 v[94:95], v[94:95], v[98:99] op_sel_hi:[1,0]
	v_cmp_gt_i32_e32 vcc, s2, v102
	v_pk_mul_f32 v[38:39], v[34:35], v[38:39]
	v_pk_mul_f32 v[36:37], v[32:33], v[36:37]
	v_pk_mul_f32 v[96:97], v[30:31], v[94:95]
	v_pk_mul_f32 v[100:101], v[28:29], v[100:101]
	s_and_saveexec_b64 s[2:3], vcc
	s_cbranch_execz .LBB0_306
	s_and_b32 s30, s4, 0x7c0
	v_add_u32_e32 v94, s30, v225
	ds_read_b128 v[106:109], v94
	v_add_u32_e32 v94, s30, v225
	ds_read_b128 v[110:113], v94 offset:4096
	s_waitcnt lgkmcnt(1)
	v_pk_mul_f32 v[94:95], v[96:97], v[108:109]
	v_pk_mul_f32 v[114:115], v[100:101], v[106:107]
	v_pk_mul_f32 v[108:109], v[38:39], v[108:109]
	v_pk_mul_f32 v[106:107], v[36:37], v[106:107]
	s_waitcnt lgkmcnt(0)
	v_pk_fma_f32 v[38:39], v[38:39], v[112:113], v[94:95] neg_lo:[0,0,1] neg_hi:[0,0,1]
	v_pk_fma_f32 v[36:37], v[36:37], v[110:111], v[114:115] neg_lo:[0,0,1] neg_hi:[0,0,1]
	v_pk_fma_f32 v[96:97], v[96:97], v[112:113], v[108:109]
	v_pk_fma_f32 v[100:101], v[100:101], v[110:111], v[106:107]
; __device__ __forceinline__ unsigned pk2(float lo, float hi) { f32x2_t v = {lo, hi}; bf16x2_t b = __builtin_convertvector(v, bf16x2_t); return __builtin_bit_cast(unsigned, b); }
; __device__ __forceinline__ float shx(float v, int m, int lane) { return __int_as_float(__builtin_amdgcn_ds_bpermute((lane ^ m) << 2, __float_as_int(v))); }
;     __device__ __forceinline__ void operator()(const pg8::i32x4 (&acc)[2][2][4][2], const Unit& u, int wr, int wc, int fr, int fq) const {
;     ...
; #pragma unroll
;             for (int ai = 0; ai < 2; ++ai)
; #pragma unroll
;                 for (int m = 0; m < 4; ++m) {
;                     const int row = u.pm * 256 + ai * 128 + wr * 64 + m * 16 + fr;
;                     float ss = 0.f; const float sa = sah[row]; f32x4 xf[2][2];
; #pragma unroll
;                     for (int bj = 0; bj < 2; ++bj)
; #pragma unroll
;                         for (int n = 0; n < 2; ++n) { f32x4 x;
; #pragma unroll
;                             for (int i = 0; i < 4; ++i) x[i] = (float)acc[ai][bj][m][n][i] * (sa * swv[bj][n][i]);
;                             xf[bj][n] = x; ss += x[0] * x[0] + x[1] * x[1] + x[2] * x[2] + x[3] * x[3]; }
;                     { const int ln = fq * 16 + fr; ss += shx(ss, 16, ln); ss += shx(ss, 32, ln); }
;                     const float rstd = rsqrtf(ss * (1.f / 64.f) + EPS);
;                     const bool lat = row < NL; const int tok = row & 2047;
; #pragma unroll
;                     for (int bj = 0; bj < 2; ++bj) {
;                         f32x4 x1 = xf[bj][0] * rstd * w[bj][0], x2 = xf[bj][1] * rstd * w[bj][1];
;                         if (lat) { const int pos = bj ? (tok & 63) : (tok >> 6); const f32x4 c = *(const f32x4*)(ropec + pos * 16 + 4 * fq), s = *(const f32x4*)(ropes + pos * 16 + 4 * fq);
;                             const f32x4 o1 = x1 * c - x2 * s, o2 = x1 * s + x2 * c; x1 = o1; x2 = o2; }
;                         x1 = x1 * osc; x2 = x2 * osc;
;                         bf16_t* p = base + (size_t)row * 512 + 64 * hg + 32 * bj + 4 * fq;
;                         *(u32x2*)p = (u32x2){pk2(x1[0], x1[1]), pk2(x1[2], x1[3])};
;                         *(u32x2*)(p + 16) = (u32x2){pk2(x2[0], x2[1]), pk2(x2[2], x2[3])};
;                     }
.LBB0_306:
	s_or_b64 exec, exec, s[2:3]
	v_lshlrev_b64 v[94:95], 10, v[102:103]
	v_pk_mul_f32 v[38:39], v[104:105], v[38:39]
	v_pk_mul_f32 v[36:37], v[118:119], v[36:37]
	v_lshl_add_u64 v[94:95], v[128:129], 0, v[94:95]
	v_pk_mul_f32 v[96:97], v[104:105], v[96:97]
	v_pk_mul_f32 v[100:101], v[118:119], v[100:101]
	v_cvt_pk_bf16_f32 v36, v36, v37
	v_cvt_pk_bf16_f32 v37, v38, v39
	v_mov_b32_e32 v99, v98
	global_store_dwordx2 v[94:95], v[36:37], off
	v_cvt_pk_bf16_f32 v36, v100, v101
	v_cvt_pk_bf16_f32 v37, v96, v97
	global_store_dwordx2 v[94:95], v[36:37], off offset:32
	v_pk_mul_f32 v[36:37], v[92:93], v[98:99]
	v_mov_b32_e32 v92, v98
	v_mov_b32_e32 v93, v98
	v_pk_mul_f32 v[38:39], v[90:91], v[92:93]
	v_pk_mul_f32 v[88:89], v[88:89], v[98:99]
	v_pk_mul_f32 v[86:87], v[86:87], v[92:93]
	v_pk_mul_f32 v[38:39], v[26:27], v[38:39]
	v_pk_mul_f32 v[36:37], v[24:25], v[36:37]
	v_pk_mul_f32 v[86:87], v[22:23], v[86:87]
	v_pk_mul_f32 v[90:91], v[20:21], v[88:89]
	s_and_saveexec_b64 s[2:3], vcc
	s_cbranch_execz .LBB0_308
	ds_read_b128 v[96:99], v226
	ds_read_b128 v[104:107], v226 offset:4096
	s_waitcnt lgkmcnt(1)
	v_pk_mul_f32 v[88:89], v[86:87], v[98:99]
	v_pk_mul_f32 v[92:93], v[90:91], v[96:97]
	v_pk_mul_f32 v[98:99], v[38:39], v[98:99]
	v_pk_mul_f32 v[96:97], v[36:37], v[96:97]
	s_waitcnt lgkmcnt(0)
	v_pk_fma_f32 v[38:39], v[38:39], v[106:107], v[88:89] neg_lo:[0,0,1] neg_hi:[0,0,1]
	v_pk_fma_f32 v[36:37], v[36:37], v[104:105], v[92:93] neg_lo:[0,0,1] neg_hi:[0,0,1]
	v_pk_fma_f32 v[86:87], v[86:87], v[106:107], v[98:99]
	v_pk_fma_f32 v[90:91], v[90:91], v[104:105], v[96:97]
.LBB0_308:
	s_or_b64 exec, exec, s[2:3]
	v_mov_b32_e32 v88, v118
	v_mov_b32_e32 v89, v118
	v_pk_mul_f32 v[38:39], v[88:89], v[38:39]
	v_pk_mul_f32 v[36:37], v[118:119], v[36:37]
	v_pk_mul_f32 v[86:87], v[88:89], v[86:87]
	v_cvt_pk_bf16_f32 v36, v36, v37
	v_cvt_pk_bf16_f32 v37, v38, v39
	v_pk_mul_f32 v[90:91], v[118:119], v[90:91]
	global_store_dwordx2 v[94:95], v[36:37], off offset:64
	v_cvt_pk_bf16_f32 v37, v86, v87
	v_or_b32_e32 v86, 16, v102
	v_cvt_pk_bf16_f32 v36, v90, v91
	v_ashrrev_i32_e32 v87, 31, v86
	global_store_dwordx2 v[94:95], v[36:37], off offset:96
	v_lshl_add_u64 v[36:37], v[86:87], 2, s[44:45]
	v_mov_b32_e32 v0, v221
	s_mov_b32 s2, 0x8000
	v_pk_mul_f32 v[38:39], v[18:19], v[0:1] op_sel_hi:[1,0]
	v_pk_mul_f32 v[36:37], v[16:17], v[0:1] op_sel_hi:[1,0]
	v_pk_mul_f32 v[38:39], v[38:39], v[82:83]
	v_pk_mul_f32 v[82:83], v[12:13], v[0:1] op_sel_hi:[1,0]
	v_pk_mul_f32 v[36:37], v[36:37], v[84:85]
	v_pk_mul_f32 v[80:81], v[82:83], v[80:81]
	v_pk_mul_f32 v[82:83], v[14:15], v[0:1] op_sel_hi:[1,0]
	v_mov_b32_e32 v84, v37
	v_mov_b32_e32 v85, v81
	v_pk_mul_f32 v[78:79], v[82:83], v[78:79]
	v_mov_b32_e32 v82, v36
	v_mov_b32_e32 v83, v80
	v_pk_mul_f32 v[84:85], v[84:85], v[84:85]
	s_nop 0
	v_pk_fma_f32 v[82:83], v[82:83], v[82:83], v[84:85]
	v_mov_b32_e32 v84, v38
	v_mov_b32_e32 v85, v78
	v_pk_fma_f32 v[82:83], v[84:85], v[84:85], v[82:83]
	v_mov_b32_e32 v84, v39
	v_mov_b32_e32 v85, v79
	v_pk_fma_f32 v[82:83], v[84:85], v[84:85], v[82:83]
	v_pk_mul_f32 v[84:85], v[8:9], v[0:1] op_sel_hi:[1,0]
	s_nop 0
	v_pk_mul_f32 v[76:77], v[84:85], v[76:77]
	v_pk_mul_f32 v[84:85], v[10:11], v[0:1] op_sel_hi:[1,0]
	v_mov_b32_e32 v91, v77
	v_pk_mul_f32 v[74:75], v[84:85], v[74:75]
	v_pk_mul_f32 v[84:85], v[4:5], v[0:1] op_sel_hi:[1,0]
	s_nop 0
	v_pk_mul_f32 v[72:73], v[84:85], v[72:73]
	v_pk_mul_f32 v[84:85], v[6:7], v[0:1] op_sel_hi:[1,0]
	v_mov_b32_e32 v90, v73
	v_pk_mul_f32 v[70:71], v[84:85], v[70:71]
	v_mov_b32_e32 v84, v72
	v_mov_b32_e32 v85, v76
	v_pk_mul_f32 v[90:91], v[90:91], v[90:91]
	v_add_f32_e32 v0, v82, v83
	v_pk_fma_f32 v[84:85], v[84:85], v[84:85], v[90:91]
	v_mov_b32_e32 v90, v70
	v_mov_b32_e32 v91, v74
	v_pk_fma_f32 v[84:85], v[90:91], v[90:91], v[84:85]
	v_mov_b32_e32 v90, v71
	v_mov_b32_e32 v91, v75
	v_pk_fma_f32 v[84:85], v[90:91], v[90:91], v[84:85]
	s_nop 0
	v_add_f32_e32 v0, v85, v0
	v_add_f32_e32 v0, v84, v0
	ds_bpermute_b32 v3, v204, v0
	s_waitcnt lgkmcnt(0)
	v_add_f32_e32 v0, v0, v3
	ds_bpermute_b32 v3, v205, v0
	s_waitcnt lgkmcnt(0)
	v_add_f32_e32 v0, v0, v3
	v_fmamk_f32 v0, v0, 0x3c800000, v246
	v_cmp_gt_f32_e32 vcc, s22, v0
	v_mul_f32_e32 v3, 0x4b800000, v0
	s_nop 0
	v_cndmask_b32_e32 v0, v0, v3, vcc
	v_rsq_f32_e32 v0, v0
	s_nop 0
	v_mul_f32_e32 v3, 0x45800000, v0
	v_cndmask_b32_e32 v82, v0, v3, vcc
	v_pk_mul_f32 v[36:37], v[36:37], v[82:83] op_sel_hi:[1,0]
	v_pk_mul_f32 v[38:39], v[38:39], v[82:83] op_sel_hi:[1,0]
	v_pk_mul_f32 v[84:85], v[80:81], v[82:83] op_sel_hi:[1,0]
	v_pk_mul_f32 v[78:79], v[78:79], v[82:83] op_sel_hi:[1,0]
	v_cmp_gt_i32_e32 vcc, s2, v86
	v_pk_mul_f32 v[38:39], v[34:35], v[38:39]
	v_pk_mul_f32 v[36:37], v[32:33], v[36:37]
	v_pk_mul_f32 v[80:81], v[30:31], v[78:79]
	v_pk_mul_f32 v[84:85], v[28:29], v[84:85]
	s_and_saveexec_b64 s[2:3], vcc
	s_cbranch_execz .LBB0_310
	s_and_b32 s30, s4, 0x7c0
	v_add_u32_e32 v78, s30, v225
	ds_read_b128 v[90:93], v78
	v_add_u32_e32 v78, s30, v225
	ds_read_b128 v[94:97], v78 offset:4096
	s_waitcnt lgkmcnt(1)
	v_pk_mul_f32 v[78:79], v[80:81], v[92:93]
	v_pk_mul_f32 v[98:99], v[84:85], v[90:91]
	v_pk_mul_f32 v[92:93], v[38:39], v[92:93]
	v_pk_mul_f32 v[90:91], v[36:37], v[90:91]
	s_waitcnt lgkmcnt(0)
	v_pk_fma_f32 v[38:39], v[38:39], v[96:97], v[78:79] neg_lo:[0,0,1] neg_hi:[0,0,1]
	v_pk_fma_f32 v[36:37], v[36:37], v[94:95], v[98:99] neg_lo:[0,0,1] neg_hi:[0,0,1]
	v_pk_fma_f32 v[80:81], v[80:81], v[96:97], v[92:93]
	v_pk_fma_f32 v[84:85], v[84:85], v[94:95], v[90:91]
; __device__ __forceinline__ unsigned pk2(float lo, float hi) { f32x2_t v = {lo, hi}; bf16x2_t b = __builtin_convertvector(v, bf16x2_t); return __builtin_bit_cast(unsigned, b); }
; __device__ __forceinline__ float shx(float v, int m, int lane) { return __int_as_float(__builtin_amdgcn_ds_bpermute((lane ^ m) << 2, __float_as_int(v))); }
;     __device__ __forceinline__ void operator()(const pg8::i32x4 (&acc)[2][2][4][2], const Unit& u, int wr, int wc, int fr, int fq) const {
;     ...
; #pragma unroll
;             for (int ai = 0; ai < 2; ++ai)
; #pragma unroll
;                 for (int m = 0; m < 4; ++m) {
;                     const int row = u.pm * 256 + ai * 128 + wr * 64 + m * 16 + fr;
;                     float ss = 0.f; const float sa = sah[row]; f32x4 xf[2][2];
; #pragma unroll
;                     for (int bj = 0; bj < 2; ++bj)
; #pragma unroll
;                         for (int n = 0; n < 2; ++n) { f32x4 x;
; #pragma unroll
;                             for (int i = 0; i < 4; ++i) x[i] = (float)acc[ai][bj][m][n][i] * (sa * swv[bj][n][i]);
;                             xf[bj][n] = x; ss += x[0] * x[0] + x[1] * x[1] + x[2] * x[2] + x[3] * x[3]; }
;                     { const int ln = fq * 16 + fr; ss += shx(ss, 16, ln); ss += shx(ss, 32, ln); }
;                     const float rstd = rsqrtf(ss * (1.f / 64.f) + EPS);
;                     const bool lat = row < NL; const int tok = row & 2047;
; #pragma unroll
;                     for (int bj = 0; bj < 2; ++bj) {
;                         f32x4 x1 = xf[bj][0] * rstd * w[bj][0], x2 = xf[bj][1] * rstd * w[bj][1];
;                         if (lat) { const int pos = bj ? (tok & 63) : (tok >> 6); const f32x4 c = *(const f32x4*)(ropec + pos * 16 + 4 * fq), s = *(const f32x4*)(ropes + pos * 16 + 4 * fq);
;                             const f32x4 o1 = x1 * c - x2 * s, o2 = x1 * s + x2 * c; x1 = o1; x2 = o2; }
;                         x1 = x1 * osc; x2 = x2 * osc;
;                         bf16_t* p = base + (size_t)row * 512 + 64 * hg + 32 * bj + 4 * fq;
;                         *(u32x2*)p = (u32x2){pk2(x1[0], x1[1]), pk2(x1[2], x1[3])};
;                         *(u32x2*)(p + 16) = (u32x2){pk2(x2[0], x2[1]), pk2(x2[2], x2[3])};
;                     }
.LBB0_310:
	s_or_b64 exec, exec, s[2:3]
	v_lshlrev_b64 v[78:79], 10, v[86:87]
	v_pk_mul_f32 v[38:39], v[88:89], v[38:39]
	v_pk_mul_f32 v[36:37], v[118:119], v[36:37]
	v_lshl_add_u64 v[78:79], v[128:129], 0, v[78:79]
	v_pk_mul_f32 v[80:81], v[88:89], v[80:81]
	v_pk_mul_f32 v[84:85], v[118:119], v[84:85]
	v_cvt_pk_bf16_f32 v36, v36, v37
	v_cvt_pk_bf16_f32 v37, v38, v39
	v_mov_b32_e32 v83, v82
	global_store_dwordx2 v[78:79], v[36:37], off
	v_cvt_pk_bf16_f32 v36, v84, v85
	v_cvt_pk_bf16_f32 v37, v80, v81
	global_store_dwordx2 v[78:79], v[36:37], off offset:32
	v_pk_mul_f32 v[36:37], v[76:77], v[82:83]
	v_mov_b32_e32 v76, v82
	v_mov_b32_e32 v77, v82
	v_pk_mul_f32 v[38:39], v[74:75], v[76:77]
	v_pk_mul_f32 v[72:73], v[72:73], v[82:83]
	v_pk_mul_f32 v[70:71], v[70:71], v[76:77]
	v_pk_mul_f32 v[38:39], v[26:27], v[38:39]
	v_pk_mul_f32 v[36:37], v[24:25], v[36:37]
	v_pk_mul_f32 v[70:71], v[22:23], v[70:71]
	v_pk_mul_f32 v[74:75], v[20:21], v[72:73]
	s_and_saveexec_b64 s[2:3], vcc
	s_cbranch_execz .LBB0_312
	v_lshlrev_b32_e32 v0, 6, v86
	v_and_b32_e32 v72, 0x7c0, v0
	v_mov_b32_e32 v73, v145
	v_add_u32_e32 v76, v72, v225
	ds_read_b128 v[80:83], v76
	v_add_u32_e32 v72, v72, v225
	ds_read_b128 v[84:87], v72 offset:4096
	s_waitcnt lgkmcnt(1)
	v_pk_mul_f32 v[72:73], v[70:71], v[82:83]
	v_pk_mul_f32 v[76:77], v[74:75], v[80:81]
	v_pk_mul_f32 v[82:83], v[38:39], v[82:83]
	v_pk_mul_f32 v[80:81], v[36:37], v[80:81]
	s_waitcnt lgkmcnt(0)
	v_pk_fma_f32 v[38:39], v[38:39], v[86:87], v[72:73] neg_lo:[0,0,1] neg_hi:[0,0,1]
	v_pk_fma_f32 v[36:37], v[36:37], v[84:85], v[76:77] neg_lo:[0,0,1] neg_hi:[0,0,1]
	v_pk_fma_f32 v[70:71], v[70:71], v[86:87], v[82:83]
	v_pk_fma_f32 v[74:75], v[74:75], v[84:85], v[80:81]
.LBB0_312:
	s_or_b64 exec, exec, s[2:3]
	v_mov_b32_e32 v72, v118
	v_mov_b32_e32 v73, v118
	v_pk_mul_f32 v[38:39], v[72:73], v[38:39]
	v_pk_mul_f32 v[36:37], v[118:119], v[36:37]
	v_pk_mul_f32 v[70:71], v[72:73], v[70:71]
	v_cvt_pk_bf16_f32 v36, v36, v37
	v_cvt_pk_bf16_f32 v37, v38, v39
	v_pk_mul_f32 v[74:75], v[118:119], v[74:75]
	global_store_dwordx2 v[78:79], v[36:37], off offset:64
	v_cvt_pk_bf16_f32 v37, v70, v71
	v_or_b32_e32 v70, 32, v102
	v_cvt_pk_bf16_f32 v36, v74, v75
	v_ashrrev_i32_e32 v71, 31, v70
	global_store_dwordx2 v[78:79], v[36:37], off offset:96
	v_lshl_add_u64 v[36:37], v[70:71], 2, s[44:45]
	v_mov_b32_e32 v0, v222
	s_mov_b32 s2, 0x8000
	v_pk_mul_f32 v[38:39], v[18:19], v[0:1] op_sel_hi:[1,0]
	v_pk_mul_f32 v[36:37], v[16:17], v[0:1] op_sel_hi:[1,0]
	v_pk_mul_f32 v[38:39], v[38:39], v[66:67]
	v_pk_mul_f32 v[66:67], v[12:13], v[0:1] op_sel_hi:[1,0]
	v_pk_mul_f32 v[36:37], v[36:37], v[68:69]
	v_pk_mul_f32 v[64:65], v[66:67], v[64:65]
	v_pk_mul_f32 v[66:67], v[14:15], v[0:1] op_sel_hi:[1,0]
	v_mov_b32_e32 v68, v37
	v_mov_b32_e32 v69, v65
	v_pk_mul_f32 v[62:63], v[66:67], v[62:63]
	v_mov_b32_e32 v66, v36
	v_mov_b32_e32 v67, v64
	v_pk_mul_f32 v[68:69], v[68:69], v[68:69]
	s_nop 0
	v_pk_fma_f32 v[66:67], v[66:67], v[66:67], v[68:69]
	v_mov_b32_e32 v68, v38
	v_mov_b32_e32 v69, v62
	v_pk_fma_f32 v[66:67], v[68:69], v[68:69], v[66:67]
	v_mov_b32_e32 v68, v39
	v_mov_b32_e32 v69, v63
	v_pk_fma_f32 v[66:67], v[68:69], v[68:69], v[66:67]
	v_pk_mul_f32 v[68:69], v[8:9], v[0:1] op_sel_hi:[1,0]
	s_nop 0
	v_pk_mul_f32 v[60:61], v[68:69], v[60:61]
	v_pk_mul_f32 v[68:69], v[10:11], v[0:1] op_sel_hi:[1,0]
	v_mov_b32_e32 v75, v61
	v_pk_mul_f32 v[58:59], v[68:69], v[58:59]
	v_pk_mul_f32 v[68:69], v[4:5], v[0:1] op_sel_hi:[1,0]
	s_nop 0
	v_pk_mul_f32 v[56:57], v[68:69], v[56:57]
	v_pk_mul_f32 v[68:69], v[6:7], v[0:1] op_sel_hi:[1,0]
	v_mov_b32_e32 v74, v57
	v_pk_mul_f32 v[54:55], v[68:69], v[54:55]
	v_mov_b32_e32 v68, v56
	v_mov_b32_e32 v69, v60
	v_pk_mul_f32 v[74:75], v[74:75], v[74:75]
	v_add_f32_e32 v0, v66, v67
	v_pk_fma_f32 v[68:69], v[68:69], v[68:69], v[74:75]
	v_mov_b32_e32 v74, v54
	v_mov_b32_e32 v75, v58
	v_pk_fma_f32 v[68:69], v[74:75], v[74:75], v[68:69]
	v_mov_b32_e32 v74, v55
	v_mov_b32_e32 v75, v59
	v_pk_fma_f32 v[68:69], v[74:75], v[74:75], v[68:69]
	s_nop 0
	v_add_f32_e32 v0, v69, v0
	v_add_f32_e32 v0, v68, v0
	ds_bpermute_b32 v3, v204, v0
	s_waitcnt lgkmcnt(0)
	v_add_f32_e32 v0, v0, v3
	ds_bpermute_b32 v3, v205, v0
	s_waitcnt lgkmcnt(0)
	v_add_f32_e32 v0, v0, v3
	v_fmamk_f32 v0, v0, 0x3c800000, v246
	v_cmp_gt_f32_e32 vcc, s22, v0
	v_mul_f32_e32 v3, 0x4b800000, v0
	s_nop 0
	v_cndmask_b32_e32 v0, v0, v3, vcc
	v_rsq_f32_e32 v0, v0
	s_nop 0
	v_mul_f32_e32 v3, 0x45800000, v0
	v_cndmask_b32_e32 v66, v0, v3, vcc
	v_pk_mul_f32 v[36:37], v[36:37], v[66:67] op_sel_hi:[1,0]
	v_pk_mul_f32 v[38:39], v[38:39], v[66:67] op_sel_hi:[1,0]
	v_pk_mul_f32 v[68:69], v[64:65], v[66:67] op_sel_hi:[1,0]
	v_pk_mul_f32 v[62:63], v[62:63], v[66:67] op_sel_hi:[1,0]
	v_cmp_gt_i32_e32 vcc, s2, v70
	v_pk_mul_f32 v[38:39], v[34:35], v[38:39]
	v_pk_mul_f32 v[36:37], v[32:33], v[36:37]
	v_pk_mul_f32 v[64:65], v[30:31], v[62:63]
	v_pk_mul_f32 v[68:69], v[28:29], v[68:69]
	s_and_saveexec_b64 s[2:3], vcc
	s_cbranch_execz .LBB0_314
	s_and_b32 s30, s4, 0x7c0
	v_add_u32_e32 v62, s30, v225
	ds_read_b128 v[74:77], v62
	v_add_u32_e32 v62, s30, v225
	ds_read_b128 v[78:81], v62 offset:4096
	s_waitcnt lgkmcnt(1)
	v_pk_mul_f32 v[62:63], v[64:65], v[76:77]
	v_pk_mul_f32 v[82:83], v[68:69], v[74:75]
	v_pk_mul_f32 v[76:77], v[38:39], v[76:77]
	v_pk_mul_f32 v[74:75], v[36:37], v[74:75]
	s_waitcnt lgkmcnt(0)
	v_pk_fma_f32 v[38:39], v[38:39], v[80:81], v[62:63] neg_lo:[0,0,1] neg_hi:[0,0,1]
	v_pk_fma_f32 v[36:37], v[36:37], v[78:79], v[82:83] neg_lo:[0,0,1] neg_hi:[0,0,1]
	v_pk_fma_f32 v[64:65], v[64:65], v[80:81], v[76:77]
	v_pk_fma_f32 v[68:69], v[68:69], v[78:79], v[74:75]
; __device__ __forceinline__ unsigned pk2(float lo, float hi) { f32x2_t v = {lo, hi}; bf16x2_t b = __builtin_convertvector(v, bf16x2_t); return __builtin_bit_cast(unsigned, b); }
;     __device__ __forceinline__ void operator()(const pg8::i32x4 (&acc)[2][2][4][2], const Unit& u, int wr, int wc, int fr, int fq) const {
;     ...
;                     for (int bj = 0; bj < 2; ++bj) {
;                         f32x4 x1 = xf[bj][0] * rstd * w[bj][0], x2 = xf[bj][1] * rstd * w[bj][1];
;                         if (lat) { const int pos = bj ? (tok & 63) : (tok >> 6); const f32x4 c = *(const f32x4*)(ropec + pos * 16 + 4 * fq), s = *(const f32x4*)(ropes + pos * 16 + 4 * fq);
;                             const f32x4 o1 = x1 * c - x2 * s, o2 = x1 * s + x2 * c; x1 = o1; x2 = o2; }
;                         x1 = x1 * osc; x2 = x2 * osc;
;                         bf16_t* p = base + (size_t)row * 512 + 64 * hg + 32 * bj + 4 * fq;
;                         *(u32x2*)p = (u32x2){pk2(x1[0], x1[1]), pk2(x1[2], x1[3])};
;                         *(u32x2*)(p + 16) = (u32x2){pk2(x2[0], x2[1]), pk2(x2[2], x2[3])};
;                     }
.LBB0_314:
	s_or_b64 exec, exec, s[2:3]
	v_lshlrev_b64 v[62:63], 10, v[70:71]
	v_pk_mul_f32 v[38:39], v[72:73], v[38:39]
	v_pk_mul_f32 v[36:37], v[118:119], v[36:37]
	v_lshl_add_u64 v[62:63], v[128:129], 0, v[62:63]
	v_pk_mul_f32 v[64:65], v[72:73], v[64:65]
	v_pk_mul_f32 v[68:69], v[118:119], v[68:69]
	v_cvt_pk_bf16_f32 v36, v36, v37
	v_cvt_pk_bf16_f32 v37, v38, v39
	v_mov_b32_e32 v67, v66
	global_store_dwordx2 v[62:63], v[36:37], off
	v_cvt_pk_bf16_f32 v36, v68, v69
	v_cvt_pk_bf16_f32 v37, v64, v65
	global_store_dwordx2 v[62:63], v[36:37], off offset:32
	v_pk_mul_f32 v[36:37], v[60:61], v[66:67]
	v_mov_b32_e32 v60, v66
	v_mov_b32_e32 v61, v66
	v_pk_mul_f32 v[38:39], v[58:59], v[60:61]
	v_pk_mul_f32 v[58:59], v[56:57], v[66:67]
	v_pk_mul_f32 v[54:55], v[54:55], v[60:61]
	v_pk_mul_f32 v[38:39], v[26:27], v[38:39]
	v_pk_mul_f32 v[36:37], v[24:25], v[36:37]
	v_pk_mul_f32 v[56:57], v[22:23], v[54:55]
	v_pk_mul_f32 v[58:59], v[20:21], v[58:59]
	s_and_saveexec_b64 s[2:3], vcc
	s_cbranch_execz .LBB0_316
	v_lshlrev_b32_e32 v0, 6, v70
	v_and_b32_e32 v54, 0xbc0, v0
	v_mov_b32_e32 v55, v145
	v_add_u32_e32 v60, v54, v225
	ds_read_b128 v[64:67], v60
	v_add_u32_e32 v54, v54, v225
	ds_read_b128 v[68:71], v54 offset:4096
	s_waitcnt lgkmcnt(1)
	v_pk_mul_f32 v[54:55], v[56:57], v[66:67]
	v_pk_mul_f32 v[60:61], v[58:59], v[64:65]
	v_pk_mul_f32 v[66:67], v[38:39], v[66:67]
	v_pk_mul_f32 v[64:65], v[36:37], v[64:65]
	s_waitcnt lgkmcnt(0)
	v_pk_fma_f32 v[38:39], v[38:39], v[70:71], v[54:55] neg_lo:[0,0,1] neg_hi:[0,0,1]
	v_pk_fma_f32 v[36:37], v[36:37], v[68:69], v[60:61] neg_lo:[0,0,1] neg_hi:[0,0,1]
	v_pk_fma_f32 v[56:57], v[56:57], v[70:71], v[66:67]
	v_pk_fma_f32 v[58:59], v[58:59], v[68:69], v[64:65]
; __device__ __forceinline__ unsigned pk2(float lo, float hi) { f32x2_t v = {lo, hi}; bf16x2_t b = __builtin_convertvector(v, bf16x2_t); return __builtin_bit_cast(unsigned, b); }
; __device__ __forceinline__ float shx(float v, int m, int lane) { return __int_as_float(__builtin_amdgcn_ds_bpermute((lane ^ m) << 2, __float_as_int(v))); }
;     __device__ __forceinline__ void operator()(const pg8::i32x4 (&acc)[2][2][4][2], const Unit& u, int wr, int wc, int fr, int fq) const {
;     ...
; #pragma unroll
;             for (int ai = 0; ai < 2; ++ai)
; #pragma unroll
;                 for (int m = 0; m < 4; ++m) {
;                     const int row = u.pm * 256 + ai * 128 + wr * 64 + m * 16 + fr;
;                     float ss = 0.f; const float sa = sah[row]; f32x4 xf[2][2];
; #pragma unroll
;                     for (int bj = 0; bj < 2; ++bj)
; #pragma unroll
;                         for (int n = 0; n < 2; ++n) { f32x4 x;
; #pragma unroll
;                             for (int i = 0; i < 4; ++i) x[i] = (float)acc[ai][bj][m][n][i] * (sa * swv[bj][n][i]);
;                             xf[bj][n] = x; ss += x[0] * x[0] + x[1] * x[1] + x[2] * x[2] + x[3] * x[3]; }
;                     { const int ln = fq * 16 + fr; ss += shx(ss, 16, ln); ss += shx(ss, 32, ln); }
;                     const float rstd = rsqrtf(ss * (1.f / 64.f) + EPS);
;                     const bool lat = row < NL; const int tok = row & 2047;
; #pragma unroll
;                     for (int bj = 0; bj < 2; ++bj) {
;                         f32x4 x1 = xf[bj][0] * rstd * w[bj][0], x2 = xf[bj][1] * rstd * w[bj][1];
;                         if (lat) { const int pos = bj ? (tok & 63) : (tok >> 6); const f32x4 c = *(const f32x4*)(ropec + pos * 16 + 4 * fq), s = *(const f32x4*)(ropes + pos * 16 + 4 * fq);
;                             const f32x4 o1 = x1 * c - x2 * s, o2 = x1 * s + x2 * c; x1 = o1; x2 = o2; }
;                         x1 = x1 * osc; x2 = x2 * osc;
;                         bf16_t* p = base + (size_t)row * 512 + 64 * hg + 32 * bj + 4 * fq;
;                         *(u32x2*)p = (u32x2){pk2(x1[0], x1[1]), pk2(x1[2], x1[3])};
;                         *(u32x2*)(p + 16) = (u32x2){pk2(x2[0], x2[1]), pk2(x2[2], x2[3])};
;                     }
.LBB0_316:
	s_or_b64 exec, exec, s[2:3]
	v_mov_b32_e32 v54, v118
	v_mov_b32_e32 v55, v118
	v_pk_mul_f32 v[38:39], v[54:55], v[38:39]
	v_pk_mul_f32 v[36:37], v[118:119], v[36:37]
	v_pk_mul_f32 v[56:57], v[54:55], v[56:57]
	v_pk_mul_f32 v[58:59], v[118:119], v[58:59]
	v_cvt_pk_bf16_f32 v36, v36, v37
	v_cvt_pk_bf16_f32 v37, v38, v39
	global_store_dwordx2 v[62:63], v[36:37], off offset:64
	v_cvt_pk_bf16_f32 v36, v58, v59
	v_cvt_pk_bf16_f32 v37, v56, v57
	global_store_dwordx2 v[62:63], v[36:37], off offset:96
	v_or_b32_e32 v36, 48, v102
	v_ashrrev_i32_e32 v37, 31, v36
	v_lshl_add_u64 v[38:39], v[36:37], 2, s[44:45]
	v_mov_b32_e32 v56, v223
	v_cvt_f32_i32_e32 v0, v2
	s_mov_b32 s2, 0x8000
	v_pk_mul_f32 v[16:17], v[16:17], v[56:57] op_sel_hi:[1,0]
	s_nop 0
	v_pk_mul_f32 v[38:39], v[16:17], v[50:51]
	v_pk_mul_f32 v[16:17], v[18:19], v[56:57] op_sel_hi:[1,0]
	v_pk_mul_f32 v[12:13], v[12:13], v[56:57] op_sel_hi:[1,0]
	v_pk_mul_f32 v[18:19], v[16:17], v[52:53]
	v_pk_mul_f32 v[16:17], v[12:13], v[46:47]
	v_pk_mul_f32 v[12:13], v[14:15], v[56:57] op_sel_hi:[1,0]
	v_mov_b32_e32 v46, v39
	v_mov_b32_e32 v47, v17
	v_pk_mul_f32 v[14:15], v[12:13], v[48:49]
	v_mov_b32_e32 v12, v38
	v_mov_b32_e32 v13, v16
	v_pk_mul_f32 v[46:47], v[46:47], v[46:47]
	v_pk_mul_f32 v[8:9], v[8:9], v[56:57] op_sel_hi:[1,0]
	v_pk_fma_f32 v[12:13], v[12:13], v[12:13], v[46:47]
	v_mov_b32_e32 v46, v18
	v_mov_b32_e32 v47, v14
	v_pk_fma_f32 v[12:13], v[46:47], v[46:47], v[12:13]
	v_mov_b32_e32 v46, v19
	v_mov_b32_e32 v47, v15
	v_pk_mul_f32 v[4:5], v[4:5], v[56:57] op_sel_hi:[1,0]
	v_pk_fma_f32 v[46:47], v[46:47], v[46:47], v[12:13]
	v_pk_mul_f32 v[12:13], v[8:9], v[42:43]
	v_pk_mul_f32 v[4:5], v[4:5], v[40:41]
	v_pk_mul_f32 v[2:3], v[6:7], v[56:57] op_sel_hi:[1,0]
	v_pk_mul_f32 v[8:9], v[10:11], v[56:57] op_sel_hi:[1,0]
	v_pk_mul_f32 v[6:7], v[2:3], v[0:1]
	v_mov_b32_e32 v2, v5
	v_mov_b32_e32 v3, v13
	v_pk_mul_f32 v[8:9], v[8:9], v[44:45]
	v_mov_b32_e32 v0, v4
	v_mov_b32_e32 v1, v12
	v_pk_mul_f32 v[2:3], v[2:3], v[2:3]
	s_nop 0
	v_pk_fma_f32 v[0:1], v[0:1], v[0:1], v[2:3]
	v_mov_b32_e32 v2, v6
	v_mov_b32_e32 v3, v8
	v_pk_fma_f32 v[0:1], v[2:3], v[2:3], v[0:1]
	v_mov_b32_e32 v2, v7
	v_mov_b32_e32 v3, v9
	v_pk_fma_f32 v[0:1], v[2:3], v[2:3], v[0:1]
	v_add_f32_e32 v2, v46, v47
	v_add_f32_e32 v1, v1, v2
	v_add_f32_e32 v0, v0, v1
	ds_bpermute_b32 v1, v204, v0
	s_waitcnt lgkmcnt(0)
	v_add_f32_e32 v0, v0, v1
	ds_bpermute_b32 v1, v205, v0
	s_waitcnt lgkmcnt(0)
	v_add_f32_e32 v0, v0, v1
	v_fmamk_f32 v0, v0, 0x3c800000, v246
	v_cmp_gt_f32_e32 vcc, s22, v0
	v_mul_f32_e32 v1, 0x4b800000, v0
	s_nop 0
	v_cndmask_b32_e32 v0, v0, v1, vcc
	v_rsq_f32_e32 v0, v0
	s_nop 0
	v_mul_f32_e32 v1, 0x45800000, v0
	v_cndmask_b32_e32 v10, v0, v1, vcc
	v_pk_mul_f32 v[0:1], v[38:39], v[10:11] op_sel_hi:[1,0]
	v_pk_mul_f32 v[2:3], v[18:19], v[10:11] op_sel_hi:[1,0]
	v_pk_mul_f32 v[18:19], v[16:17], v[10:11] op_sel_hi:[1,0]
	v_pk_mul_f32 v[14:15], v[14:15], v[10:11] op_sel_hi:[1,0]
	v_cmp_gt_i32_e32 vcc, s2, v36
	v_pk_mul_f32 v[2:3], v[34:35], v[2:3]
	v_pk_mul_f32 v[0:1], v[32:33], v[0:1]
	v_pk_mul_f32 v[16:17], v[30:31], v[14:15]
	v_pk_mul_f32 v[18:19], v[28:29], v[18:19]
	s_and_saveexec_b64 s[2:3], vcc
	s_cbranch_execz .LBB0_318
	s_and_b32 s30, s4, 0x7c0
	v_add_u32_e32 v14, s30, v225
	ds_read_b128 v[28:31], v14
	v_add_u32_e32 v14, s30, v225
	ds_read_b128 v[32:35], v14 offset:4096
	s_waitcnt lgkmcnt(1)
	v_pk_mul_f32 v[14:15], v[16:17], v[30:31]
	v_pk_mul_f32 v[38:39], v[18:19], v[28:29]
	v_pk_mul_f32 v[30:31], v[2:3], v[30:31]
	v_pk_mul_f32 v[28:29], v[0:1], v[28:29]
	s_waitcnt lgkmcnt(0)
	v_pk_fma_f32 v[2:3], v[2:3], v[34:35], v[14:15] neg_lo:[0,0,1] neg_hi:[0,0,1]
	v_pk_fma_f32 v[0:1], v[0:1], v[32:33], v[38:39] neg_lo:[0,0,1] neg_hi:[0,0,1]
	v_pk_fma_f32 v[16:17], v[16:17], v[34:35], v[30:31]
	v_pk_fma_f32 v[18:19], v[18:19], v[32:33], v[28:29]
.LBB0_318:
	s_or_b64 exec, exec, s[2:3]
	v_lshlrev_b64 v[14:15], 10, v[36:37]
	v_pk_mul_f32 v[2:3], v[54:55], v[2:3]
	v_pk_mul_f32 v[0:1], v[118:119], v[0:1]
	v_lshl_add_u64 v[14:15], v[128:129], 0, v[14:15]
	v_pk_mul_f32 v[16:17], v[54:55], v[16:17]
	v_pk_mul_f32 v[18:19], v[118:119], v[18:19]
	v_cvt_pk_bf16_f32 v0, v0, v1
	v_cvt_pk_bf16_f32 v1, v2, v3
	v_mov_b32_e32 v11, v10
	global_store_dwordx2 v[14:15], v[0:1], off
	v_cvt_pk_bf16_f32 v0, v18, v19
	v_cvt_pk_bf16_f32 v1, v16, v17
	global_store_dwordx2 v[14:15], v[0:1], off offset:32
	v_pk_mul_f32 v[0:1], v[12:13], v[10:11]
	v_mov_b32_e32 v12, v10
	v_mov_b32_e32 v13, v10
	v_pk_mul_f32 v[2:3], v[8:9], v[12:13]
	v_pk_mul_f32 v[8:9], v[4:5], v[10:11]
	v_pk_mul_f32 v[4:5], v[6:7], v[12:13]
	v_pk_mul_f32 v[2:3], v[26:27], v[2:3]
	v_pk_mul_f32 v[0:1], v[24:25], v[0:1]
	v_pk_mul_f32 v[4:5], v[22:23], v[4:5]
	v_pk_mul_f32 v[6:7], v[20:21], v[8:9]
	s_and_saveexec_b64 s[2:3], vcc
	s_cbranch_execz .LBB0_320
	v_lshlrev_b32_e32 v8, 6, v36
	v_and_b32_e32 v12, 0xfc0, v8
	v_mov_b32_e32 v13, v145
	v_add_u32_e32 v8, v12, v225
	ds_read_b128 v[8:11], v8
	v_add_u32_e32 v12, v12, v225
	ds_read_b128 v[16:19], v12 offset:4096
	s_waitcnt lgkmcnt(1)
	v_pk_mul_f32 v[12:13], v[4:5], v[10:11]
	v_pk_mul_f32 v[20:21], v[6:7], v[8:9]
	v_pk_mul_f32 v[10:11], v[2:3], v[10:11]
	v_pk_mul_f32 v[8:9], v[0:1], v[8:9]
	s_waitcnt lgkmcnt(0)
	v_pk_fma_f32 v[2:3], v[2:3], v[18:19], v[12:13] neg_lo:[0,0,1] neg_hi:[0,0,1]
	v_pk_fma_f32 v[0:1], v[0:1], v[16:17], v[20:21] neg_lo:[0,0,1] neg_hi:[0,0,1]
	v_pk_fma_f32 v[4:5], v[4:5], v[18:19], v[10:11]
	v_pk_fma_f32 v[6:7], v[6:7], v[16:17], v[8:9]

;     __device__ __forceinline__ void operator()(const pg8::i32x4 (&acc)[2][2][4][2], const Unit& u, int wr, int wc, int fr, int fq) const {
;         const int j = u.pn % 11;
;         f32x4 sg[2], su[2];
; #pragma unroll
;         for (int n = 0; n < 2; ++n) { sg[n] = *(const f32x4*)(sw + (size_t)u.pn * 256 + 32 * wc + 16 * n + 4 * fq); su[n] = *(const f32x4*)(sw + (size_t)u.pn * 256 + 128 + 32 * wc + 16 * n + 4 * fq); }
; #pragma unroll
;         for (int ai = 0; ai < 2; ++ai)
; #pragma unroll
;             for (int m = 0; m < 4; ++m) {
;                 const int row = u.pm * 256 + ai * 128 + wr * 64 + m * 16 + fr; const float sa = say[row];
;                 f32x4 h0, h1;
; #pragma unroll
;                 for (int i = 0; i < 4; ++i) { const float g0 = (float)acc[ai][0][m][0][i] * (sa * sg[0][i]), g1 = (float)acc[ai][0][m][1][i] * (sa * sg[1][i]);
;                     const float u0 = (float)acc[ai][1][m][0][i] * (sa * su[0][i]), u1 = (float)acc[ai][1][m][1][i] * (sa * su[1][i]);
;                     h0[i] = g0 * __builtin_amdgcn_rcpf(1.f + __expf(-g0)) * u0; h1[i] = g1 * __builtin_amdgcn_rcpf(1.f + __expf(-g1)) * u1; }
.LBB0_1191:
	s_ashr_i32 s3, s2, 31
	s_lshl_b64 s[4:5], s[2:3], 10
	s_mul_hi_i32 s3, s2, 0x2e8ba2e9
	v_lshl_add_u64 v[32:33], v[150:151], 0, s[4:5]
	s_lshr_b32 s4, s3, 31
	s_lshr_b32 s3, s3, 1
	s_add_i32 s3, s3, s4
	s_lshl_b32 s4, s62, 8
	v_add_u32_e32 v154, s4, v160
	v_lshlrev_b32_e32 v186, 2, v154
	global_load_dword v178, v186, s[52:53]
	global_load_dword v179, v186, s[52:53] offset:64
	global_load_dword v180, v186, s[52:53] offset:128
	global_load_dword v181, v186, s[52:53] offset:192
	global_load_dword v182, v186, s[52:53] offset:512
	global_load_dword v183, v186, s[52:53] offset:576
	global_load_dword v184, v186, s[52:53] offset:640
	global_load_dword v185, v186, s[52:53] offset:704
	v_ashrrev_i32_e32 v155, 31, v154
	v_lshl_add_u64 v[170:171], v[154:155], 2, s[52:53]
	global_load_dwordx4 v[44:47], v[32:33], off
	global_load_dwordx4 v[40:43], v[32:33], off offset:512
	global_load_dwordx4 v[36:39], v[32:33], off offset:64
	s_nop 0
	global_load_dwordx4 v[32:35], v[32:33], off offset:576
	v_cvt_f32_i32_e32 v141, v141
	v_cvt_f32_i32_e32 v140, v140
	v_cvt_f32_i32_e32 v137, v137
	v_cvt_f32_i32_e32 v136, v136
	v_cvt_f32_i32_e32 v133, v133
	v_cvt_f32_i32_e32 v132, v132
	v_cvt_f32_i32_e32 v129, v129
	v_cvt_f32_i32_e32 v128, v128
	v_cvt_f32_i32_e32 v139, v139
	v_cvt_f32_i32_e32 v138, v138
	v_cvt_f32_i32_e32 v131, v131
	v_cvt_f32_i32_e32 v130, v130
	s_mul_i32 s3, s3, 11
	s_sub_i32 s2, s2, s3
	s_lshl_b32 s2, s2, 7
	s_ashr_i32 s3, s2, 31
	s_movk_i32 s5, 0xb00
	s_lshl_b64 s[62:63], s[2:3], 1
	v_cvt_f32_i32_e32 v125, v125
	v_cvt_f32_i32_e32 v124, v124
	v_cvt_f32_i32_e32 v121, v121
	v_cvt_f32_i32_e32 v120, v120
	v_cvt_f32_i32_e32 v117, v117
	v_cvt_f32_i32_e32 v116, v116
	v_cvt_f32_i32_e32 v113, v113
	v_cvt_f32_i32_e32 v112, v112
	v_cvt_f32_i32_e32 v123, v123
	v_cvt_f32_i32_e32 v122, v122
	v_cvt_f32_i32_e32 v115, v115
	v_cvt_f32_i32_e32 v114, v114
	v_cvt_f32_i32_e32 v109, v109
	v_cvt_f32_i32_e32 v108, v108
	v_cvt_f32_i32_e32 v105, v105
	v_cvt_f32_i32_e32 v104, v104
	v_cvt_f32_i32_e32 v101, v101
	v_cvt_f32_i32_e32 v100, v100
	v_cvt_f32_i32_e32 v97, v97
	v_cvt_f32_i32_e32 v96, v96
	v_cvt_f32_i32_e32 v107, v107
	v_cvt_f32_i32_e32 v106, v106
	v_cvt_f32_i32_e32 v99, v99
	v_cvt_f32_i32_e32 v98, v98
	v_cvt_f32_i32_e32 v93, v93
	v_cvt_f32_i32_e32 v92, v92
	v_cvt_f32_i32_e32 v89, v89
	v_cvt_f32_i32_e32 v88, v88
	v_cvt_f32_i32_e32 v85, v85
	v_cvt_f32_i32_e32 v84, v84
	v_cvt_f32_i32_e32 v81, v81
	v_cvt_f32_i32_e32 v80, v80
	v_cvt_f32_i32_e32 v91, v91
	v_cvt_f32_i32_e32 v90, v90
	v_cvt_f32_i32_e32 v83, v83
	v_cvt_f32_i32_e32 v82, v82
	v_cvt_f32_i32_e32 v77, v77
	v_cvt_f32_i32_e32 v76, v76
	v_cvt_f32_i32_e32 v73, v73
	v_cvt_f32_i32_e32 v72, v72
	v_cvt_f32_i32_e32 v69, v69
	v_cvt_f32_i32_e32 v68, v68
	v_cvt_f32_i32_e32 v65, v65
	v_cvt_f32_i32_e32 v64, v64
	v_cvt_f32_i32_e32 v75, v75
	v_cvt_f32_i32_e32 v74, v74
	v_cvt_f32_i32_e32 v67, v67
	v_cvt_f32_i32_e32 v66, v66
	v_cvt_f32_i32_e32 v61, v61
	v_cvt_f32_i32_e32 v60, v60
	v_cvt_f32_i32_e32 v57, v57
	v_cvt_f32_i32_e32 v56, v56
	v_cvt_f32_i32_e32 v53, v53
	v_cvt_f32_i32_e32 v52, v52
	v_cvt_f32_i32_e32 v49, v49
	v_cvt_f32_i32_e32 v48, v48
	v_cvt_f32_i32_e32 v59, v59
	v_cvt_f32_i32_e32 v58, v58
	v_cvt_f32_i32_e32 v51, v51
	v_cvt_f32_i32_e32 v50, v50
	v_cvt_f32_i32_e32 v25, v25
	v_cvt_f32_i32_e32 v24, v24
	s_waitcnt vmcnt(0)
	v_mov_b32_e32 v144, v178
	v_pk_mul_f32 v[170:171], v[44:45], v[144:145] op_sel_hi:[1,0]
	v_pk_mul_f32 v[172:173], v[40:41], v[144:145] op_sel_hi:[1,0]
	v_pk_mul_f32 v[140:141], v[170:171], v[140:141]
	v_pk_mul_f32 v[136:137], v[172:173], v[136:137]
	v_mul_f32_e32 v153, 0xbfb8aa3b, v140
	v_exp_f32_e32 v153, v153
	v_cvt_f32_i32_e32 v29, v29
	v_cvt_f32_i32_e32 v28, v28
	v_cvt_f32_i32_e32 v17, v17
	v_add_f32_e32 v153, 1.0, v153
	v_rcp_f32_e32 v170, v153
	v_mul_f32_e32 v153, 0xbfb8aa3b, v141
	v_exp_f32_e32 v153, v153
	v_cvt_f32_i32_e32 v16, v16
	v_cvt_f32_i32_e32 v21, v21
	v_cvt_f32_i32_e32 v20, v20
	v_add_f32_e32 v153, 1.0, v153
	v_rcp_f32_e32 v171, v153
	v_mov_b32_e32 v153, v145
	v_cvt_f32_i32_e32 v23, v23
	v_cvt_f32_i32_e32 v22, v22
	v_pk_mul_f32 v[140:141], v[140:141], v[170:171]
	v_pk_mul_f32 v[170:171], v[32:33], v[144:145] op_sel_hi:[1,0]
	v_pk_mul_f32 v[136:137], v[136:137], v[140:141]
	v_pk_mul_f32 v[140:141], v[36:37], v[144:145] op_sel_hi:[1,0]
	v_pk_mul_f32 v[128:129], v[170:171], v[128:129]
	v_pk_mul_f32 v[132:133], v[140:141], v[132:133]
	v_cvt_f32_i32_e32 v9, v9
	v_mul_f32_e32 v140, 0xbfb8aa3b, v132
	v_mul_f32_e32 v141, 0xbfb8aa3b, v133
	v_exp_f32_e32 v140, v140
	v_exp_f32_e32 v141, v141
	v_cvt_f32_i32_e32 v8, v8
	v_cvt_f32_i32_e32 v13, v13
	v_add_f32_e32 v140, 1.0, v140
	v_add_f32_e32 v141, 1.0, v141
	v_rcp_f32_e32 v140, v140
	v_rcp_f32_e32 v141, v141
	v_cvt_f32_i32_e32 v12, v12
	v_cvt_f32_i32_e32 v1, v1
	v_cvt_f32_i32_e32 v0, v0
	v_pk_mul_f32 v[132:133], v[132:133], v[140:141]
	v_pk_mul_f32 v[140:141], v[46:47], v[144:145] op_sel_hi:[1,0]
	v_pk_mul_f32 v[132:133], v[128:129], v[132:133]
	v_cvt_f32_i32_e32 v129, v143
	v_cvt_f32_i32_e32 v128, v142
	v_pk_mul_f32 v[142:143], v[42:43], v[144:145] op_sel_hi:[1,0]
	v_cvt_f32_i32_e32 v5, v5
	v_pk_mul_f32 v[138:139], v[142:143], v[138:139]
	v_pk_mul_f32 v[128:129], v[140:141], v[128:129]
	v_cvt_f32_i32_e32 v4, v4
	v_mul_f32_e32 v140, 0xbfb8aa3b, v128
	v_mul_f32_e32 v141, 0xbfb8aa3b, v129
	v_exp_f32_e32 v140, v140
	v_exp_f32_e32 v141, v141
	v_cvt_f32_i32_e32 v7, v7
	v_cvt_f32_i32_e32 v6, v6
	v_add_f32_e32 v140, 1.0, v140
	v_add_f32_e32 v141, 1.0, v141
	v_rcp_f32_e32 v140, v140
	v_rcp_f32_e32 v141, v141
	s_and_b64 vcc, exec, s[38:39]
	v_pk_mul_f32 v[128:129], v[128:129], v[140:141]
	s_nop 0
	v_pk_mul_f32 v[138:139], v[138:139], v[128:129]
; __device__ __forceinline__ u32x4 pack8(f32x4 a, f32x4 b) { u32x4 w; w.x = pk2(a[0], a[1]); w.y = pk2(a[2], a[3]); w.z = pk2(b[0], b[1]); w.w = pk2(b[2], b[3]); return w; }
;     __device__ __forceinline__ void operator()(const pg8::i32x4 (&acc)[2][2][4][2], const Unit& u, int wr, int wc, int fr, int fq) const {
;     ...
;         for (int ai = 0; ai < 2; ++ai)
; #pragma unroll
;             for (int m = 0; m < 4; ++m) {
;                 const int row = u.pm * 256 + ai * 128 + wr * 64 + m * 16 + fr; const float sa = say[row];
;                 f32x4 h0, h1;
; #pragma unroll
;                 for (int i = 0; i < 4; ++i) { const float g0 = (float)acc[ai][0][m][0][i] * (sa * sg[0][i]), g1 = (float)acc[ai][0][m][1][i] * (sa * sg[1][i]);
;                     const float u0 = (float)acc[ai][1][m][0][i] * (sa * su[0][i]), u1 = (float)acc[ai][1][m][1][i] * (sa * su[1][i]);
;                     h0[i] = g0 * __builtin_amdgcn_rcpf(1.f + __expf(-g0)) * u0; h1[i] = g1 * __builtin_amdgcn_rcpf(1.f + __expf(-g1)) * u1; }
;                 *(u32x4*)(HID + (size_t)row * DE + 128 * j + 32 * wc + 8 * fq) = pack8(h0, h1);
	v_cvt_f32_i32_e32 v129, v135
	v_cvt_f32_i32_e32 v128, v134
	v_pk_mul_f32 v[134:135], v[38:39], v[144:145] op_sel_hi:[1,0]
	v_pk_mul_f32 v[140:141], v[34:35], v[144:145] op_sel_hi:[1,0]
	v_pk_mul_f32 v[128:129], v[134:135], v[128:129]
	s_nop 0
	v_mul_f32_e32 v134, 0xbfb8aa3b, v128
	v_mul_f32_e32 v135, 0xbfb8aa3b, v129
	v_exp_f32_e32 v134, v134
	v_exp_f32_e32 v135, v135
	v_pk_mul_f32 v[130:131], v[140:141], v[130:131]
	v_add_f32_e32 v134, 1.0, v134
	v_add_f32_e32 v135, 1.0, v135
	v_rcp_f32_e32 v134, v134
	v_rcp_f32_e32 v135, v135
	s_nop 0
	v_pk_mul_f32 v[128:129], v[128:129], v[134:135]
	s_nop 0
	v_pk_mul_f32 v[134:135], v[130:131], v[128:129]
	v_cvt_pk_bf16_f32 v130, v132, v133
	v_mov_b64_e32 v[132:133], s[50:51]
	v_cvt_pk_bf16_f32 v131, v134, v135
	v_mad_i64_i32 v[134:135], s[6:7], v154, s5, v[132:133]
	v_lshl_add_u64 v[134:135], v[134:135], 0, s[62:63]
	v_lshl_add_u64 v[134:135], v[134:135], 0, s[30:31]
	v_cvt_pk_bf16_f32 v128, v136, v137
	v_cvt_pk_bf16_f32 v129, v138, v139
	v_lshl_add_u64 v[134:135], v[134:135], 0, v[152:153]
	global_store_dwordx4 v[134:135], v[128:131], off
	s_nop 1
	v_add_u32_e32 v128, s4, v162
	v_ashrrev_i32_e32 v129, 31, v128
	v_lshl_add_u64 v[130:131], v[128:129], 2, s[52:53]
	v_mov_b32_e32 v130, v179
	v_pk_mul_f32 v[134:135], v[44:45], v[130:131] op_sel_hi:[1,0]
	s_nop 0
	v_pk_mul_f32 v[124:125], v[134:135], v[124:125]
	v_pk_mul_f32 v[136:137], v[40:41], v[130:131] op_sel_hi:[1,0]
	v_mul_f32_e32 v129, 0xbfb8aa3b, v124
	v_exp_f32_e32 v129, v129
	v_pk_mul_f32 v[120:121], v[136:137], v[120:121]
	v_add_f32_e32 v129, 1.0, v129
	v_rcp_f32_e32 v134, v129
	v_mul_f32_e32 v129, 0xbfb8aa3b, v125
	v_exp_f32_e32 v129, v129
	s_nop 0
	v_add_f32_e32 v129, 1.0, v129
	v_rcp_f32_e32 v135, v129
	s_nop 0
	v_pk_mul_f32 v[124:125], v[124:125], v[134:135]
	s_nop 0
	v_pk_mul_f32 v[120:121], v[120:121], v[124:125]
	v_pk_mul_f32 v[124:125], v[36:37], v[130:131] op_sel_hi:[1,0]
	v_pk_mul_f32 v[134:135], v[32:33], v[130:131] op_sel_hi:[1,0]
	v_pk_mul_f32 v[116:117], v[124:125], v[116:117]
	v_pk_mul_f32 v[112:113], v[134:135], v[112:113]
	v_mul_f32_e32 v124, 0xbfb8aa3b, v116
	v_mul_f32_e32 v125, 0xbfb8aa3b, v117
	v_exp_f32_e32 v124, v124
	v_exp_f32_e32 v125, v125
	v_add_f32_e32 v124, 1.0, v124
	v_add_f32_e32 v125, 1.0, v125
	v_rcp_f32_e32 v124, v124
	v_rcp_f32_e32 v125, v125
	s_nop 0
	v_pk_mul_f32 v[116:117], v[116:117], v[124:125]
	s_nop 0
	v_pk_mul_f32 v[116:117], v[112:113], v[116:117]
	v_cvt_f32_i32_e32 v113, v127
	v_cvt_f32_i32_e32 v112, v126
	v_pk_mul_f32 v[124:125], v[46:47], v[130:131] op_sel_hi:[1,0]
	v_pk_mul_f32 v[126:127], v[42:43], v[130:131] op_sel_hi:[1,0]
	v_pk_mul_f32 v[112:113], v[124:125], v[112:113]
	s_nop 0
	v_mul_f32_e32 v124, 0xbfb8aa3b, v112
	v_mul_f32_e32 v125, 0xbfb8aa3b, v113
	v_exp_f32_e32 v124, v124
	v_exp_f32_e32 v125, v125
	v_pk_mul_f32 v[122:123], v[126:127], v[122:123]
	v_add_f32_e32 v124, 1.0, v124
	v_add_f32_e32 v125, 1.0, v125
	v_rcp_f32_e32 v124, v124
	v_rcp_f32_e32 v125, v125
	s_nop 0
	v_pk_mul_f32 v[112:113], v[112:113], v[124:125]
	s_nop 0
	v_pk_mul_f32 v[122:123], v[122:123], v[112:113]
	v_cvt_f32_i32_e32 v113, v119
	v_cvt_f32_i32_e32 v112, v118
	v_pk_mul_f32 v[118:119], v[38:39], v[130:131] op_sel_hi:[1,0]
	v_pk_mul_f32 v[124:125], v[34:35], v[130:131] op_sel_hi:[1,0]
	v_pk_mul_f32 v[112:113], v[118:119], v[112:113]
	s_nop 0
	v_mul_f32_e32 v118, 0xbfb8aa3b, v112
	v_mul_f32_e32 v119, 0xbfb8aa3b, v113
	v_exp_f32_e32 v118, v118
	v_exp_f32_e32 v119, v119
	v_pk_mul_f32 v[114:115], v[124:125], v[114:115]
	v_add_f32_e32 v118, 1.0, v118
	v_add_f32_e32 v119, 1.0, v119
	v_rcp_f32_e32 v118, v118
	v_rcp_f32_e32 v119, v119
	s_nop 0
	v_pk_mul_f32 v[112:113], v[112:113], v[118:119]
	s_nop 0
	v_pk_mul_f32 v[118:119], v[114:115], v[112:113]
	v_cvt_pk_bf16_f32 v114, v116, v117
	v_mad_i64_i32 v[116:117], s[2:3], v128, s5, v[132:133]
	v_lshl_add_u64 v[116:117], v[116:117], 0, s[62:63]
	v_lshl_add_u64 v[116:117], v[116:117], 0, s[30:31]
	v_cvt_pk_bf16_f32 v112, v120, v121
	v_cvt_pk_bf16_f32 v113, v122, v123
	v_cvt_pk_bf16_f32 v115, v118, v119
	v_lshl_add_u64 v[116:117], v[116:117], 0, v[152:153]
	global_store_dwordx4 v[116:117], v[112:115], off
	s_nop 1
	v_add_u32_e32 v112, s4, v163
	v_ashrrev_i32_e32 v113, 31, v112
	v_lshl_add_u64 v[114:115], v[112:113], 2, s[52:53]
	v_mov_b32_e32 v114, v180
	v_pk_mul_f32 v[116:117], v[44:45], v[114:115] op_sel_hi:[1,0]
	s_nop 0
	v_pk_mul_f32 v[108:109], v[116:117], v[108:109]
	v_pk_mul_f32 v[118:119], v[40:41], v[114:115] op_sel_hi:[1,0]
	v_mul_f32_e32 v113, 0xbfb8aa3b, v108
	v_exp_f32_e32 v113, v113
	v_pk_mul_f32 v[104:105], v[118:119], v[104:105]
	v_add_f32_e32 v113, 1.0, v113
	v_rcp_f32_e32 v116, v113
	v_mul_f32_e32 v113, 0xbfb8aa3b, v109
	v_exp_f32_e32 v113, v113
	s_nop 0
	v_add_f32_e32 v113, 1.0, v113
	v_rcp_f32_e32 v117, v113
	s_nop 0
	v_pk_mul_f32 v[108:109], v[108:109], v[116:117]
	s_nop 0
	v_pk_mul_f32 v[104:105], v[104:105], v[108:109]
	v_pk_mul_f32 v[108:109], v[36:37], v[114:115] op_sel_hi:[1,0]
	v_pk_mul_f32 v[116:117], v[32:33], v[114:115] op_sel_hi:[1,0]
	v_pk_mul_f32 v[100:101], v[108:109], v[100:101]
	v_pk_mul_f32 v[96:97], v[116:117], v[96:97]
	v_mul_f32_e32 v108, 0xbfb8aa3b, v100
	v_mul_f32_e32 v109, 0xbfb8aa3b, v101
	v_exp_f32_e32 v108, v108
	v_exp_f32_e32 v109, v109
	v_add_f32_e32 v108, 1.0, v108
	v_add_f32_e32 v109, 1.0, v109
	v_rcp_f32_e32 v108, v108
	v_rcp_f32_e32 v109, v109
	s_nop 0
	v_pk_mul_f32 v[100:101], v[100:101], v[108:109]
	s_nop 0
	v_pk_mul_f32 v[100:101], v[96:97], v[100:101]
	v_cvt_f32_i32_e32 v97, v111
	v_cvt_f32_i32_e32 v96, v110
	v_pk_mul_f32 v[108:109], v[46:47], v[114:115] op_sel_hi:[1,0]
	v_pk_mul_f32 v[110:111], v[42:43], v[114:115] op_sel_hi:[1,0]
; __device__ __forceinline__ u32x4 pack8(f32x4 a, f32x4 b) { u32x4 w; w.x = pk2(a[0], a[1]); w.y = pk2(a[2], a[3]); w.z = pk2(b[0], b[1]); w.w = pk2(b[2], b[3]); return w; }
;     __device__ __forceinline__ void operator()(const pg8::i32x4 (&acc)[2][2][4][2], const Unit& u, int wr, int wc, int fr, int fq) const {
;     ...
;         for (int ai = 0; ai < 2; ++ai)
; #pragma unroll
;             for (int m = 0; m < 4; ++m) {
;                 const int row = u.pm * 256 + ai * 128 + wr * 64 + m * 16 + fr; const float sa = say[row];
;                 f32x4 h0, h1;
; #pragma unroll
;                 for (int i = 0; i < 4; ++i) { const float g0 = (float)acc[ai][0][m][0][i] * (sa * sg[0][i]), g1 = (float)acc[ai][0][m][1][i] * (sa * sg[1][i]);
;                     const float u0 = (float)acc[ai][1][m][0][i] * (sa * su[0][i]), u1 = (float)acc[ai][1][m][1][i] * (sa * su[1][i]);
;                     h0[i] = g0 * __builtin_amdgcn_rcpf(1.f + __expf(-g0)) * u0; h1[i] = g1 * __builtin_amdgcn_rcpf(1.f + __expf(-g1)) * u1; }
;                 *(u32x4*)(HID + (size_t)row * DE + 128 * j + 32 * wc + 8 * fq) = pack8(h0, h1);
	v_pk_mul_f32 v[96:97], v[108:109], v[96:97]
	s_nop 0
	v_mul_f32_e32 v108, 0xbfb8aa3b, v96
	v_mul_f32_e32 v109, 0xbfb8aa3b, v97
	v_exp_f32_e32 v108, v108
	v_exp_f32_e32 v109, v109
	v_pk_mul_f32 v[106:107], v[110:111], v[106:107]
	v_add_f32_e32 v108, 1.0, v108
	v_add_f32_e32 v109, 1.0, v109
	v_rcp_f32_e32 v108, v108
	v_rcp_f32_e32 v109, v109
	s_nop 0
	v_pk_mul_f32 v[96:97], v[96:97], v[108:109]
	s_nop 0
	v_pk_mul_f32 v[106:107], v[106:107], v[96:97]
	v_cvt_f32_i32_e32 v97, v103
	v_cvt_f32_i32_e32 v96, v102
	v_pk_mul_f32 v[102:103], v[38:39], v[114:115] op_sel_hi:[1,0]
	v_pk_mul_f32 v[108:109], v[34:35], v[114:115] op_sel_hi:[1,0]
	v_pk_mul_f32 v[96:97], v[102:103], v[96:97]
	s_nop 0
	v_mul_f32_e32 v102, 0xbfb8aa3b, v96
	v_mul_f32_e32 v103, 0xbfb8aa3b, v97
	v_exp_f32_e32 v102, v102
	v_exp_f32_e32 v103, v103
	v_pk_mul_f32 v[98:99], v[108:109], v[98:99]
	v_add_f32_e32 v102, 1.0, v102
	v_add_f32_e32 v103, 1.0, v103
	v_rcp_f32_e32 v102, v102
	v_rcp_f32_e32 v103, v103
	s_nop 0
	v_pk_mul_f32 v[96:97], v[96:97], v[102:103]
	s_nop 0
	v_pk_mul_f32 v[102:103], v[98:99], v[96:97]
	v_cvt_pk_bf16_f32 v98, v100, v101
	v_mad_i64_i32 v[100:101], s[2:3], v112, s5, v[132:133]
	v_lshl_add_u64 v[100:101], v[100:101], 0, s[62:63]
	v_lshl_add_u64 v[100:101], v[100:101], 0, s[30:31]
	v_cvt_pk_bf16_f32 v96, v104, v105
	v_cvt_pk_bf16_f32 v97, v106, v107
	v_cvt_pk_bf16_f32 v99, v102, v103
	v_lshl_add_u64 v[100:101], v[100:101], 0, v[152:153]
	global_store_dwordx4 v[100:101], v[96:99], off
	s_nop 1
	v_add_u32_e32 v96, s4, v164
	v_ashrrev_i32_e32 v97, 31, v96
	v_lshl_add_u64 v[98:99], v[96:97], 2, s[52:53]
	v_mov_b32_e32 v98, v181
	v_pk_mul_f32 v[100:101], v[44:45], v[98:99] op_sel_hi:[1,0]
	s_nop 0
	v_pk_mul_f32 v[92:93], v[100:101], v[92:93]
	v_pk_mul_f32 v[102:103], v[40:41], v[98:99] op_sel_hi:[1,0]
	v_mul_f32_e32 v97, 0xbfb8aa3b, v92
	v_exp_f32_e32 v97, v97
	v_pk_mul_f32 v[88:89], v[102:103], v[88:89]
	v_add_f32_e32 v97, 1.0, v97
	v_rcp_f32_e32 v100, v97
	v_mul_f32_e32 v97, 0xbfb8aa3b, v93
	v_exp_f32_e32 v97, v97
	s_nop 0
	v_add_f32_e32 v97, 1.0, v97
	v_rcp_f32_e32 v101, v97
	s_nop 0
	v_pk_mul_f32 v[92:93], v[92:93], v[100:101]
	s_nop 0
	v_pk_mul_f32 v[88:89], v[88:89], v[92:93]
	v_pk_mul_f32 v[92:93], v[36:37], v[98:99] op_sel_hi:[1,0]
	v_pk_mul_f32 v[100:101], v[32:33], v[98:99] op_sel_hi:[1,0]
	v_pk_mul_f32 v[84:85], v[92:93], v[84:85]
	v_pk_mul_f32 v[80:81], v[100:101], v[80:81]
	v_mul_f32_e32 v92, 0xbfb8aa3b, v84
	v_mul_f32_e32 v93, 0xbfb8aa3b, v85
	v_exp_f32_e32 v92, v92
	v_exp_f32_e32 v93, v93
	v_add_f32_e32 v92, 1.0, v92
	v_add_f32_e32 v93, 1.0, v93
	v_rcp_f32_e32 v92, v92
	v_rcp_f32_e32 v93, v93
	s_nop 0
	v_pk_mul_f32 v[84:85], v[84:85], v[92:93]
	s_nop 0
	v_pk_mul_f32 v[84:85], v[80:81], v[84:85]
	v_cvt_f32_i32_e32 v81, v95
	v_cvt_f32_i32_e32 v80, v94
	v_pk_mul_f32 v[92:93], v[46:47], v[98:99] op_sel_hi:[1,0]
	v_pk_mul_f32 v[94:95], v[42:43], v[98:99] op_sel_hi:[1,0]
	v_pk_mul_f32 v[80:81], v[92:93], v[80:81]
	s_nop 0
	v_mul_f32_e32 v92, 0xbfb8aa3b, v80
	v_mul_f32_e32 v93, 0xbfb8aa3b, v81
	v_exp_f32_e32 v92, v92
	v_exp_f32_e32 v93, v93
	v_pk_mul_f32 v[90:91], v[94:95], v[90:91]
	v_add_f32_e32 v92, 1.0, v92
	v_add_f32_e32 v93, 1.0, v93
	v_rcp_f32_e32 v92, v92
	v_rcp_f32_e32 v93, v93
	s_nop 0
	v_pk_mul_f32 v[80:81], v[80:81], v[92:93]
	s_nop 0
	v_pk_mul_f32 v[90:91], v[90:91], v[80:81]
	v_cvt_f32_i32_e32 v81, v87
	v_cvt_f32_i32_e32 v80, v86
	v_pk_mul_f32 v[86:87], v[38:39], v[98:99] op_sel_hi:[1,0]
	v_pk_mul_f32 v[92:93], v[34:35], v[98:99] op_sel_hi:[1,0]
	v_pk_mul_f32 v[80:81], v[86:87], v[80:81]
	s_nop 0
	v_mul_f32_e32 v86, 0xbfb8aa3b, v80
	v_mul_f32_e32 v87, 0xbfb8aa3b, v81
	v_exp_f32_e32 v86, v86
	v_exp_f32_e32 v87, v87
	v_pk_mul_f32 v[82:83], v[92:93], v[82:83]
	v_add_f32_e32 v86, 1.0, v86
	v_add_f32_e32 v87, 1.0, v87
	v_rcp_f32_e32 v86, v86
	v_rcp_f32_e32 v87, v87
	s_nop 0
	v_pk_mul_f32 v[80:81], v[80:81], v[86:87]
	s_nop 0
	v_pk_mul_f32 v[86:87], v[82:83], v[80:81]
	v_cvt_pk_bf16_f32 v82, v84, v85
	v_mad_i64_i32 v[84:85], s[2:3], v96, s5, v[132:133]
	v_lshl_add_u64 v[84:85], v[84:85], 0, s[62:63]
	v_lshl_add_u64 v[84:85], v[84:85], 0, s[30:31]
	v_cvt_pk_bf16_f32 v80, v88, v89
	v_cvt_pk_bf16_f32 v81, v90, v91
	v_cvt_pk_bf16_f32 v83, v86, v87
	v_lshl_add_u64 v[84:85], v[84:85], 0, v[152:153]
	global_store_dwordx4 v[84:85], v[80:83], off
	s_nop 1
	v_add_u32_e32 v80, 0x80, v154
	v_ashrrev_i32_e32 v81, 31, v80
	v_lshl_add_u64 v[82:83], v[80:81], 2, s[52:53]
	v_mov_b32_e32 v82, v182
	v_pk_mul_f32 v[84:85], v[44:45], v[82:83] op_sel_hi:[1,0]
	s_nop 0
	v_pk_mul_f32 v[76:77], v[84:85], v[76:77]
	v_pk_mul_f32 v[86:87], v[40:41], v[82:83] op_sel_hi:[1,0]
	v_mul_f32_e32 v81, 0xbfb8aa3b, v76
	v_exp_f32_e32 v81, v81
	v_pk_mul_f32 v[72:73], v[86:87], v[72:73]
	v_add_f32_e32 v81, 1.0, v81
	v_rcp_f32_e32 v84, v81
	v_mul_f32_e32 v81, 0xbfb8aa3b, v77
	v_exp_f32_e32 v81, v81
	s_nop 0
	v_add_f32_e32 v81, 1.0, v81
	v_rcp_f32_e32 v85, v81
	s_nop 0
	v_pk_mul_f32 v[76:77], v[76:77], v[84:85]
	s_nop 0
	v_pk_mul_f32 v[72:73], v[72:73], v[76:77]
	v_pk_mul_f32 v[76:77], v[36:37], v[82:83] op_sel_hi:[1,0]
	v_pk_mul_f32 v[84:85], v[32:33], v[82:83] op_sel_hi:[1,0]
	v_pk_mul_f32 v[68:69], v[76:77], v[68:69]
	v_pk_mul_f32 v[64:65], v[84:85], v[64:65]
	v_mul_f32_e32 v76, 0xbfb8aa3b, v68
	v_mul_f32_e32 v77, 0xbfb8aa3b, v69
	v_exp_f32_e32 v76, v76
	v_exp_f32_e32 v77, v77
	v_add_f32_e32 v76, 1.0, v76
	v_add_f32_e32 v77, 1.0, v77
	v_rcp_f32_e32 v76, v76
	v_rcp_f32_e32 v77, v77
	s_nop 0
	v_pk_mul_f32 v[68:69], v[68:69], v[76:77]
	s_nop 0
	v_pk_mul_f32 v[68:69], v[64:65], v[68:69]
	v_cvt_f32_i32_e32 v65, v79
	v_cvt_f32_i32_e32 v64, v78
	v_pk_mul_f32 v[76:77], v[46:47], v[82:83] op_sel_hi:[1,0]
; __device__ __forceinline__ u32x4 pack8(f32x4 a, f32x4 b) { u32x4 w; w.x = pk2(a[0], a[1]); w.y = pk2(a[2], a[3]); w.z = pk2(b[0], b[1]); w.w = pk2(b[2], b[3]); return w; }
;     __device__ __forceinline__ void operator()(const pg8::i32x4 (&acc)[2][2][4][2], const Unit& u, int wr, int wc, int fr, int fq) const {
;     ...
;         for (int ai = 0; ai < 2; ++ai)
; #pragma unroll
;             for (int m = 0; m < 4; ++m) {
;                 const int row = u.pm * 256 + ai * 128 + wr * 64 + m * 16 + fr; const float sa = say[row];
;                 f32x4 h0, h1;
; #pragma unroll
;                 for (int i = 0; i < 4; ++i) { const float g0 = (float)acc[ai][0][m][0][i] * (sa * sg[0][i]), g1 = (float)acc[ai][0][m][1][i] * (sa * sg[1][i]);
;                     const float u0 = (float)acc[ai][1][m][0][i] * (sa * su[0][i]), u1 = (float)acc[ai][1][m][1][i] * (sa * su[1][i]);
;                     h0[i] = g0 * __builtin_amdgcn_rcpf(1.f + __expf(-g0)) * u0; h1[i] = g1 * __builtin_amdgcn_rcpf(1.f + __expf(-g1)) * u1; }
;                 *(u32x4*)(HID + (size_t)row * DE + 128 * j + 32 * wc + 8 * fq) = pack8(h0, h1);
	v_pk_mul_f32 v[78:79], v[42:43], v[82:83] op_sel_hi:[1,0]
	v_pk_mul_f32 v[64:65], v[76:77], v[64:65]
	s_nop 0
	v_mul_f32_e32 v76, 0xbfb8aa3b, v64
	v_mul_f32_e32 v77, 0xbfb8aa3b, v65
	v_exp_f32_e32 v76, v76
	v_exp_f32_e32 v77, v77
	v_pk_mul_f32 v[74:75], v[78:79], v[74:75]
	v_add_f32_e32 v76, 1.0, v76
	v_add_f32_e32 v77, 1.0, v77
	v_rcp_f32_e32 v76, v76
	v_rcp_f32_e32 v77, v77
	s_nop 0
	v_pk_mul_f32 v[64:65], v[64:65], v[76:77]
	s_nop 0
	v_pk_mul_f32 v[74:75], v[74:75], v[64:65]
	v_cvt_f32_i32_e32 v65, v71
	v_cvt_f32_i32_e32 v64, v70
	v_pk_mul_f32 v[70:71], v[38:39], v[82:83] op_sel_hi:[1,0]
	v_pk_mul_f32 v[76:77], v[34:35], v[82:83] op_sel_hi:[1,0]
	v_pk_mul_f32 v[64:65], v[70:71], v[64:65]
	s_nop 0
	v_mul_f32_e32 v70, 0xbfb8aa3b, v64
	v_mul_f32_e32 v71, 0xbfb8aa3b, v65
	v_exp_f32_e32 v70, v70
	v_exp_f32_e32 v71, v71
	v_pk_mul_f32 v[66:67], v[76:77], v[66:67]
	v_add_f32_e32 v70, 1.0, v70
	v_add_f32_e32 v71, 1.0, v71
	v_rcp_f32_e32 v70, v70
	v_rcp_f32_e32 v71, v71
	s_nop 0
	v_pk_mul_f32 v[64:65], v[64:65], v[70:71]
	s_nop 0
	v_pk_mul_f32 v[70:71], v[66:67], v[64:65]
	v_cvt_pk_bf16_f32 v66, v68, v69
	v_mad_i64_i32 v[68:69], s[2:3], v80, s5, v[132:133]
	v_lshl_add_u64 v[68:69], v[68:69], 0, s[62:63]
	v_lshl_add_u64 v[68:69], v[68:69], 0, s[30:31]
	v_cvt_pk_bf16_f32 v64, v72, v73
	v_cvt_pk_bf16_f32 v65, v74, v75
	v_cvt_pk_bf16_f32 v67, v70, v71
	v_lshl_add_u64 v[68:69], v[68:69], 0, v[152:153]
	global_store_dwordx4 v[68:69], v[64:67], off
	s_nop 1
	v_add_u32_e32 v64, 0x90, v154
	v_ashrrev_i32_e32 v65, 31, v64
	v_lshl_add_u64 v[66:67], v[64:65], 2, s[52:53]
	v_mov_b32_e32 v66, v183
	v_pk_mul_f32 v[68:69], v[44:45], v[66:67] op_sel_hi:[1,0]
	s_nop 0
	v_pk_mul_f32 v[60:61], v[68:69], v[60:61]
	v_pk_mul_f32 v[70:71], v[40:41], v[66:67] op_sel_hi:[1,0]
	v_mul_f32_e32 v65, 0xbfb8aa3b, v60
	v_exp_f32_e32 v65, v65
	v_pk_mul_f32 v[56:57], v[70:71], v[56:57]
	v_add_f32_e32 v65, 1.0, v65
	v_rcp_f32_e32 v68, v65
	v_mul_f32_e32 v65, 0xbfb8aa3b, v61
	v_exp_f32_e32 v65, v65
	s_nop 0
	v_add_f32_e32 v65, 1.0, v65
	v_rcp_f32_e32 v69, v65
	s_nop 0
	v_pk_mul_f32 v[60:61], v[60:61], v[68:69]
	s_nop 0
	v_pk_mul_f32 v[56:57], v[56:57], v[60:61]
	v_pk_mul_f32 v[60:61], v[36:37], v[66:67] op_sel_hi:[1,0]
	v_pk_mul_f32 v[68:69], v[32:33], v[66:67] op_sel_hi:[1,0]
	v_pk_mul_f32 v[52:53], v[60:61], v[52:53]
	v_pk_mul_f32 v[48:49], v[68:69], v[48:49]
	v_mul_f32_e32 v60, 0xbfb8aa3b, v52
	v_mul_f32_e32 v61, 0xbfb8aa3b, v53
	v_exp_f32_e32 v60, v60
	v_exp_f32_e32 v61, v61
	v_add_f32_e32 v60, 1.0, v60
	v_add_f32_e32 v61, 1.0, v61
	v_rcp_f32_e32 v60, v60
	v_rcp_f32_e32 v61, v61
	s_nop 0
	v_pk_mul_f32 v[52:53], v[52:53], v[60:61]
	s_nop 0
	v_pk_mul_f32 v[52:53], v[48:49], v[52:53]
	v_cvt_f32_i32_e32 v49, v63
	v_cvt_f32_i32_e32 v48, v62
	v_pk_mul_f32 v[60:61], v[46:47], v[66:67] op_sel_hi:[1,0]
	v_pk_mul_f32 v[62:63], v[42:43], v[66:67] op_sel_hi:[1,0]
	v_pk_mul_f32 v[48:49], v[60:61], v[48:49]
	s_nop 0
	v_mul_f32_e32 v60, 0xbfb8aa3b, v48
	v_mul_f32_e32 v61, 0xbfb8aa3b, v49
	v_exp_f32_e32 v60, v60
	v_exp_f32_e32 v61, v61
	v_pk_mul_f32 v[58:59], v[62:63], v[58:59]
	v_add_f32_e32 v60, 1.0, v60
	v_add_f32_e32 v61, 1.0, v61
	v_rcp_f32_e32 v60, v60
	v_rcp_f32_e32 v61, v61
	s_nop 0
	v_pk_mul_f32 v[48:49], v[48:49], v[60:61]
	s_nop 0
	v_pk_mul_f32 v[58:59], v[58:59], v[48:49]
	v_cvt_f32_i32_e32 v49, v55
	v_cvt_f32_i32_e32 v48, v54
	v_pk_mul_f32 v[54:55], v[38:39], v[66:67] op_sel_hi:[1,0]
	v_pk_mul_f32 v[60:61], v[34:35], v[66:67] op_sel_hi:[1,0]
	v_pk_mul_f32 v[48:49], v[54:55], v[48:49]
	s_nop 0
	v_mul_f32_e32 v54, 0xbfb8aa3b, v48
	v_mul_f32_e32 v55, 0xbfb8aa3b, v49
	v_exp_f32_e32 v54, v54
	v_exp_f32_e32 v55, v55
	v_pk_mul_f32 v[50:51], v[60:61], v[50:51]
	v_add_f32_e32 v54, 1.0, v54
	v_add_f32_e32 v55, 1.0, v55
	v_rcp_f32_e32 v54, v54
	v_rcp_f32_e32 v55, v55
	s_nop 0
	v_pk_mul_f32 v[48:49], v[48:49], v[54:55]
	s_nop 0
	v_pk_mul_f32 v[54:55], v[50:51], v[48:49]
	v_cvt_pk_bf16_f32 v50, v52, v53
	v_mad_i64_i32 v[52:53], s[2:3], v64, s5, v[132:133]
	v_lshl_add_u64 v[52:53], v[52:53], 0, s[62:63]
	v_lshl_add_u64 v[52:53], v[52:53], 0, s[30:31]
	v_cvt_pk_bf16_f32 v48, v56, v57
	v_cvt_pk_bf16_f32 v49, v58, v59
	v_cvt_pk_bf16_f32 v51, v54, v55
	v_lshl_add_u64 v[52:53], v[52:53], 0, v[152:153]
	global_store_dwordx4 v[52:53], v[48:51], off
	s_nop 1
	v_add_u32_e32 v48, 0xa0, v154
	v_ashrrev_i32_e32 v49, 31, v48
	v_lshl_add_u64 v[50:51], v[48:49], 2, s[52:53]
	v_mov_b32_e32 v50, v184
	v_pk_mul_f32 v[52:53], v[44:45], v[50:51] op_sel_hi:[1,0]
	s_nop 0
	v_pk_mul_f32 v[24:25], v[52:53], v[24:25]
	v_pk_mul_f32 v[54:55], v[40:41], v[50:51] op_sel_hi:[1,0]
	v_mul_f32_e32 v49, 0xbfb8aa3b, v24
	v_exp_f32_e32 v49, v49
	v_pk_mul_f32 v[28:29], v[54:55], v[28:29]
	v_add_f32_e32 v49, 1.0, v49
	v_rcp_f32_e32 v52, v49
	v_mul_f32_e32 v49, 0xbfb8aa3b, v25
	v_exp_f32_e32 v49, v49
	s_nop 0
	v_add_f32_e32 v49, 1.0, v49
	v_rcp_f32_e32 v53, v49
	s_nop 0
	v_pk_mul_f32 v[24:25], v[24:25], v[52:53]
	s_nop 0
	v_pk_mul_f32 v[24:25], v[28:29], v[24:25]
; __device__ __forceinline__ u32x4 pack8(f32x4 a, f32x4 b) { u32x4 w; w.x = pk2(a[0], a[1]); w.y = pk2(a[2], a[3]); w.z = pk2(b[0], b[1]); w.w = pk2(b[2], b[3]); return w; }
;     __device__ __forceinline__ void operator()(const pg8::i32x4 (&acc)[2][2][4][2], const Unit& u, int wr, int wc, int fr, int fq) const {
;     ...
;         for (int ai = 0; ai < 2; ++ai)
; #pragma unroll
;             for (int m = 0; m < 4; ++m) {
;                 const int row = u.pm * 256 + ai * 128 + wr * 64 + m * 16 + fr; const float sa = say[row];
;                 f32x4 h0, h1;
; #pragma unroll
;                 for (int i = 0; i < 4; ++i) { const float g0 = (float)acc[ai][0][m][0][i] * (sa * sg[0][i]), g1 = (float)acc[ai][0][m][1][i] * (sa * sg[1][i]);
;                     const float u0 = (float)acc[ai][1][m][0][i] * (sa * su[0][i]), u1 = (float)acc[ai][1][m][1][i] * (sa * su[1][i]);
;                     h0[i] = g0 * __builtin_amdgcn_rcpf(1.f + __expf(-g0)) * u0; h1[i] = g1 * __builtin_amdgcn_rcpf(1.f + __expf(-g1)) * u1; }
;                 *(u32x4*)(HID + (size_t)row * DE + 128 * j + 32 * wc + 8 * fq) = pack8(h0, h1);
;             }
;     }
	v_pk_mul_f32 v[28:29], v[36:37], v[50:51] op_sel_hi:[1,0]
	v_pk_mul_f32 v[52:53], v[32:33], v[50:51] op_sel_hi:[1,0]
	v_pk_mul_f32 v[16:17], v[28:29], v[16:17]
	v_pk_mul_f32 v[20:21], v[52:53], v[20:21]
	v_mul_f32_e32 v28, 0xbfb8aa3b, v16
	v_mul_f32_e32 v29, 0xbfb8aa3b, v17
	v_exp_f32_e32 v28, v28
	v_exp_f32_e32 v29, v29
	v_add_f32_e32 v28, 1.0, v28
	v_add_f32_e32 v29, 1.0, v29
	v_rcp_f32_e32 v28, v28
	v_rcp_f32_e32 v29, v29
	s_nop 0
	v_pk_mul_f32 v[16:17], v[16:17], v[28:29]
	s_nop 0
	v_pk_mul_f32 v[20:21], v[20:21], v[16:17]
	v_cvt_f32_i32_e32 v17, v27
	v_cvt_f32_i32_e32 v16, v26
	v_pk_mul_f32 v[26:27], v[46:47], v[50:51] op_sel_hi:[1,0]
	v_cvt_f32_i32_e32 v29, v31
	v_cvt_f32_i32_e32 v28, v30
	v_pk_mul_f32 v[16:17], v[26:27], v[16:17]
	v_pk_mul_f32 v[30:31], v[42:43], v[50:51] op_sel_hi:[1,0]
	v_mul_f32_e32 v26, 0xbfb8aa3b, v16
	v_mul_f32_e32 v27, 0xbfb8aa3b, v17
	v_exp_f32_e32 v26, v26
	v_exp_f32_e32 v27, v27
	v_pk_mul_f32 v[28:29], v[30:31], v[28:29]
	v_add_f32_e32 v26, 1.0, v26
	v_add_f32_e32 v27, 1.0, v27
	v_rcp_f32_e32 v26, v26
	v_rcp_f32_e32 v27, v27
	s_nop 0
	v_pk_mul_f32 v[16:17], v[16:17], v[26:27]
	s_nop 0
	v_pk_mul_f32 v[26:27], v[28:29], v[16:17]
	v_cvt_f32_i32_e32 v17, v19
	v_cvt_f32_i32_e32 v16, v18
	v_pk_mul_f32 v[18:19], v[38:39], v[50:51] op_sel_hi:[1,0]
	v_pk_mul_f32 v[28:29], v[34:35], v[50:51] op_sel_hi:[1,0]
	v_pk_mul_f32 v[16:17], v[18:19], v[16:17]
	s_nop 0
	v_mul_f32_e32 v18, 0xbfb8aa3b, v16
	v_mul_f32_e32 v19, 0xbfb8aa3b, v17
	v_exp_f32_e32 v18, v18
	v_exp_f32_e32 v19, v19
	v_pk_mul_f32 v[22:23], v[28:29], v[22:23]
	v_add_f32_e32 v18, 1.0, v18
	v_add_f32_e32 v19, 1.0, v19
	v_rcp_f32_e32 v18, v18
	v_rcp_f32_e32 v19, v19
	s_nop 0
	v_pk_mul_f32 v[16:17], v[16:17], v[18:19]
	v_cvt_pk_bf16_f32 v18, v20, v21
	v_mad_i64_i32 v[20:21], s[2:3], v48, s5, v[132:133]
	v_lshl_add_u64 v[20:21], v[20:21], 0, s[62:63]
	v_pk_mul_f32 v[22:23], v[22:23], v[16:17]
	v_lshl_add_u64 v[20:21], v[20:21], 0, s[30:31]
	v_cvt_pk_bf16_f32 v16, v24, v25
	v_cvt_pk_bf16_f32 v17, v26, v27
	v_cvt_pk_bf16_f32 v19, v22, v23
	v_lshl_add_u64 v[20:21], v[20:21], 0, v[152:153]
	global_store_dwordx4 v[20:21], v[16:19], off
	s_nop 1
	v_add_u32_e32 v16, 0xb0, v154
	v_ashrrev_i32_e32 v17, 31, v16
	v_lshl_add_u64 v[18:19], v[16:17], 2, s[52:53]
	v_mov_b32_e32 v18, v185
	v_pk_mul_f32 v[20:21], v[44:45], v[18:19] op_sel_hi:[1,0]
	s_nop 0
	v_pk_mul_f32 v[8:9], v[20:21], v[8:9]
	v_pk_mul_f32 v[22:23], v[40:41], v[18:19] op_sel_hi:[1,0]
	v_mul_f32_e32 v17, 0xbfb8aa3b, v8
	v_exp_f32_e32 v17, v17
	v_pk_mul_f32 v[12:13], v[22:23], v[12:13]
	v_add_f32_e32 v17, 1.0, v17
	v_rcp_f32_e32 v20, v17
	v_mul_f32_e32 v17, 0xbfb8aa3b, v9
	v_exp_f32_e32 v17, v17
	s_nop 0
	v_add_f32_e32 v17, 1.0, v17
	v_rcp_f32_e32 v21, v17
	s_nop 0
	v_pk_mul_f32 v[8:9], v[8:9], v[20:21]
	s_nop 0
	v_pk_mul_f32 v[8:9], v[12:13], v[8:9]
	v_pk_mul_f32 v[12:13], v[36:37], v[18:19] op_sel_hi:[1,0]
	v_pk_mul_f32 v[20:21], v[32:33], v[18:19] op_sel_hi:[1,0]
	v_pk_mul_f32 v[0:1], v[12:13], v[0:1]
	v_pk_mul_f32 v[4:5], v[20:21], v[4:5]
	v_mul_f32_e32 v12, 0xbfb8aa3b, v0
	v_mul_f32_e32 v13, 0xbfb8aa3b, v1
	v_exp_f32_e32 v12, v12
	v_exp_f32_e32 v13, v13
	v_add_f32_e32 v12, 1.0, v12
	v_add_f32_e32 v13, 1.0, v13
	v_rcp_f32_e32 v12, v12
	v_rcp_f32_e32 v13, v13
	s_nop 0
	v_pk_mul_f32 v[0:1], v[0:1], v[12:13]
	s_nop 0
	v_pk_mul_f32 v[4:5], v[4:5], v[0:1]
	v_cvt_f32_i32_e32 v1, v11
	v_cvt_f32_i32_e32 v0, v10
	v_pk_mul_f32 v[10:11], v[46:47], v[18:19] op_sel_hi:[1,0]
	v_cvt_f32_i32_e32 v13, v15
	v_cvt_f32_i32_e32 v12, v14
	v_pk_mul_f32 v[0:1], v[10:11], v[0:1]
	v_pk_mul_f32 v[14:15], v[42:43], v[18:19] op_sel_hi:[1,0]
	v_mul_f32_e32 v10, 0xbfb8aa3b, v0
	v_mul_f32_e32 v11, 0xbfb8aa3b, v1
	v_exp_f32_e32 v10, v10
	v_exp_f32_e32 v11, v11
	v_pk_mul_f32 v[12:13], v[14:15], v[12:13]
	v_add_f32_e32 v10, 1.0, v10
	v_add_f32_e32 v11, 1.0, v11
	v_rcp_f32_e32 v10, v10
	v_rcp_f32_e32 v11, v11
	s_nop 0
	v_pk_mul_f32 v[0:1], v[0:1], v[10:11]
	s_nop 0
	v_pk_mul_f32 v[10:11], v[12:13], v[0:1]
	v_cvt_f32_i32_e32 v1, v3
	v_cvt_f32_i32_e32 v0, v2
	v_pk_mul_f32 v[2:3], v[38:39], v[18:19] op_sel_hi:[1,0]
	v_pk_mul_f32 v[12:13], v[34:35], v[18:19] op_sel_hi:[1,0]
	v_pk_mul_f32 v[0:1], v[2:3], v[0:1]
	s_nop 0
	v_mul_f32_e32 v2, 0xbfb8aa3b, v0
	v_mul_f32_e32 v3, 0xbfb8aa3b, v1
	v_exp_f32_e32 v2, v2
	v_exp_f32_e32 v3, v3
	v_pk_mul_f32 v[6:7], v[12:13], v[6:7]
	v_add_f32_e32 v2, 1.0, v2
	v_add_f32_e32 v3, 1.0, v3
	v_rcp_f32_e32 v2, v2
	v_rcp_f32_e32 v3, v3
	s_nop 0
	v_pk_mul_f32 v[0:1], v[0:1], v[2:3]
	v_cvt_pk_bf16_f32 v2, v4, v5
	v_mad_i64_i32 v[4:5], s[2:3], v16, s5, v[132:133]
	v_lshl_add_u64 v[4:5], v[4:5], 0, s[62:63]
	v_pk_mul_f32 v[6:7], v[6:7], v[0:1]
	v_lshl_add_u64 v[4:5], v[4:5], 0, s[30:31]
	v_cvt_pk_bf16_f32 v0, v8, v9
	v_cvt_pk_bf16_f32 v1, v10, v11
	v_cvt_pk_bf16_f32 v3, v6, v7
	v_lshl_add_u64 v[4:5], v[4:5], 0, v[152:153]
	s_mov_b64 s[2:3], -1
	global_store_dwordx4 v[4:5], v[0:3], off
	s_cbranch_vccnz .LBB0_1168
	s_andn2_b64 vcc, exec, s[48:49]
	s_cbranch_vccnz .LBB0_1167
	s_barrier
	s_branch .LBB0_1167

; __device__ __forceinline__ u32x4 pack8(f32x4 a, f32x4 b) { u32x4 w; w.x = pk2(a[0], a[1]); w.y = pk2(a[2], a[3]); w.z = pk2(b[0], b[1]); w.w = pk2(b[2], b[3]); return w; }
;     __device__ __forceinline__ void operator()(const f32x4 (&acc)[2][2][4][2], const Unit& u, int wr, int wc, int fr, int fq) const {
;     ...
;         for (int ai = 0; ai < 2; ++ai)
; #pragma unroll
;             for (int m = 0; m < 4; ++m) {
;                 const int row = u.pm * 256 + ai * 128 + wr * 64 + m * 16 + fr; const float gt = gate[row];
; #pragma unroll
;                 for (int bj = 0; bj < 2; ++bj) *(u32x4*)(Y + (size_t)row * D + 256 * jn + 128 * bj + 32 * wc + 8 * fq) = pack8(acc[ai][bj][m][0] * gt, acc[ai][bj][m][1] * gt);
.LBB0_1301:
	s_lshl_b32 s2, s30, 8
	v_add_u32_e32 v136, s2, v138
	v_lshlrev_b32_e32 v160, 2, v136
	global_load_dword v152, v160, s[46:47]
	global_load_dword v153, v160, s[46:47] offset:64
	global_load_dword v154, v160, s[46:47] offset:128
	global_load_dword v155, v160, s[46:47] offset:192
	global_load_dword v156, v160, s[46:47] offset:512
	global_load_dword v157, v160, s[46:47] offset:576
	global_load_dword v158, v160, s[46:47] offset:640
	global_load_dword v159, v160, s[46:47] offset:704
	v_ashrrev_i32_e32 v137, 31, v136
	v_lshl_add_u64 v[146:147], v[136:137], 2, s[46:47]
	v_lshlrev_b64 v[148:149], 11, v[136:137]
	s_lshl_b32 s3, s51, 9
	s_and_b32 s30, s3, 0x600
	s_mov_b32 s51, s31
	s_and_b64 vcc, exec, s[38:39]
	s_waitcnt vmcnt(0)
	v_mov_b32_e32 v146, v152
	v_pk_mul_f32 v[124:125], v[124:125], v[146:147] op_sel_hi:[1,0]
	v_pk_mul_f32 v[150:151], v[122:123], v[146:147] op_sel_hi:[1,0]
	v_pk_mul_f32 v[122:123], v[120:121], v[146:147] op_sel_hi:[1,0]
	v_cvt_pk_bf16_f32 v120, v124, v125
	v_lshl_add_u64 v[124:125], s[44:45], 0, v[148:149]
	v_lshl_add_u64 v[124:125], v[124:125], 0, s[30:31]
	v_pk_mul_f32 v[126:127], v[126:127], v[146:147] op_sel_hi:[1,0]
	v_lshl_add_u64 v[124:125], v[124:125], 0, s[50:51]
	v_cvt_pk_bf16_f32 v121, v126, v127
	v_cvt_pk_bf16_f32 v122, v122, v123
	v_cvt_pk_bf16_f32 v123, v150, v151
	v_lshl_add_u64 v[124:125], v[124:125], 0, v[144:145]
	global_store_dwordx4 v[124:125], v[120:123], off
	v_pk_mul_f32 v[118:119], v[118:119], v[146:147] op_sel_hi:[1,0]
	v_pk_mul_f32 v[116:117], v[116:117], v[146:147] op_sel_hi:[1,0]
	v_pk_mul_f32 v[120:121], v[114:115], v[146:147] op_sel_hi:[1,0]
	v_pk_mul_f32 v[114:115], v[112:113], v[146:147] op_sel_hi:[1,0]
	v_cvt_pk_bf16_f32 v112, v116, v117
	v_cvt_pk_bf16_f32 v113, v118, v119
	v_cvt_pk_bf16_f32 v114, v114, v115
	v_cvt_pk_bf16_f32 v115, v120, v121
	global_store_dwordx4 v[124:125], v[112:115], off offset:256
	s_nop 1
	v_add_u32_e32 v112, s2, v140
	v_ashrrev_i32_e32 v113, 31, v112
	v_lshl_add_u64 v[114:115], v[112:113], 2, s[46:47]
	v_mov_b32_e32 v114, v153
	v_lshlrev_b64 v[112:113], 11, v[112:113]
	v_pk_mul_f32 v[108:109], v[108:109], v[114:115] op_sel_hi:[1,0]
	v_pk_mul_f32 v[116:117], v[106:107], v[114:115] op_sel_hi:[1,0]
	v_pk_mul_f32 v[106:107], v[104:105], v[114:115] op_sel_hi:[1,0]
	v_cvt_pk_bf16_f32 v104, v108, v109
	v_lshl_add_u64 v[108:109], s[44:45], 0, v[112:113]
	v_lshl_add_u64 v[108:109], v[108:109], 0, s[30:31]
	v_pk_mul_f32 v[110:111], v[110:111], v[114:115] op_sel_hi:[1,0]
	v_lshl_add_u64 v[108:109], v[108:109], 0, s[50:51]
	v_cvt_pk_bf16_f32 v105, v110, v111
	v_cvt_pk_bf16_f32 v106, v106, v107
	v_cvt_pk_bf16_f32 v107, v116, v117
	v_lshl_add_u64 v[108:109], v[108:109], 0, v[144:145]
	global_store_dwordx4 v[108:109], v[104:107], off
	v_pk_mul_f32 v[102:103], v[102:103], v[114:115] op_sel_hi:[1,0]
	v_pk_mul_f32 v[100:101], v[100:101], v[114:115] op_sel_hi:[1,0]
	v_pk_mul_f32 v[104:105], v[98:99], v[114:115] op_sel_hi:[1,0]
	v_pk_mul_f32 v[98:99], v[96:97], v[114:115] op_sel_hi:[1,0]
	v_cvt_pk_bf16_f32 v96, v100, v101
	v_cvt_pk_bf16_f32 v97, v102, v103
	v_cvt_pk_bf16_f32 v98, v98, v99
	v_cvt_pk_bf16_f32 v99, v104, v105
	global_store_dwordx4 v[108:109], v[96:99], off offset:256
	s_nop 1
	v_add_u32_e32 v96, s2, v141
	v_ashrrev_i32_e32 v97, 31, v96
	v_lshl_add_u64 v[98:99], v[96:97], 2, s[46:47]
	v_mov_b32_e32 v98, v154
	v_lshlrev_b64 v[96:97], 11, v[96:97]
	v_pk_mul_f32 v[92:93], v[92:93], v[98:99] op_sel_hi:[1,0]
	v_pk_mul_f32 v[100:101], v[90:91], v[98:99] op_sel_hi:[1,0]
	v_pk_mul_f32 v[90:91], v[88:89], v[98:99] op_sel_hi:[1,0]
	v_cvt_pk_bf16_f32 v88, v92, v93
	v_lshl_add_u64 v[92:93], s[44:45], 0, v[96:97]
	v_lshl_add_u64 v[92:93], v[92:93], 0, s[30:31]
	v_pk_mul_f32 v[94:95], v[94:95], v[98:99] op_sel_hi:[1,0]
	v_lshl_add_u64 v[92:93], v[92:93], 0, s[50:51]
	v_cvt_pk_bf16_f32 v89, v94, v95
	v_cvt_pk_bf16_f32 v90, v90, v91
	v_cvt_pk_bf16_f32 v91, v100, v101
	v_lshl_add_u64 v[92:93], v[92:93], 0, v[144:145]
	global_store_dwordx4 v[92:93], v[88:91], off
	v_pk_mul_f32 v[86:87], v[86:87], v[98:99] op_sel_hi:[1,0]
	v_pk_mul_f32 v[84:85], v[84:85], v[98:99] op_sel_hi:[1,0]
	v_pk_mul_f32 v[88:89], v[82:83], v[98:99] op_sel_hi:[1,0]
	v_pk_mul_f32 v[82:83], v[80:81], v[98:99] op_sel_hi:[1,0]
	v_cvt_pk_bf16_f32 v80, v84, v85
	v_cvt_pk_bf16_f32 v81, v86, v87
	v_cvt_pk_bf16_f32 v82, v82, v83
	v_cvt_pk_bf16_f32 v83, v88, v89
	global_store_dwordx4 v[92:93], v[80:83], off offset:256
	s_nop 1
	v_add_u32_e32 v80, s2, v142
	v_ashrrev_i32_e32 v81, 31, v80
	v_lshl_add_u64 v[82:83], v[80:81], 2, s[46:47]
	v_mov_b32_e32 v82, v155
	v_lshlrev_b64 v[80:81], 11, v[80:81]
	s_mov_b64 s[2:3], -1
	v_pk_mul_f32 v[76:77], v[76:77], v[82:83] op_sel_hi:[1,0]
	v_pk_mul_f32 v[84:85], v[74:75], v[82:83] op_sel_hi:[1,0]
	v_pk_mul_f32 v[74:75], v[72:73], v[82:83] op_sel_hi:[1,0]
	v_cvt_pk_bf16_f32 v72, v76, v77
	v_lshl_add_u64 v[76:77], s[44:45], 0, v[80:81]
	v_lshl_add_u64 v[76:77], v[76:77], 0, s[30:31]
	v_pk_mul_f32 v[78:79], v[78:79], v[82:83] op_sel_hi:[1,0]
	v_lshl_add_u64 v[76:77], v[76:77], 0, s[50:51]
	v_cvt_pk_bf16_f32 v73, v78, v79
	v_cvt_pk_bf16_f32 v74, v74, v75
	v_cvt_pk_bf16_f32 v75, v84, v85
	v_lshl_add_u64 v[76:77], v[76:77], 0, v[144:145]
	global_store_dwordx4 v[76:77], v[72:75], off
	v_pk_mul_f32 v[70:71], v[70:71], v[82:83] op_sel_hi:[1,0]
; __device__ __forceinline__ u32x4 pack8(f32x4 a, f32x4 b) { u32x4 w; w.x = pk2(a[0], a[1]); w.y = pk2(a[2], a[3]); w.z = pk2(b[0], b[1]); w.w = pk2(b[2], b[3]); return w; }
;     __device__ __forceinline__ void operator()(const f32x4 (&acc)[2][2][4][2], const Unit& u, int wr, int wc, int fr, int fq) const {
;     ...
;         for (int ai = 0; ai < 2; ++ai)
; #pragma unroll
;             for (int m = 0; m < 4; ++m) {
;                 const int row = u.pm * 256 + ai * 128 + wr * 64 + m * 16 + fr; const float gt = gate[row];
; #pragma unroll
;                 for (int bj = 0; bj < 2; ++bj) *(u32x4*)(Y + (size_t)row * D + 256 * jn + 128 * bj + 32 * wc + 8 * fq) = pack8(acc[ai][bj][m][0] * gt, acc[ai][bj][m][1] * gt);
	v_pk_mul_f32 v[68:69], v[68:69], v[82:83] op_sel_hi:[1,0]
	v_pk_mul_f32 v[72:73], v[66:67], v[82:83] op_sel_hi:[1,0]
	v_pk_mul_f32 v[66:67], v[64:65], v[82:83] op_sel_hi:[1,0]
	v_cvt_pk_bf16_f32 v64, v68, v69
	v_cvt_pk_bf16_f32 v65, v70, v71
	v_cvt_pk_bf16_f32 v66, v66, v67
	v_cvt_pk_bf16_f32 v67, v72, v73
	global_store_dwordx4 v[76:77], v[64:67], off offset:256
	s_nop 1
	v_add_u32_e32 v64, 0x80, v136
	v_ashrrev_i32_e32 v65, 31, v64
	v_lshl_add_u64 v[66:67], v[64:65], 2, s[46:47]
	v_mov_b32_e32 v66, v156
	v_lshlrev_b64 v[64:65], 11, v[64:65]
	v_pk_mul_f32 v[60:61], v[60:61], v[66:67] op_sel_hi:[1,0]
	v_pk_mul_f32 v[68:69], v[58:59], v[66:67] op_sel_hi:[1,0]
	v_pk_mul_f32 v[58:59], v[56:57], v[66:67] op_sel_hi:[1,0]
	v_cvt_pk_bf16_f32 v56, v60, v61
	v_lshl_add_u64 v[60:61], s[44:45], 0, v[64:65]
	v_lshl_add_u64 v[60:61], v[60:61], 0, s[30:31]
	v_pk_mul_f32 v[62:63], v[62:63], v[66:67] op_sel_hi:[1,0]
	v_lshl_add_u64 v[60:61], v[60:61], 0, s[50:51]
	v_cvt_pk_bf16_f32 v57, v62, v63
	v_cvt_pk_bf16_f32 v58, v58, v59
	v_cvt_pk_bf16_f32 v59, v68, v69
	v_lshl_add_u64 v[60:61], v[60:61], 0, v[144:145]
	global_store_dwordx4 v[60:61], v[56:59], off
	v_pk_mul_f32 v[54:55], v[54:55], v[66:67] op_sel_hi:[1,0]
	v_pk_mul_f32 v[52:53], v[52:53], v[66:67] op_sel_hi:[1,0]
	v_pk_mul_f32 v[56:57], v[50:51], v[66:67] op_sel_hi:[1,0]
	v_pk_mul_f32 v[50:51], v[48:49], v[66:67] op_sel_hi:[1,0]
	v_cvt_pk_bf16_f32 v48, v52, v53
	v_cvt_pk_bf16_f32 v49, v54, v55
	v_cvt_pk_bf16_f32 v50, v50, v51
	v_cvt_pk_bf16_f32 v51, v56, v57
	global_store_dwordx4 v[60:61], v[48:51], off offset:256
	s_nop 1
	v_add_u32_e32 v48, 0x90, v136
	v_ashrrev_i32_e32 v49, 31, v48
	v_lshl_add_u64 v[50:51], v[48:49], 2, s[46:47]
	v_mov_b32_e32 v50, v157
	v_lshlrev_b64 v[48:49], 11, v[48:49]
	v_pk_mul_f32 v[44:45], v[44:45], v[50:51] op_sel_hi:[1,0]
	v_pk_mul_f32 v[52:53], v[42:43], v[50:51] op_sel_hi:[1,0]
	v_pk_mul_f32 v[42:43], v[40:41], v[50:51] op_sel_hi:[1,0]
	v_cvt_pk_bf16_f32 v40, v44, v45
	v_lshl_add_u64 v[44:45], s[44:45], 0, v[48:49]
	v_lshl_add_u64 v[44:45], v[44:45], 0, s[30:31]
	v_pk_mul_f32 v[46:47], v[46:47], v[50:51] op_sel_hi:[1,0]
	v_lshl_add_u64 v[44:45], v[44:45], 0, s[50:51]
	v_cvt_pk_bf16_f32 v41, v46, v47
	v_cvt_pk_bf16_f32 v42, v42, v43
	v_cvt_pk_bf16_f32 v43, v52, v53
	v_lshl_add_u64 v[44:45], v[44:45], 0, v[144:145]
	global_store_dwordx4 v[44:45], v[40:43], off
	v_pk_mul_f32 v[38:39], v[38:39], v[50:51] op_sel_hi:[1,0]
	v_pk_mul_f32 v[36:37], v[36:37], v[50:51] op_sel_hi:[1,0]
	v_pk_mul_f32 v[40:41], v[34:35], v[50:51] op_sel_hi:[1,0]
	v_pk_mul_f32 v[34:35], v[32:33], v[50:51] op_sel_hi:[1,0]
	v_cvt_pk_bf16_f32 v32, v36, v37
	v_cvt_pk_bf16_f32 v33, v38, v39
	v_cvt_pk_bf16_f32 v34, v34, v35
	v_cvt_pk_bf16_f32 v35, v40, v41
	global_store_dwordx4 v[44:45], v[32:35], off offset:256
	s_nop 1
	v_add_u32_e32 v32, 0xa0, v136
	v_ashrrev_i32_e32 v33, 31, v32
	v_lshl_add_u64 v[34:35], v[32:33], 2, s[46:47]
	v_mov_b32_e32 v34, v158
	v_lshlrev_b64 v[32:33], 11, v[32:33]
	v_pk_mul_f32 v[28:29], v[28:29], v[34:35] op_sel_hi:[1,0]
	v_pk_mul_f32 v[36:37], v[26:27], v[34:35] op_sel_hi:[1,0]
	v_pk_mul_f32 v[26:27], v[24:25], v[34:35] op_sel_hi:[1,0]
	v_cvt_pk_bf16_f32 v24, v28, v29
	v_lshl_add_u64 v[28:29], s[44:45], 0, v[32:33]
	v_lshl_add_u64 v[28:29], v[28:29], 0, s[30:31]
	v_pk_mul_f32 v[30:31], v[30:31], v[34:35] op_sel_hi:[1,0]
	v_lshl_add_u64 v[28:29], v[28:29], 0, s[50:51]
	v_cvt_pk_bf16_f32 v25, v30, v31
	v_cvt_pk_bf16_f32 v26, v26, v27
	v_cvt_pk_bf16_f32 v27, v36, v37
	v_lshl_add_u64 v[28:29], v[28:29], 0, v[144:145]
	global_store_dwordx4 v[28:29], v[24:27], off
	v_pk_mul_f32 v[22:23], v[22:23], v[34:35] op_sel_hi:[1,0]
	v_pk_mul_f32 v[20:21], v[20:21], v[34:35] op_sel_hi:[1,0]
	v_pk_mul_f32 v[24:25], v[18:19], v[34:35] op_sel_hi:[1,0]
	v_pk_mul_f32 v[18:19], v[16:17], v[34:35] op_sel_hi:[1,0]
	v_cvt_pk_bf16_f32 v16, v20, v21
	v_cvt_pk_bf16_f32 v17, v22, v23
	v_cvt_pk_bf16_f32 v18, v18, v19
	v_cvt_pk_bf16_f32 v19, v24, v25
	global_store_dwordx4 v[28:29], v[16:19], off offset:256
	s_nop 1
	v_add_u32_e32 v16, 0xb0, v136
	v_ashrrev_i32_e32 v17, 31, v16
	v_lshl_add_u64 v[18:19], v[16:17], 2, s[46:47]
	v_mov_b32_e32 v18, v159
	v_lshlrev_b64 v[16:17], 11, v[16:17]
	v_pk_mul_f32 v[12:13], v[12:13], v[18:19] op_sel_hi:[1,0]
	v_pk_mul_f32 v[20:21], v[10:11], v[18:19] op_sel_hi:[1,0]
	v_pk_mul_f32 v[10:11], v[8:9], v[18:19] op_sel_hi:[1,0]
	v_cvt_pk_bf16_f32 v8, v12, v13
	v_lshl_add_u64 v[12:13], s[44:45], 0, v[16:17]
	v_lshl_add_u64 v[12:13], v[12:13], 0, s[30:31]
	v_pk_mul_f32 v[14:15], v[14:15], v[18:19] op_sel_hi:[1,0]
	v_lshl_add_u64 v[12:13], v[12:13], 0, s[50:51]
	v_cvt_pk_bf16_f32 v9, v14, v15
	v_cvt_pk_bf16_f32 v10, v10, v11
	v_cvt_pk_bf16_f32 v11, v20, v21
	v_lshl_add_u64 v[12:13], v[12:13], 0, v[144:145]
	global_store_dwordx4 v[12:13], v[8:11], off
	v_pk_mul_f32 v[6:7], v[6:7], v[18:19] op_sel_hi:[1,0]
	v_pk_mul_f32 v[4:5], v[4:5], v[18:19] op_sel_hi:[1,0]
	v_pk_mul_f32 v[8:9], v[2:3], v[18:19] op_sel_hi:[1,0]
	v_pk_mul_f32 v[2:3], v[0:1], v[18:19] op_sel_hi:[1,0]
	v_cvt_pk_bf16_f32 v0, v4, v5
	v_cvt_pk_bf16_f32 v1, v6, v7
	v_cvt_pk_bf16_f32 v2, v2, v3
	v_cvt_pk_bf16_f32 v3, v8, v9
	global_store_dwordx4 v[12:13], v[0:3], off offset:256
	s_cbranch_vccnz .LBB0_1274
	s_andn2_b64 vcc, exec, s[42:43]
	s_cbranch_vccnz .LBB0_1273
	s_barrier
	s_branch .LBB0_1273
